# GEMM K-loops: back-edge rotation (trip counter, pointer bumps and exit test moved in front of the trip's closing barrier; in-proj loops take the barrier at the loop head)
# speedup vs baseline: 1.0036x; 1.0036x over previous
; #define PG8_STAGE(bufoff, gbase, voff) do { _Pragma("unroll") for (int _i = 0; _i < 2; ++_i) \
;         __builtin_amdgcn_global_load_lds((const unsigned*)((const char*)(gbase) + (voff)[_i]), (PG8_LAS unsigned*)(lds + (bufoff) + ldsw + _i * 8192), 16, 0, 0); } while (0)
; #define PG8_STAGE_A(bufoff, kbase, h, gv) do { if constexpr (GATHER) { PG8_STAGE(bufoff, kbase, (gv)[h]); } else { PG8_STAGE(bufoff, (kbase) + (h) * hstep, voffA); } } while (0)
; #define PG8_WAIT_V(n) asm volatile("s_waitcnt vmcnt(" #n ")" ::: "memory")
; #define PG8_WAIT_L(n) asm volatile("s_waitcnt lgkmcnt(" #n ")" ::: "memory")
; #define PG8_BAR __builtin_amdgcn_s_barrier()
; #define PG8_SCHED __builtin_amdgcn_sched_barrier(0)
;     __device__ __forceinline__ int brow(const pg8::Unit& u) const { return (u.pn >> 8) * Nper + (u.pn & 255) * 256; }
; template <class Epi, class Sched, bool ALIGN_EPI = false, bool SP2 = false, bool FP8 = false, bool GATHER = false>
; __device__ __forceinline__ void gemm_phase(PG8_LAS unsigned char* lds, const Gemm g, const Sched& S, const Epi& E) {
;     ...
;         const bool has_next = S.next(ui + 1, nxt);
;         const char* nA = (has_next && !GATHER) ? (const char*)g.A + (size_t)nxt.pm * tstep : cA; const char* nB = has_next ? (const char*)g.Bt + (size_t)S.brow(nxt) * (size_t)K * 2 : cB;
; #pragma nounroll
;         for (int t = 0; t < nt; t += 2) {
;             const bool last = (t == nt - 2);
;             const char* a1 = cA + (size_t)(t + 1) * kstep;
;             const char* a2 = last ? nA : cA + (size_t)(t + 2) * kstep; const char* b2 = last ? nB : cB + (size_t)(t + 2) * kstep;
;     ...
;             PG8_LDB(B0, 0, 0); PG8_LDB(B1, 0, 1); PG8_SCHED; PG8_LDA(At, 0, 0); PG8_STAGE_A(PG8_SA(1, 1), a1, 1, gcur);
;             PG8_WAIT_V(8); PG8_WAIT_L(0); PG8_BAR; PG8_MMA(0, 0, At, B0); PG8_MMA(0, 1, At, B1); PG8_BAR; PG8_SCHED;
;             PG8_LDA(At, 0, 1); PG8_STAGE(PG8_SB(0, 0), b2, voffB); PG8_STAGE(PG8_SB(0, 1), b2 + hstep, voffB); PG8_STAGE_A(PG8_SA(0, 0), a2, 0, gsel);
;             PG8_WAIT_V(8); PG8_WAIT_L(0); PG8_BAR; PG8_MMA(1, 0, At, B0); PG8_MMA(1, 1, At, B1); PG8_BAR; PG8_SCHED;
.LBB0_222:
	s_mov_b32 s44, s5
	s_ashr_i32 s45, s5, 31
	s_lshl_b64 s[10:11], s[44:45], 19
	s_add_u32 s48, s65, s10
	s_addc_u32 s49, s66, s11
	s_mov_b32 s93, s12
	s_and_b64 s[10:11], s[46:47], exec
	s_cselect_b32 s5, s49, s7
	s_cselect_b32 s12, s48, s6
	s_lshl_b32 s10, s93, 8
	s_ashr_i32 s11, s10, 31
	s_lshl_b64 s[10:11], s[10:11], 11
	s_add_u32 s50, s62, s10
	s_addc_u32 s51, s63, s11
	s_and_b64 s[10:11], s[46:47], exec
	s_cselect_b32 s13, s51, s9
	s_cselect_b32 s14, s50, s8
	s_add_u32 s6, s6, 0x40080
	s_addc_u32 s7, s7, 0
	s_add_u32 s15, s8, 0x100
	s_addc_u32 s16, s9, 0
	s_mov_b32 s45, -2
	ds_read_b128 v[74:77], v164
	ds_read_b128 v[78:81], v164 offset:1024
	ds_read_b128 v[152:155], v164 offset:2048
	ds_read_b128 v[156:159], v164 offset:3072
	ds_read_b128 v[170:173], v165
	ds_read_b128 v[174:177], v165 offset:1024
	ds_read_b128 v[178:181], v165 offset:2048
	ds_read_b128 v[182:185], v165 offset:3072
	s_add_u32 s8, s6, 0xfffc0080
	s_addc_u32 s9, s7, -1
	s_cmp_eq_u32 s45, 12
	s_cselect_b32 s11, s5, s9
	s_cselect_b32 s10, s12, s8
	s_cselect_b32 s9, s13, s16
	s_cselect_b32 s8, s14, s15
	v_lshl_add_u64 v[160:161], s[6:7], 0, v[146:147]
	s_add_i32 m0, s67, 0xc000
	ds_read_b128 v[186:189], v166
	ds_read_b128 v[190:193], v166 offset:1024
	ds_read_b128 v[194:197], v166 offset:2048
	ds_read_b128 v[198:201], v166 offset:3072
	ds_read_b128 v[202:205], v166 offset:4096
	ds_read_b128 v[206:209], v166 offset:5120
	ds_read_b128 v[210:213], v166 offset:6144
	ds_read_b128 v[214:217], v166 offset:7168
	global_load_lds_dwordx4 v[160:161], off
	v_lshl_add_u64 v[160:161], s[6:7], 0, v[148:149]
	s_add_i32 m0, s67, 0xe000
	s_nop 0
	global_load_lds_dwordx4 v[160:161], off
	s_waitcnt vmcnt(8)
	s_waitcnt lgkmcnt(0)
	s_barrier
	s_setprio 1
	s_waitcnt lgkmcnt(0)
	v_mfma_f32_16x16x32_bf16 v[134:137], v[74:77], v[186:189], 0
	v_mfma_f32_16x16x32_bf16 v[130:133], v[152:155], v[186:189], 0
	v_mfma_f32_16x16x32_bf16 v[126:129], v[74:77], v[194:197], 0
	v_mfma_f32_16x16x32_bf16 v[122:125], v[152:155], v[194:197], 0
	v_mfma_f32_16x16x32_bf16 v[118:121], v[74:77], v[202:205], 0
	v_mfma_f32_16x16x32_bf16 v[114:117], v[152:155], v[202:205], 0
	v_mfma_f32_16x16x32_bf16 v[110:113], v[74:77], v[210:213], 0
	v_mfma_f32_16x16x32_bf16 v[106:109], v[152:155], v[210:213], 0
	v_mfma_f32_16x16x32_bf16 v[134:137], v[78:81], v[190:193], v[134:137]
	v_mfma_f32_16x16x32_bf16 v[130:133], v[156:159], v[190:193], v[130:133]
	v_mfma_f32_16x16x32_bf16 v[126:129], v[78:81], v[198:201], v[126:129]
	v_mfma_f32_16x16x32_bf16 v[122:125], v[156:159], v[198:201], v[122:125]
	v_mfma_f32_16x16x32_bf16 v[118:121], v[78:81], v[206:209], v[118:121]
	v_mfma_f32_16x16x32_bf16 v[114:117], v[156:159], v[206:209], v[114:117]
	v_mfma_f32_16x16x32_bf16 v[110:113], v[78:81], v[214:217], v[110:113]
	v_mfma_f32_16x16x32_bf16 v[106:109], v[156:159], v[214:217], v[106:109]
	s_setprio 0
	s_setprio 1
	v_mfma_f32_16x16x32_bf16 v[62:65], v[170:173], v[186:189], 0
	v_mfma_f32_16x16x32_bf16 v[58:61], v[178:181], v[186:189], 0
	v_mfma_f32_16x16x32_bf16 v[54:57], v[170:173], v[194:197], 0
	v_mfma_f32_16x16x32_bf16 v[50:53], v[178:181], v[194:197], 0
	v_mfma_f32_16x16x32_bf16 v[46:49], v[170:173], v[202:205], 0
	v_mfma_f32_16x16x32_bf16 v[42:45], v[178:181], v[202:205], 0
	v_mfma_f32_16x16x32_bf16 v[38:41], v[170:173], v[210:213], 0
	v_mfma_f32_16x16x32_bf16 v[34:37], v[178:181], v[210:213], 0
	v_mfma_f32_16x16x32_bf16 v[62:65], v[174:177], v[190:193], v[62:65]
	v_mfma_f32_16x16x32_bf16 v[58:61], v[182:185], v[190:193], v[58:61]
	v_mfma_f32_16x16x32_bf16 v[54:57], v[174:177], v[198:201], v[54:57]
	v_mfma_f32_16x16x32_bf16 v[50:53], v[182:185], v[198:201], v[50:53]
	v_mfma_f32_16x16x32_bf16 v[46:49], v[174:177], v[206:209], v[46:49]
	v_mfma_f32_16x16x32_bf16 v[42:45], v[182:185], v[206:209], v[42:45]
	v_mfma_f32_16x16x32_bf16 v[38:41], v[174:177], v[214:217], v[38:41]
	v_mfma_f32_16x16x32_bf16 v[34:37], v[182:185], v[214:217], v[34:37]
	s_setprio 0
	s_barrier
	s_add_i32 s53, s85, s35
	v_lshl_add_u64 v[160:161], s[8:9], 0, v[140:141]
	s_mov_b32 m0, s53
	ds_read_b128 v[186:189], v166 offset:16384
	ds_read_b128 v[190:193], v166 offset:17408
	ds_read_b128 v[194:197], v166 offset:18432
	ds_read_b128 v[198:201], v166 offset:19456
	ds_read_b128 v[202:205], v166 offset:20480
	ds_read_b128 v[206:209], v166 offset:21504
	ds_read_b128 v[210:213], v166 offset:22528
	ds_read_b128 v[214:217], v166 offset:23552
	global_load_lds_dwordx4 v[160:161], off
	s_add_i32 m0, s53, 0x2000
	s_add_u32 s54, s8, 0x40000
	v_lshl_add_u64 v[218:219], s[8:9], 0, v[144:145]
	s_addc_u32 s55, s9, 0
	s_add_i32 s53, s86, s35
	global_load_lds_dwordx4 v[218:219], off
	v_lshl_add_u64 v[220:221], s[54:55], 0, v[140:141]
	s_mov_b32 m0, s53
	v_lshl_add_u64 v[222:223], s[10:11], 0, v[142:143]
	global_load_lds_dwordx4 v[220:221], off
	v_lshl_add_u64 v[220:221], s[54:55], 0, v[144:145]
	s_add_i32 m0, s53, 0x2000
	s_nop 0
	global_load_lds_dwordx4 v[220:221], off
	v_lshl_add_u64 v[220:221], s[10:11], 0, v[138:139]
	s_mov_b32 m0, s67
	s_nop 0
	global_load_lds_dwordx4 v[220:221], off
	s_mov_b32 m0, s68
	s_nop 0
	global_load_lds_dwordx4 v[222:223], off
	s_waitcnt vmcnt(8)
	s_waitcnt lgkmcnt(0)
	s_barrier
; #define PG8_STAGE_A(bufoff, kbase, h, gv) do { if constexpr (GATHER) { PG8_STAGE(bufoff, kbase, (gv)[h]); } else { PG8_STAGE(bufoff, (kbase) + (h) * hstep, voffA); } } while (0)
; #define PG8_WAIT_V(n) asm volatile("s_waitcnt vmcnt(" #n ")" ::: "memory")
; #define PG8_WAIT_L(n) asm volatile("s_waitcnt lgkmcnt(" #n ")" ::: "memory")
; #define PG8_BAR __builtin_amdgcn_s_barrier()
; #define PG8_SCHED __builtin_amdgcn_sched_barrier(0)
; template <class Epi, class Sched, bool ALIGN_EPI = false, bool SP2 = false, bool FP8 = false, bool GATHER = false>
; __device__ __forceinline__ void gemm_phase(PG8_LAS unsigned char* lds, const Gemm g, const Sched& S, const Epi& E) {
;     ...
;             PG8_WAIT_V(8); PG8_WAIT_L(0); PG8_BAR; PG8_MMA(1, 0, At, B0); PG8_MMA(1, 1, At, B1); PG8_BAR; PG8_SCHED;
;             PG8_LDB(B0, 1, 0); PG8_LDB(B1, 1, 1); PG8_SCHED; PG8_LDA(At, 1, 0); PG8_STAGE_A(PG8_SA(0, 1), a2, 1, gsel);
;             PG8_WAIT_V(8); PG8_WAIT_L(0); PG8_BAR; PG8_MMA(0, 0, At, B0); PG8_MMA(0, 1, At, B1); PG8_BAR; PG8_SCHED;
	s_setprio 1
	s_waitcnt lgkmcnt(0)
	v_mfma_f32_16x16x32_bf16 v[102:105], v[74:77], v[186:189], 0
	v_mfma_f32_16x16x32_bf16 v[98:101], v[152:155], v[186:189], 0
	v_mfma_f32_16x16x32_bf16 v[94:97], v[74:77], v[194:197], 0
	v_mfma_f32_16x16x32_bf16 v[90:93], v[152:155], v[194:197], 0
	v_mfma_f32_16x16x32_bf16 v[86:89], v[74:77], v[202:205], 0
	v_mfma_f32_16x16x32_bf16 v[82:85], v[152:155], v[202:205], 0
	v_mfma_f32_16x16x32_bf16 v[70:73], v[74:77], v[210:213], 0
	v_mfma_f32_16x16x32_bf16 v[66:69], v[152:155], v[210:213], 0
	v_mfma_f32_16x16x32_bf16 v[102:105], v[78:81], v[190:193], v[102:105]
	v_mfma_f32_16x16x32_bf16 v[98:101], v[156:159], v[190:193], v[98:101]
	v_mfma_f32_16x16x32_bf16 v[94:97], v[78:81], v[198:201], v[94:97]
	v_mfma_f32_16x16x32_bf16 v[90:93], v[156:159], v[198:201], v[90:93]
	v_mfma_f32_16x16x32_bf16 v[86:89], v[78:81], v[206:209], v[86:89]
	v_mfma_f32_16x16x32_bf16 v[82:85], v[156:159], v[206:209], v[82:85]
	v_mfma_f32_16x16x32_bf16 v[70:73], v[78:81], v[214:217], v[70:73]
	v_mfma_f32_16x16x32_bf16 v[66:69], v[156:159], v[214:217], v[66:69]
	s_setprio 0
	s_setprio 1
	v_mfma_f32_16x16x32_bf16 v[30:33], v[170:173], v[186:189], 0
	v_mfma_f32_16x16x32_bf16 v[26:29], v[178:181], v[186:189], 0
	v_mfma_f32_16x16x32_bf16 v[22:25], v[170:173], v[194:197], 0
	v_mfma_f32_16x16x32_bf16 v[18:21], v[178:181], v[194:197], 0
	v_mfma_f32_16x16x32_bf16 v[14:17], v[170:173], v[202:205], 0
	v_mfma_f32_16x16x32_bf16 v[10:13], v[178:181], v[202:205], 0
	v_mfma_f32_16x16x32_bf16 v[6:9], v[170:173], v[210:213], 0
	v_mfma_f32_16x16x32_bf16 v[2:5], v[178:181], v[210:213], 0
	v_mfma_f32_16x16x32_bf16 v[30:33], v[174:177], v[190:193], v[30:33]
	v_mfma_f32_16x16x32_bf16 v[26:29], v[182:185], v[190:193], v[26:29]
	v_mfma_f32_16x16x32_bf16 v[22:25], v[174:177], v[198:201], v[22:25]
	v_mfma_f32_16x16x32_bf16 v[18:21], v[182:185], v[198:201], v[18:21]
	v_mfma_f32_16x16x32_bf16 v[14:17], v[174:177], v[206:209], v[14:17]
	v_mfma_f32_16x16x32_bf16 v[10:13], v[182:185], v[206:209], v[10:13]
	v_mfma_f32_16x16x32_bf16 v[6:9], v[174:177], v[214:217], v[6:9]
	v_mfma_f32_16x16x32_bf16 v[2:5], v[182:185], v[214:217], v[2:5]
	s_setprio 0
	s_barrier
	s_add_i32 s53, 0, 0x18000
	s_add_i32 s54, 0, 0x1c000
	v_add_u32_e32 v156, s53, v163
	v_add_u32_e32 v182, s54, v163
	ds_read_b128 v[74:77], v156
	ds_read_b128 v[78:81], v156 offset:1024
	ds_read_b128 v[152:155], v156 offset:2048
	ds_read_b128 v[156:159], v156 offset:3072
	ds_read_b128 v[170:173], v182
	ds_read_b128 v[174:177], v182 offset:1024
	ds_read_b128 v[178:181], v182 offset:2048
	ds_read_b128 v[182:185], v182 offset:3072
	s_add_u32 s10, s10, 0x40000
	s_addc_u32 s11, s11, 0
	s_mov_b32 m0, s69
	v_lshl_add_u64 v[224:225], s[10:11], 0, v[138:139]
	ds_read_b128 v[186:189], v166 offset:32768
	ds_read_b128 v[190:193], v166 offset:33792
	ds_read_b128 v[194:197], v166 offset:34816
	ds_read_b128 v[198:201], v166 offset:35840
	ds_read_b128 v[202:205], v166 offset:36864
	ds_read_b128 v[206:209], v166 offset:37888
	ds_read_b128 v[210:213], v166 offset:38912
	ds_read_b128 v[214:217], v166 offset:39936
	global_load_lds_dwordx4 v[224:225], off
	v_lshl_add_u64 v[224:225], s[10:11], 0, v[142:143]
	s_mov_b32 m0, s70
	s_nop 0
	global_load_lds_dwordx4 v[224:225], off
	s_waitcnt vmcnt(8)
	s_waitcnt lgkmcnt(0)
	s_barrier
	s_setprio 1
	s_waitcnt lgkmcnt(0)
	v_mfma_f32_16x16x32_bf16 v[134:137], v[74:77], v[186:189], v[134:137]
	v_mfma_f32_16x16x32_bf16 v[130:133], v[152:155], v[186:189], v[130:133]
	v_mfma_f32_16x16x32_bf16 v[126:129], v[74:77], v[194:197], v[126:129]
	v_mfma_f32_16x16x32_bf16 v[122:125], v[152:155], v[194:197], v[122:125]
	v_mfma_f32_16x16x32_bf16 v[118:121], v[74:77], v[202:205], v[118:121]
	v_mfma_f32_16x16x32_bf16 v[114:117], v[152:155], v[202:205], v[114:117]
	v_mfma_f32_16x16x32_bf16 v[110:113], v[74:77], v[210:213], v[110:113]
	v_mfma_f32_16x16x32_bf16 v[106:109], v[152:155], v[210:213], v[106:109]
	v_mfma_f32_16x16x32_bf16 v[134:137], v[78:81], v[190:193], v[134:137]
	v_mfma_f32_16x16x32_bf16 v[130:133], v[156:159], v[190:193], v[130:133]
	v_mfma_f32_16x16x32_bf16 v[126:129], v[78:81], v[198:201], v[126:129]
	v_mfma_f32_16x16x32_bf16 v[122:125], v[156:159], v[198:201], v[122:125]
	v_mfma_f32_16x16x32_bf16 v[118:121], v[78:81], v[206:209], v[118:121]
	v_mfma_f32_16x16x32_bf16 v[114:117], v[156:159], v[206:209], v[114:117]
	v_mfma_f32_16x16x32_bf16 v[110:113], v[78:81], v[214:217], v[110:113]
	v_mfma_f32_16x16x32_bf16 v[106:109], v[156:159], v[214:217], v[106:109]
	s_setprio 0
	s_setprio 1
	v_mfma_f32_16x16x32_bf16 v[62:65], v[170:173], v[186:189], v[62:65]
	v_mfma_f32_16x16x32_bf16 v[58:61], v[178:181], v[186:189], v[58:61]
	v_mfma_f32_16x16x32_bf16 v[54:57], v[170:173], v[194:197], v[54:57]
	v_mfma_f32_16x16x32_bf16 v[50:53], v[178:181], v[194:197], v[50:53]
	v_mfma_f32_16x16x32_bf16 v[46:49], v[170:173], v[202:205], v[46:49]
	v_mfma_f32_16x16x32_bf16 v[42:45], v[178:181], v[202:205], v[42:45]
	v_mfma_f32_16x16x32_bf16 v[38:41], v[170:173], v[210:213], v[38:41]
	v_mfma_f32_16x16x32_bf16 v[34:37], v[178:181], v[210:213], v[34:37]
	v_mfma_f32_16x16x32_bf16 v[62:65], v[174:177], v[190:193], v[62:65]
	v_mfma_f32_16x16x32_bf16 v[58:61], v[182:185], v[190:193], v[58:61]
	v_mfma_f32_16x16x32_bf16 v[54:57], v[174:177], v[198:201], v[54:57]
	v_mfma_f32_16x16x32_bf16 v[50:53], v[182:185], v[198:201], v[50:53]
	v_mfma_f32_16x16x32_bf16 v[46:49], v[174:177], v[206:209], v[46:49]
	v_mfma_f32_16x16x32_bf16 v[42:45], v[182:185], v[206:209], v[42:45]
	v_mfma_f32_16x16x32_bf16 v[38:41], v[174:177], v[214:217], v[38:41]
	v_mfma_f32_16x16x32_bf16 v[34:37], v[182:185], v[214:217], v[34:37]
	s_setprio 0
	s_barrier
; #define PG8_STAGE(bufoff, gbase, voff) do { _Pragma("unroll") for (int _i = 0; _i < 2; ++_i) \
;         __builtin_amdgcn_global_load_lds((const unsigned*)((const char*)(gbase) + (voff)[_i]), (PG8_LAS unsigned*)(lds + (bufoff) + ldsw + _i * 8192), 16, 0, 0); } while (0)
; #define PG8_STAGE_A(bufoff, kbase, h, gv) do { if constexpr (GATHER) { PG8_STAGE(bufoff, kbase, (gv)[h]); } else { PG8_STAGE(bufoff, (kbase) + (h) * hstep, voffA); } } while (0)
; #define PG8_WAIT_V(n) asm volatile("s_waitcnt vmcnt(" #n ")" ::: "memory")
; #define PG8_WAIT_L(n) asm volatile("s_waitcnt lgkmcnt(" #n ")" ::: "memory")
; #define PG8_BAR __builtin_amdgcn_s_barrier()
; #define PG8_SCHED __builtin_amdgcn_sched_barrier(0)
; template <class Epi, class Sched, bool ALIGN_EPI = false, bool SP2 = false, bool FP8 = false, bool GATHER = false>
; __device__ __forceinline__ void gemm_phase(PG8_LAS unsigned char* lds, const Gemm g, const Sched& S, const Epi& E) {
;     ...
;         for (int t = 0; t < nt; t += 2) {
;     ...
;             PG8_LDB(B0, 0, 0); PG8_LDB(B1, 0, 1); PG8_SCHED; PG8_LDA(At, 0, 0); PG8_STAGE_A(PG8_SA(1, 1), a1, 1, gcur);
;             PG8_WAIT_V(8); PG8_WAIT_L(0); PG8_BAR; PG8_MMA(0, 0, At, B0); PG8_MMA(0, 1, At, B1); PG8_BAR; PG8_SCHED;
;             PG8_LDA(At, 0, 1); PG8_STAGE(PG8_SB(0, 0), b2, voffB); PG8_STAGE(PG8_SB(0, 1), b2 + hstep, voffB); PG8_STAGE_A(PG8_SA(0, 0), a2, 0, gsel);
;     ...
;             PG8_LDA(At, 1, 1); PG8_STAGE(PG8_SB(1, 0), b3, voffB); PG8_STAGE(PG8_SB(1, 1), b3 + hstep, voffB); PG8_STAGE_A(PG8_SA(1, 0), a3, 0, gsel);
;             PG8_WAIT_V(8); PG8_WAIT_L(0); PG8_BAR; PG8_MMA(1, 0, At, B0); PG8_MMA(1, 1, At, B1); PG8_BAR; PG8_SCHED;
	s_add_i32 s10, s53, s35
	v_lshl_add_u64 v[160:161], v[160:161], 0, s[26:27]
	s_mov_b32 m0, s10
	ds_read_b128 v[186:189], v166 offset:49152
	ds_read_b128 v[190:193], v166 offset:50176
	ds_read_b128 v[194:197], v166 offset:51200
	ds_read_b128 v[198:201], v166 offset:52224
	ds_read_b128 v[202:205], v166 offset:53248
	ds_read_b128 v[206:209], v166 offset:54272
	ds_read_b128 v[210:213], v166 offset:55296
	ds_read_b128 v[214:217], v166 offset:56320
	global_load_lds_dwordx4 v[160:161], off
	s_add_i32 m0, s10, 0x2000
	s_add_u32 s8, s8, 0x40080
	v_lshl_add_u64 v[160:161], v[218:219], 0, s[26:27]
	s_addc_u32 s9, s9, 0
	s_add_i32 s10, s54, s35
	global_load_lds_dwordx4 v[160:161], off
	v_lshl_add_u64 v[160:161], s[8:9], 0, v[140:141]
	s_mov_b32 m0, s10
	s_nop 0
	global_load_lds_dwordx4 v[160:161], off
	v_lshl_add_u64 v[160:161], s[8:9], 0, v[144:145]
	s_add_i32 m0, s10, 0x2000
	s_nop 0
	global_load_lds_dwordx4 v[160:161], off
	v_lshl_add_u64 v[160:161], v[220:221], 0, s[26:27]
	s_mov_b32 m0, s77
	s_nop 0
	global_load_lds_dwordx4 v[160:161], off
	v_lshl_add_u64 v[160:161], v[222:223], 0, s[26:27]
	s_mov_b32 m0, s78
	s_nop 0
	global_load_lds_dwordx4 v[160:161], off
	s_waitcnt vmcnt(8)
	s_waitcnt lgkmcnt(0)
	s_barrier
	s_setprio 1
	s_waitcnt lgkmcnt(0)
	v_mfma_f32_16x16x32_bf16 v[102:105], v[74:77], v[186:189], v[102:105]
	v_mfma_f32_16x16x32_bf16 v[98:101], v[152:155], v[186:189], v[98:101]
	v_mfma_f32_16x16x32_bf16 v[94:97], v[74:77], v[194:197], v[94:97]
	v_mfma_f32_16x16x32_bf16 v[90:93], v[152:155], v[194:197], v[90:93]
	v_mfma_f32_16x16x32_bf16 v[86:89], v[74:77], v[202:205], v[86:89]
	v_mfma_f32_16x16x32_bf16 v[82:85], v[152:155], v[202:205], v[82:85]
	v_mfma_f32_16x16x32_bf16 v[70:73], v[74:77], v[210:213], v[70:73]
	v_mfma_f32_16x16x32_bf16 v[66:69], v[152:155], v[210:213], v[66:69]
	v_mfma_f32_16x16x32_bf16 v[102:105], v[78:81], v[190:193], v[102:105]
	v_mfma_f32_16x16x32_bf16 v[98:101], v[156:159], v[190:193], v[98:101]
	v_mfma_f32_16x16x32_bf16 v[94:97], v[78:81], v[198:201], v[94:97]
	v_mfma_f32_16x16x32_bf16 v[90:93], v[156:159], v[198:201], v[90:93]
	v_mfma_f32_16x16x32_bf16 v[86:89], v[78:81], v[206:209], v[86:89]
	v_mfma_f32_16x16x32_bf16 v[82:85], v[156:159], v[206:209], v[82:85]
	v_mfma_f32_16x16x32_bf16 v[70:73], v[78:81], v[214:217], v[70:73]
	v_mfma_f32_16x16x32_bf16 v[66:69], v[156:159], v[214:217], v[66:69]
	s_setprio 0
	s_setprio 1
	v_mfma_f32_16x16x32_bf16 v[30:33], v[170:173], v[186:189], v[30:33]
	v_mfma_f32_16x16x32_bf16 v[26:29], v[178:181], v[186:189], v[26:29]
	v_mfma_f32_16x16x32_bf16 v[22:25], v[170:173], v[194:197], v[22:25]
	v_mfma_f32_16x16x32_bf16 v[18:21], v[178:181], v[194:197], v[18:21]
	v_mfma_f32_16x16x32_bf16 v[14:17], v[170:173], v[202:205], v[14:17]
	v_mfma_f32_16x16x32_bf16 v[10:13], v[178:181], v[202:205], v[10:13]
	v_mfma_f32_16x16x32_bf16 v[6:9], v[170:173], v[210:213], v[6:9]
	v_mfma_f32_16x16x32_bf16 v[2:5], v[178:181], v[210:213], v[2:5]
	v_mfma_f32_16x16x32_bf16 v[30:33], v[174:177], v[190:193], v[30:33]
	v_mfma_f32_16x16x32_bf16 v[26:29], v[182:185], v[190:193], v[26:29]
	v_mfma_f32_16x16x32_bf16 v[22:25], v[174:177], v[198:201], v[22:25]
	v_mfma_f32_16x16x32_bf16 v[18:21], v[182:185], v[198:201], v[18:21]
	v_mfma_f32_16x16x32_bf16 v[14:17], v[174:177], v[206:209], v[14:17]
	v_mfma_f32_16x16x32_bf16 v[10:13], v[182:185], v[206:209], v[10:13]
	v_mfma_f32_16x16x32_bf16 v[6:9], v[174:177], v[214:217], v[6:9]
	v_mfma_f32_16x16x32_bf16 v[2:5], v[182:185], v[214:217], v[2:5]
	s_setprio 0
	s_add_i32 s45, s45, 2
	s_add_u32 s6, s6, 0x100
	s_addc_u32 s7, s7, 0
	s_add_u32 s15, s15, 0x100
	s_addc_u32 s16, s16, 0
	s_cmp_gt_u32 s45, 13
.LBB0_223:
	s_barrier
	ds_read_b128 v[74:77], v164
	ds_read_b128 v[78:81], v164 offset:1024
	ds_read_b128 v[152:155], v164 offset:2048
	ds_read_b128 v[156:159], v164 offset:3072
	ds_read_b128 v[170:173], v165
	ds_read_b128 v[174:177], v165 offset:1024
	ds_read_b128 v[178:181], v165 offset:2048
	ds_read_b128 v[182:185], v165 offset:3072
	s_add_u32 s8, s6, 0xfffc0080
	s_addc_u32 s9, s7, -1
	s_cmp_eq_u32 s45, 12
	s_cselect_b32 s11, s5, s9
	s_cselect_b32 s10, s12, s8
	s_cselect_b32 s9, s13, s16
	s_cselect_b32 s8, s14, s15
	v_lshl_add_u64 v[160:161], s[6:7], 0, v[146:147]
	s_add_i32 m0, s67, 0xc000
	ds_read_b128 v[186:189], v166
	ds_read_b128 v[190:193], v166 offset:1024
	ds_read_b128 v[194:197], v166 offset:2048
	ds_read_b128 v[198:201], v166 offset:3072
	ds_read_b128 v[202:205], v166 offset:4096
	ds_read_b128 v[206:209], v166 offset:5120
	ds_read_b128 v[210:213], v166 offset:6144
	ds_read_b128 v[214:217], v166 offset:7168
	global_load_lds_dwordx4 v[160:161], off
	v_lshl_add_u64 v[160:161], s[6:7], 0, v[148:149]
	s_add_i32 m0, s67, 0xe000
	s_nop 0
	global_load_lds_dwordx4 v[160:161], off
	s_waitcnt vmcnt(8)
	s_waitcnt lgkmcnt(0)
	s_barrier
; #define PG8_STAGE(bufoff, gbase, voff) do { _Pragma("unroll") for (int _i = 0; _i < 2; ++_i) \
;         __builtin_amdgcn_global_load_lds((const unsigned*)((const char*)(gbase) + (voff)[_i]), (PG8_LAS unsigned*)(lds + (bufoff) + ldsw + _i * 8192), 16, 0, 0); } while (0)
; #define PG8_STAGE_A(bufoff, kbase, h, gv) do { if constexpr (GATHER) { PG8_STAGE(bufoff, kbase, (gv)[h]); } else { PG8_STAGE(bufoff, (kbase) + (h) * hstep, voffA); } } while (0)
; #define PG8_WAIT_V(n) asm volatile("s_waitcnt vmcnt(" #n ")" ::: "memory")
; #define PG8_WAIT_L(n) asm volatile("s_waitcnt lgkmcnt(" #n ")" ::: "memory")
; #define PG8_BAR __builtin_amdgcn_s_barrier()
; #define PG8_SCHED __builtin_amdgcn_sched_barrier(0)
; template <class Epi, class Sched, bool ALIGN_EPI = false, bool SP2 = false, bool FP8 = false, bool GATHER = false>
; __device__ __forceinline__ void gemm_phase(PG8_LAS unsigned char* lds, const Gemm g, const Sched& S, const Epi& E) {
;     ...
;             PG8_WAIT_V(8); PG8_WAIT_L(0); PG8_BAR; PG8_MMA(0, 0, At, B0); PG8_MMA(0, 1, At, B1); PG8_BAR; PG8_SCHED;
;             PG8_LDA(At, 0, 1); PG8_STAGE(PG8_SB(0, 0), b2, voffB); PG8_STAGE(PG8_SB(0, 1), b2 + hstep, voffB); PG8_STAGE_A(PG8_SA(0, 0), a2, 0, gsel);
;             PG8_WAIT_V(8); PG8_WAIT_L(0); PG8_BAR; PG8_MMA(1, 0, At, B0); PG8_MMA(1, 1, At, B1); PG8_BAR; PG8_SCHED;
	s_setprio 1
	s_waitcnt lgkmcnt(0)
	v_mfma_f32_16x16x32_bf16 v[134:137], v[74:77], v[186:189], v[134:137]
	v_mfma_f32_16x16x32_bf16 v[130:133], v[152:155], v[186:189], v[130:133]
	v_mfma_f32_16x16x32_bf16 v[126:129], v[74:77], v[194:197], v[126:129]
	v_mfma_f32_16x16x32_bf16 v[122:125], v[152:155], v[194:197], v[122:125]
	v_mfma_f32_16x16x32_bf16 v[118:121], v[74:77], v[202:205], v[118:121]
	v_mfma_f32_16x16x32_bf16 v[114:117], v[152:155], v[202:205], v[114:117]
	v_mfma_f32_16x16x32_bf16 v[110:113], v[74:77], v[210:213], v[110:113]
	v_mfma_f32_16x16x32_bf16 v[106:109], v[152:155], v[210:213], v[106:109]
	v_mfma_f32_16x16x32_bf16 v[134:137], v[78:81], v[190:193], v[134:137]
	v_mfma_f32_16x16x32_bf16 v[130:133], v[156:159], v[190:193], v[130:133]
	v_mfma_f32_16x16x32_bf16 v[126:129], v[78:81], v[198:201], v[126:129]
	v_mfma_f32_16x16x32_bf16 v[122:125], v[156:159], v[198:201], v[122:125]
	v_mfma_f32_16x16x32_bf16 v[118:121], v[78:81], v[206:209], v[118:121]
	v_mfma_f32_16x16x32_bf16 v[114:117], v[156:159], v[206:209], v[114:117]
	v_mfma_f32_16x16x32_bf16 v[110:113], v[78:81], v[214:217], v[110:113]
	v_mfma_f32_16x16x32_bf16 v[106:109], v[156:159], v[214:217], v[106:109]
	s_setprio 0
	s_setprio 1
	v_mfma_f32_16x16x32_bf16 v[62:65], v[170:173], v[186:189], v[62:65]
	v_mfma_f32_16x16x32_bf16 v[58:61], v[178:181], v[186:189], v[58:61]
	v_mfma_f32_16x16x32_bf16 v[54:57], v[170:173], v[194:197], v[54:57]
	v_mfma_f32_16x16x32_bf16 v[50:53], v[178:181], v[194:197], v[50:53]
	v_mfma_f32_16x16x32_bf16 v[46:49], v[170:173], v[202:205], v[46:49]
	v_mfma_f32_16x16x32_bf16 v[42:45], v[178:181], v[202:205], v[42:45]
	v_mfma_f32_16x16x32_bf16 v[38:41], v[170:173], v[210:213], v[38:41]
	v_mfma_f32_16x16x32_bf16 v[34:37], v[178:181], v[210:213], v[34:37]
	v_mfma_f32_16x16x32_bf16 v[62:65], v[174:177], v[190:193], v[62:65]
	v_mfma_f32_16x16x32_bf16 v[58:61], v[182:185], v[190:193], v[58:61]
	v_mfma_f32_16x16x32_bf16 v[54:57], v[174:177], v[198:201], v[54:57]
	v_mfma_f32_16x16x32_bf16 v[50:53], v[182:185], v[198:201], v[50:53]
	v_mfma_f32_16x16x32_bf16 v[46:49], v[174:177], v[206:209], v[46:49]
	v_mfma_f32_16x16x32_bf16 v[42:45], v[182:185], v[206:209], v[42:45]
	v_mfma_f32_16x16x32_bf16 v[38:41], v[174:177], v[214:217], v[38:41]
	v_mfma_f32_16x16x32_bf16 v[34:37], v[182:185], v[214:217], v[34:37]
	s_setprio 0
	s_barrier
	s_add_i32 s53, s85, s35
	v_lshl_add_u64 v[160:161], s[8:9], 0, v[140:141]
	s_mov_b32 m0, s53
	ds_read_b128 v[186:189], v166 offset:16384
	ds_read_b128 v[190:193], v166 offset:17408
	ds_read_b128 v[194:197], v166 offset:18432
	ds_read_b128 v[198:201], v166 offset:19456
	ds_read_b128 v[202:205], v166 offset:20480
	ds_read_b128 v[206:209], v166 offset:21504
	ds_read_b128 v[210:213], v166 offset:22528
	ds_read_b128 v[214:217], v166 offset:23552
	global_load_lds_dwordx4 v[160:161], off
	s_add_i32 m0, s53, 0x2000
	s_add_u32 s54, s8, 0x40000
	v_lshl_add_u64 v[218:219], s[8:9], 0, v[144:145]
	s_addc_u32 s55, s9, 0
	s_add_i32 s53, s86, s35
	global_load_lds_dwordx4 v[218:219], off
	v_lshl_add_u64 v[220:221], s[54:55], 0, v[140:141]
	s_mov_b32 m0, s53
	v_lshl_add_u64 v[222:223], s[10:11], 0, v[142:143]
	global_load_lds_dwordx4 v[220:221], off
	v_lshl_add_u64 v[220:221], s[54:55], 0, v[144:145]
	s_add_i32 m0, s53, 0x2000
	s_nop 0
	global_load_lds_dwordx4 v[220:221], off
	v_lshl_add_u64 v[220:221], s[10:11], 0, v[138:139]
	s_mov_b32 m0, s67
	s_nop 0
	global_load_lds_dwordx4 v[220:221], off
	s_mov_b32 m0, s68
	s_nop 0
	global_load_lds_dwordx4 v[222:223], off
	s_waitcnt vmcnt(8)
	s_waitcnt lgkmcnt(0)
	s_barrier
	s_setprio 1
	s_waitcnt lgkmcnt(0)
	v_mfma_f32_16x16x32_bf16 v[102:105], v[74:77], v[186:189], v[102:105]
	v_mfma_f32_16x16x32_bf16 v[98:101], v[152:155], v[186:189], v[98:101]
	v_mfma_f32_16x16x32_bf16 v[94:97], v[74:77], v[194:197], v[94:97]
	v_mfma_f32_16x16x32_bf16 v[90:93], v[152:155], v[194:197], v[90:93]
	v_mfma_f32_16x16x32_bf16 v[86:89], v[74:77], v[202:205], v[86:89]
	v_mfma_f32_16x16x32_bf16 v[82:85], v[152:155], v[202:205], v[82:85]
	v_mfma_f32_16x16x32_bf16 v[70:73], v[74:77], v[210:213], v[70:73]
	v_mfma_f32_16x16x32_bf16 v[66:69], v[152:155], v[210:213], v[66:69]
	v_mfma_f32_16x16x32_bf16 v[102:105], v[78:81], v[190:193], v[102:105]
	v_mfma_f32_16x16x32_bf16 v[98:101], v[156:159], v[190:193], v[98:101]
	v_mfma_f32_16x16x32_bf16 v[94:97], v[78:81], v[198:201], v[94:97]
	v_mfma_f32_16x16x32_bf16 v[90:93], v[156:159], v[198:201], v[90:93]
	v_mfma_f32_16x16x32_bf16 v[86:89], v[78:81], v[206:209], v[86:89]
	v_mfma_f32_16x16x32_bf16 v[82:85], v[156:159], v[206:209], v[82:85]
	v_mfma_f32_16x16x32_bf16 v[70:73], v[78:81], v[214:217], v[70:73]
	v_mfma_f32_16x16x32_bf16 v[66:69], v[156:159], v[214:217], v[66:69]
	s_setprio 0
	s_setprio 1
	v_mfma_f32_16x16x32_bf16 v[30:33], v[170:173], v[186:189], v[30:33]
	v_mfma_f32_16x16x32_bf16 v[26:29], v[178:181], v[186:189], v[26:29]
	v_mfma_f32_16x16x32_bf16 v[22:25], v[170:173], v[194:197], v[22:25]
	v_mfma_f32_16x16x32_bf16 v[18:21], v[178:181], v[194:197], v[18:21]
	v_mfma_f32_16x16x32_bf16 v[14:17], v[170:173], v[202:205], v[14:17]
	v_mfma_f32_16x16x32_bf16 v[10:13], v[178:181], v[202:205], v[10:13]
	v_mfma_f32_16x16x32_bf16 v[6:9], v[170:173], v[210:213], v[6:9]
	v_mfma_f32_16x16x32_bf16 v[2:5], v[178:181], v[210:213], v[2:5]
	v_mfma_f32_16x16x32_bf16 v[30:33], v[174:177], v[190:193], v[30:33]
	v_mfma_f32_16x16x32_bf16 v[26:29], v[182:185], v[190:193], v[26:29]
	v_mfma_f32_16x16x32_bf16 v[22:25], v[174:177], v[198:201], v[22:25]
	v_mfma_f32_16x16x32_bf16 v[18:21], v[182:185], v[198:201], v[18:21]
	v_mfma_f32_16x16x32_bf16 v[14:17], v[174:177], v[206:209], v[14:17]
	v_mfma_f32_16x16x32_bf16 v[10:13], v[182:185], v[206:209], v[10:13]
	v_mfma_f32_16x16x32_bf16 v[6:9], v[174:177], v[214:217], v[6:9]
	v_mfma_f32_16x16x32_bf16 v[2:5], v[182:185], v[214:217], v[2:5]
	s_setprio 0
	s_barrier
; #define PG8_STAGE_A(bufoff, kbase, h, gv) do { if constexpr (GATHER) { PG8_STAGE(bufoff, kbase, (gv)[h]); } else { PG8_STAGE(bufoff, (kbase) + (h) * hstep, voffA); } } while (0)
; #define PG8_WAIT_V(n) asm volatile("s_waitcnt vmcnt(" #n ")" ::: "memory")
; #define PG8_WAIT_L(n) asm volatile("s_waitcnt lgkmcnt(" #n ")" ::: "memory")
; #define PG8_BAR __builtin_amdgcn_s_barrier()
; #define PG8_SCHED __builtin_amdgcn_sched_barrier(0)
; template <class Epi, class Sched, bool ALIGN_EPI = false, bool SP2 = false, bool FP8 = false, bool GATHER = false>
; __device__ __forceinline__ void gemm_phase(PG8_LAS unsigned char* lds, const Gemm g, const Sched& S, const Epi& E) {
;     ...
;             PG8_LDB(B0, 1, 0); PG8_LDB(B1, 1, 1); PG8_SCHED; PG8_LDA(At, 1, 0); PG8_STAGE_A(PG8_SA(0, 1), a2, 1, gsel);
;             PG8_WAIT_V(8); PG8_WAIT_L(0); PG8_BAR; PG8_MMA(0, 0, At, B0); PG8_MMA(0, 1, At, B1); PG8_BAR; PG8_SCHED;
	s_add_i32 s53, 0, 0x18000
	s_add_i32 s54, 0, 0x1c000
	v_add_u32_e32 v156, s53, v163
	v_add_u32_e32 v182, s54, v163
	ds_read_b128 v[74:77], v156
	ds_read_b128 v[78:81], v156 offset:1024
	ds_read_b128 v[152:155], v156 offset:2048
	ds_read_b128 v[156:159], v156 offset:3072
	ds_read_b128 v[170:173], v182
	ds_read_b128 v[174:177], v182 offset:1024
	ds_read_b128 v[178:181], v182 offset:2048
	ds_read_b128 v[182:185], v182 offset:3072
	s_add_u32 s10, s10, 0x40000
	s_addc_u32 s11, s11, 0
	s_mov_b32 m0, s69
	v_lshl_add_u64 v[224:225], s[10:11], 0, v[138:139]
	ds_read_b128 v[186:189], v166 offset:32768
	ds_read_b128 v[190:193], v166 offset:33792
	ds_read_b128 v[194:197], v166 offset:34816
	ds_read_b128 v[198:201], v166 offset:35840
	ds_read_b128 v[202:205], v166 offset:36864
	ds_read_b128 v[206:209], v166 offset:37888
	ds_read_b128 v[210:213], v166 offset:38912
	ds_read_b128 v[214:217], v166 offset:39936
	global_load_lds_dwordx4 v[224:225], off
	v_lshl_add_u64 v[224:225], s[10:11], 0, v[142:143]
	s_mov_b32 m0, s70
	s_nop 0
	global_load_lds_dwordx4 v[224:225], off
	s_waitcnt vmcnt(8)
	s_waitcnt lgkmcnt(0)
	s_barrier
	s_setprio 1
	s_waitcnt lgkmcnt(0)
	v_mfma_f32_16x16x32_bf16 v[134:137], v[74:77], v[186:189], v[134:137]
	v_mfma_f32_16x16x32_bf16 v[130:133], v[152:155], v[186:189], v[130:133]
	v_mfma_f32_16x16x32_bf16 v[126:129], v[74:77], v[194:197], v[126:129]
	v_mfma_f32_16x16x32_bf16 v[122:125], v[152:155], v[194:197], v[122:125]
	v_mfma_f32_16x16x32_bf16 v[118:121], v[74:77], v[202:205], v[118:121]
	v_mfma_f32_16x16x32_bf16 v[114:117], v[152:155], v[202:205], v[114:117]
	v_mfma_f32_16x16x32_bf16 v[110:113], v[74:77], v[210:213], v[110:113]
	v_mfma_f32_16x16x32_bf16 v[106:109], v[152:155], v[210:213], v[106:109]
	v_mfma_f32_16x16x32_bf16 v[134:137], v[78:81], v[190:193], v[134:137]
	v_mfma_f32_16x16x32_bf16 v[130:133], v[156:159], v[190:193], v[130:133]
	v_mfma_f32_16x16x32_bf16 v[126:129], v[78:81], v[198:201], v[126:129]
	v_mfma_f32_16x16x32_bf16 v[122:125], v[156:159], v[198:201], v[122:125]
	v_mfma_f32_16x16x32_bf16 v[118:121], v[78:81], v[206:209], v[118:121]
	v_mfma_f32_16x16x32_bf16 v[114:117], v[156:159], v[206:209], v[114:117]
	v_mfma_f32_16x16x32_bf16 v[110:113], v[78:81], v[214:217], v[110:113]
	v_mfma_f32_16x16x32_bf16 v[106:109], v[156:159], v[214:217], v[106:109]
	s_setprio 0
	s_setprio 1
	v_mfma_f32_16x16x32_bf16 v[62:65], v[170:173], v[186:189], v[62:65]
	v_mfma_f32_16x16x32_bf16 v[58:61], v[178:181], v[186:189], v[58:61]
	v_mfma_f32_16x16x32_bf16 v[54:57], v[170:173], v[194:197], v[54:57]
	v_mfma_f32_16x16x32_bf16 v[50:53], v[178:181], v[194:197], v[50:53]
	v_mfma_f32_16x16x32_bf16 v[46:49], v[170:173], v[202:205], v[46:49]
	v_mfma_f32_16x16x32_bf16 v[42:45], v[178:181], v[202:205], v[42:45]
	v_mfma_f32_16x16x32_bf16 v[38:41], v[170:173], v[210:213], v[38:41]
	v_mfma_f32_16x16x32_bf16 v[34:37], v[178:181], v[210:213], v[34:37]
	v_mfma_f32_16x16x32_bf16 v[62:65], v[174:177], v[190:193], v[62:65]
	v_mfma_f32_16x16x32_bf16 v[58:61], v[182:185], v[190:193], v[58:61]
	v_mfma_f32_16x16x32_bf16 v[54:57], v[174:177], v[198:201], v[54:57]
	v_mfma_f32_16x16x32_bf16 v[50:53], v[182:185], v[198:201], v[50:53]
	v_mfma_f32_16x16x32_bf16 v[46:49], v[174:177], v[206:209], v[46:49]
	v_mfma_f32_16x16x32_bf16 v[42:45], v[182:185], v[206:209], v[42:45]
	v_mfma_f32_16x16x32_bf16 v[38:41], v[174:177], v[214:217], v[38:41]
	v_mfma_f32_16x16x32_bf16 v[34:37], v[182:185], v[214:217], v[34:37]
	s_setprio 0
	s_barrier
; #define PG8_STAGE(bufoff, gbase, voff) do { _Pragma("unroll") for (int _i = 0; _i < 2; ++_i) \
;         __builtin_amdgcn_global_load_lds((const unsigned*)((const char*)(gbase) + (voff)[_i]), (PG8_LAS unsigned*)(lds + (bufoff) + ldsw + _i * 8192), 16, 0, 0); } while (0)
; #define PG8_STAGE_A(bufoff, kbase, h, gv) do { if constexpr (GATHER) { PG8_STAGE(bufoff, kbase, (gv)[h]); } else { PG8_STAGE(bufoff, (kbase) + (h) * hstep, voffA); } } while (0)
; #define PG8_WAIT_V(n) asm volatile("s_waitcnt vmcnt(" #n ")" ::: "memory")
; #define PG8_WAIT_L(n) asm volatile("s_waitcnt lgkmcnt(" #n ")" ::: "memory")
; #define PG8_BAR __builtin_amdgcn_s_barrier()
; #define PG8_SCHED __builtin_amdgcn_sched_barrier(0)
; template <class Epi, class Sched, bool ALIGN_EPI = false, bool SP2 = false, bool FP8 = false, bool GATHER = false>
; __device__ __forceinline__ void gemm_phase(PG8_LAS unsigned char* lds, const Gemm g, const Sched& S, const Epi& E) {
;     ...
;         for (int t = 0; t < nt; t += 2) {
;     ...
;             PG8_LDA(At, 1, 1); PG8_STAGE(PG8_SB(1, 0), b3, voffB); PG8_STAGE(PG8_SB(1, 1), b3 + hstep, voffB); PG8_STAGE_A(PG8_SA(1, 0), a3, 0, gsel);
;             PG8_WAIT_V(8); PG8_WAIT_L(0); PG8_BAR; PG8_MMA(1, 0, At, B0); PG8_MMA(1, 1, At, B1); PG8_BAR; PG8_SCHED;
;     ...
;         if constexpr (ALIGN_EPI) { if (wr == 0) PG8_BAR; }
	s_add_i32 s10, s53, s35
	v_lshl_add_u64 v[160:161], v[160:161], 0, s[26:27]
	s_mov_b32 m0, s10
	ds_read_b128 v[186:189], v166 offset:49152
	ds_read_b128 v[190:193], v166 offset:50176
	ds_read_b128 v[194:197], v166 offset:51200
	ds_read_b128 v[198:201], v166 offset:52224
	ds_read_b128 v[202:205], v166 offset:53248
	ds_read_b128 v[206:209], v166 offset:54272
	ds_read_b128 v[210:213], v166 offset:55296
	ds_read_b128 v[214:217], v166 offset:56320
	global_load_lds_dwordx4 v[160:161], off
	s_add_i32 m0, s10, 0x2000
	s_add_u32 s8, s8, 0x40080
	v_lshl_add_u64 v[160:161], v[218:219], 0, s[26:27]
	s_addc_u32 s9, s9, 0
	s_add_i32 s10, s54, s35
	global_load_lds_dwordx4 v[160:161], off
	v_lshl_add_u64 v[160:161], s[8:9], 0, v[140:141]
	s_mov_b32 m0, s10
	s_nop 0
	global_load_lds_dwordx4 v[160:161], off
	v_lshl_add_u64 v[160:161], s[8:9], 0, v[144:145]
	s_add_i32 m0, s10, 0x2000
	s_nop 0
	global_load_lds_dwordx4 v[160:161], off
	v_lshl_add_u64 v[160:161], v[220:221], 0, s[26:27]
	s_mov_b32 m0, s77
	s_nop 0
	global_load_lds_dwordx4 v[160:161], off
	v_lshl_add_u64 v[160:161], v[222:223], 0, s[26:27]
	s_mov_b32 m0, s78
	s_nop 0
	global_load_lds_dwordx4 v[160:161], off
	s_waitcnt vmcnt(8)
	s_waitcnt lgkmcnt(0)
	s_barrier
	s_setprio 1
	s_waitcnt lgkmcnt(0)
	v_mfma_f32_16x16x32_bf16 v[102:105], v[74:77], v[186:189], v[102:105]
	v_mfma_f32_16x16x32_bf16 v[98:101], v[152:155], v[186:189], v[98:101]
	v_mfma_f32_16x16x32_bf16 v[94:97], v[74:77], v[194:197], v[94:97]
	v_mfma_f32_16x16x32_bf16 v[90:93], v[152:155], v[194:197], v[90:93]
	v_mfma_f32_16x16x32_bf16 v[86:89], v[74:77], v[202:205], v[86:89]
	v_mfma_f32_16x16x32_bf16 v[82:85], v[152:155], v[202:205], v[82:85]
	v_mfma_f32_16x16x32_bf16 v[70:73], v[74:77], v[210:213], v[70:73]
	v_mfma_f32_16x16x32_bf16 v[66:69], v[152:155], v[210:213], v[66:69]
	v_mfma_f32_16x16x32_bf16 v[102:105], v[78:81], v[190:193], v[102:105]
	v_mfma_f32_16x16x32_bf16 v[98:101], v[156:159], v[190:193], v[98:101]
	v_mfma_f32_16x16x32_bf16 v[94:97], v[78:81], v[198:201], v[94:97]
	v_mfma_f32_16x16x32_bf16 v[90:93], v[156:159], v[198:201], v[90:93]
	v_mfma_f32_16x16x32_bf16 v[86:89], v[78:81], v[206:209], v[86:89]
	v_mfma_f32_16x16x32_bf16 v[82:85], v[156:159], v[206:209], v[82:85]
	v_mfma_f32_16x16x32_bf16 v[70:73], v[78:81], v[214:217], v[70:73]
	v_mfma_f32_16x16x32_bf16 v[66:69], v[156:159], v[214:217], v[66:69]
	s_setprio 0
	s_setprio 1
	v_mfma_f32_16x16x32_bf16 v[30:33], v[170:173], v[186:189], v[30:33]
	v_mfma_f32_16x16x32_bf16 v[26:29], v[178:181], v[186:189], v[26:29]
	v_mfma_f32_16x16x32_bf16 v[22:25], v[170:173], v[194:197], v[22:25]
	v_mfma_f32_16x16x32_bf16 v[18:21], v[178:181], v[194:197], v[18:21]
	v_mfma_f32_16x16x32_bf16 v[14:17], v[170:173], v[202:205], v[14:17]
	v_mfma_f32_16x16x32_bf16 v[10:13], v[178:181], v[202:205], v[10:13]
	v_mfma_f32_16x16x32_bf16 v[6:9], v[170:173], v[210:213], v[6:9]
	v_mfma_f32_16x16x32_bf16 v[2:5], v[178:181], v[210:213], v[2:5]
	v_mfma_f32_16x16x32_bf16 v[30:33], v[174:177], v[190:193], v[30:33]
	v_mfma_f32_16x16x32_bf16 v[26:29], v[182:185], v[190:193], v[26:29]
	v_mfma_f32_16x16x32_bf16 v[22:25], v[174:177], v[198:201], v[22:25]
	v_mfma_f32_16x16x32_bf16 v[18:21], v[182:185], v[198:201], v[18:21]
	v_mfma_f32_16x16x32_bf16 v[14:17], v[174:177], v[206:209], v[14:17]
	v_mfma_f32_16x16x32_bf16 v[10:13], v[182:185], v[206:209], v[10:13]
	v_mfma_f32_16x16x32_bf16 v[6:9], v[174:177], v[214:217], v[6:9]
	v_mfma_f32_16x16x32_bf16 v[2:5], v[182:185], v[214:217], v[2:5]
	s_setprio 0
	s_add_i32 s45, s45, 2
	s_add_u32 s6, s6, 0x100
	s_addc_u32 s7, s7, 0
	s_add_u32 s15, s15, 0x100
	s_addc_u32 s16, s16, 0
	s_cmp_gt_u32 s45, 13
	s_cbranch_scc0 .LBB0_223
	s_barrier
	s_and_b64 vcc, exec, s[28:29]
	s_cbranch_vccz .LBB0_226
	s_barrier

; #define PG8_STAGE(bufoff, gbase, voff) do { _Pragma("unroll") for (int _i = 0; _i < 2; ++_i) \
;         __builtin_amdgcn_global_load_lds((const unsigned*)((const char*)(gbase) + (voff)[_i]), (PG8_LAS unsigned*)(lds + (bufoff) + ldsw + _i * 8192), 16, 0, 0); } while (0)
; #define PG8_STAGE_A(bufoff, kbase, h, gv) do { if constexpr (GATHER) { PG8_STAGE(bufoff, kbase, (gv)[h]); } else { PG8_STAGE(bufoff, (kbase) + (h) * hstep, voffA); } } while (0)
; #define PG8_WAIT_V(n) asm volatile("s_waitcnt vmcnt(" #n ")" ::: "memory")
; #define PG8_WAIT_L(n) asm volatile("s_waitcnt lgkmcnt(" #n ")" ::: "memory")
; #define PG8_BAR __builtin_amdgcn_s_barrier()
; #define PG8_SCHED __builtin_amdgcn_sched_barrier(0)
; template <class Epi, class Sched, bool ALIGN_EPI = false, bool SP2 = false, bool FP8 = false, bool GATHER = false>
; __device__ __forceinline__ void gemm_phase(PG8_LAS unsigned char* lds, const Gemm g, const Sched& S, const Epi& E) {
;     ...
;             PG8_LDB(B0, 0, 0); PG8_LDB(B1, 0, 1); PG8_SCHED; PG8_LDA(At, 0, 0); PG8_STAGE_A(PG8_SA(1, 1), a1, 1, gcur);
;             PG8_WAIT_V(8); PG8_WAIT_L(0); PG8_BAR; PG8_MMA(0, 0, At, B0); PG8_MMA(0, 1, At, B1); PG8_BAR; PG8_SCHED;
;             PG8_LDA(At, 0, 1); PG8_STAGE(PG8_SB(0, 0), b2, voffB); PG8_STAGE(PG8_SB(0, 1), b2 + hstep, voffB); PG8_STAGE_A(PG8_SA(0, 0), a2, 0, gsel);
;             PG8_WAIT_V(8); PG8_WAIT_L(0); PG8_BAR; PG8_MMA(1, 0, At, B0); PG8_MMA(1, 1, At, B1); PG8_BAR; PG8_SCHED;
.LBB0_592:
	v_add_u32_e32 v136, s82, v169
	ds_read_b128 v[124:127], v136
	ds_read_b128 v[128:131], v136 offset:1024
	ds_read_b128 v[132:135], v136 offset:2048
	ds_read_b128 v[164:167], v136 offset:3072
	v_add_u32_e32 v136, s83, v169
	ds_read_b128 v[172:175], v136
	ds_read_b128 v[176:179], v136 offset:1024
	ds_read_b128 v[180:183], v136 offset:2048
	ds_read_b128 v[184:187], v136 offset:3072
	s_add_u32 s60, s56, 0xfffc0080
	s_addc_u32 s61, s57, -1
	s_and_b64 s[58:59], s[58:59], exec
	s_cselect_b32 s61, s61, s47
	s_cselect_b32 s60, s60, s85
	s_cselect_b32 s59, s88, s86
	s_cselect_b32 s58, s55, s87
	v_lshl_add_u64 v[136:137], s[56:57], 0, v[154:155]
	s_add_i32 m0, s53, 0xc000
	ds_read_b128 v[188:191], v170
	ds_read_b128 v[192:195], v170 offset:1024
	ds_read_b128 v[196:199], v170 offset:2048
	ds_read_b128 v[200:203], v170 offset:3072
	ds_read_b128 v[204:207], v170 offset:4096
	ds_read_b128 v[208:211], v170 offset:5120
	ds_read_b128 v[212:215], v170 offset:6144
	ds_read_b128 v[216:219], v170 offset:7168
	global_load_lds_dwordx4 v[136:137], off
	v_lshl_add_u64 v[136:137], s[56:57], 0, v[156:157]
	s_add_i32 m0, s53, 0xe000
	s_nop 0
	global_load_lds_dwordx4 v[136:137], off
	s_waitcnt vmcnt(8)
	s_waitcnt lgkmcnt(0)
	s_barrier
	s_setprio 1
	s_waitcnt lgkmcnt(0)
	v_mfma_f32_16x16x32_bf16 v[142:145], v[124:127], v[188:191], v[142:145]
	v_mfma_f32_16x16x32_bf16 v[136:139], v[132:135], v[188:191], v[138:141]
	v_mfma_f32_16x16x32_bf16 v[118:121], v[124:127], v[196:199], v[118:121]
	v_mfma_f32_16x16x32_bf16 v[106:109], v[132:135], v[196:199], v[106:109]
	v_mfma_f32_16x16x32_bf16 v[102:105], v[124:127], v[204:207], v[102:105]
	v_mfma_f32_16x16x32_bf16 v[90:93], v[132:135], v[204:207], v[90:93]
	v_mfma_f32_16x16x32_bf16 v[86:89], v[124:127], v[212:215], v[86:89]
	v_mfma_f32_16x16x32_bf16 v[74:77], v[132:135], v[212:215], v[74:77]
	v_mfma_f32_16x16x32_bf16 v[142:145], v[128:131], v[192:195], v[142:145]
	v_mfma_f32_16x16x32_bf16 v[136:139], v[164:167], v[192:195], v[136:139]
	v_mfma_f32_16x16x32_bf16 v[118:121], v[128:131], v[200:203], v[118:121]
	v_mfma_f32_16x16x32_bf16 v[106:109], v[164:167], v[200:203], v[106:109]
	v_mfma_f32_16x16x32_bf16 v[102:105], v[128:131], v[208:211], v[102:105]
	v_mfma_f32_16x16x32_bf16 v[90:93], v[164:167], v[208:211], v[90:93]
	v_mfma_f32_16x16x32_bf16 v[86:89], v[128:131], v[216:219], v[86:89]
	v_mfma_f32_16x16x32_bf16 v[74:77], v[164:167], v[216:219], v[74:77]
	s_setprio 0
	s_setprio 1
	v_mfma_f32_16x16x32_bf16 v[114:117], v[172:175], v[188:191], v[114:117]
	v_mfma_f32_16x16x32_bf16 v[110:113], v[180:183], v[188:191], v[110:113]
	v_mfma_f32_16x16x32_bf16 v[98:101], v[172:175], v[196:199], v[98:101]
	v_mfma_f32_16x16x32_bf16 v[94:97], v[180:183], v[196:199], v[94:97]
	v_mfma_f32_16x16x32_bf16 v[82:85], v[172:175], v[204:207], v[82:85]
	v_mfma_f32_16x16x32_bf16 v[78:81], v[180:183], v[204:207], v[78:81]
	v_mfma_f32_16x16x32_bf16 v[70:73], v[172:175], v[212:215], v[70:73]
	v_mfma_f32_16x16x32_bf16 v[66:69], v[180:183], v[212:215], v[66:69]
	v_mfma_f32_16x16x32_bf16 v[114:117], v[176:179], v[192:195], v[114:117]
	v_mfma_f32_16x16x32_bf16 v[110:113], v[184:187], v[192:195], v[110:113]
	v_mfma_f32_16x16x32_bf16 v[98:101], v[176:179], v[200:203], v[98:101]
	v_mfma_f32_16x16x32_bf16 v[94:97], v[184:187], v[200:203], v[94:97]
	v_mfma_f32_16x16x32_bf16 v[82:85], v[176:179], v[208:211], v[82:85]
	v_mfma_f32_16x16x32_bf16 v[78:81], v[184:187], v[208:211], v[78:81]
	v_mfma_f32_16x16x32_bf16 v[70:73], v[176:179], v[216:219], v[70:73]
	v_mfma_f32_16x16x32_bf16 v[66:69], v[184:187], v[216:219], v[66:69]
	s_setprio 0
	s_barrier
	s_add_i32 s90, s82, s67
	v_lshl_add_u64 v[220:221], s[58:59], 0, v[150:151]
	s_mov_b32 m0, s90
	ds_read_b128 v[188:191], v170 offset:16384
	ds_read_b128 v[192:195], v170 offset:17408
	ds_read_b128 v[196:199], v170 offset:18432
	ds_read_b128 v[200:203], v170 offset:19456
	ds_read_b128 v[204:207], v170 offset:20480
	ds_read_b128 v[208:211], v170 offset:21504
	ds_read_b128 v[212:215], v170 offset:22528
	ds_read_b128 v[216:219], v170 offset:23552
	global_load_lds_dwordx4 v[220:221], off
	s_add_i32 m0, s90, 0x2000
	s_add_u32 s90, s58, 0x40000
	v_lshl_add_u64 v[222:223], s[58:59], 0, v[146:147]
	s_addc_u32 s91, s59, 0
	s_add_i32 s92, s83, s67
	global_load_lds_dwordx4 v[222:223], off
	v_lshl_add_u64 v[140:141], s[90:91], 0, v[150:151]
	s_mov_b32 m0, s92
	v_lshl_add_u64 v[224:225], s[60:61], 0, v[152:153]
	global_load_lds_dwordx4 v[140:141], off
	v_lshl_add_u64 v[140:141], s[90:91], 0, v[146:147]
	s_add_i32 m0, s92, 0x2000
	v_lshl_add_u64 v[226:227], s[60:61], 0, v[148:149]
	global_load_lds_dwordx4 v[140:141], off
	s_mov_b32 m0, s53
	s_nop 0
	global_load_lds_dwordx4 v[224:225], off
	s_mov_b32 m0, s70
	s_nop 0
	global_load_lds_dwordx4 v[226:227], off
	s_waitcnt vmcnt(8)
	s_waitcnt lgkmcnt(0)
	s_barrier
; #define PG8_STAGE_A(bufoff, kbase, h, gv) do { if constexpr (GATHER) { PG8_STAGE(bufoff, kbase, (gv)[h]); } else { PG8_STAGE(bufoff, (kbase) + (h) * hstep, voffA); } } while (0)
; #define PG8_WAIT_V(n) asm volatile("s_waitcnt vmcnt(" #n ")" ::: "memory")
; #define PG8_WAIT_L(n) asm volatile("s_waitcnt lgkmcnt(" #n ")" ::: "memory")
; #define PG8_BAR __builtin_amdgcn_s_barrier()
; #define PG8_SCHED __builtin_amdgcn_sched_barrier(0)
; template <class Epi, class Sched, bool ALIGN_EPI = false, bool SP2 = false, bool FP8 = false, bool GATHER = false>
; __device__ __forceinline__ void gemm_phase(PG8_LAS unsigned char* lds, const Gemm g, const Sched& S, const Epi& E) {
;     ...
;             PG8_WAIT_V(8); PG8_WAIT_L(0); PG8_BAR; PG8_MMA(1, 0, At, B0); PG8_MMA(1, 1, At, B1); PG8_BAR; PG8_SCHED;
;             PG8_LDB(B0, 1, 0); PG8_LDB(B1, 1, 1); PG8_SCHED; PG8_LDA(At, 1, 0); PG8_STAGE_A(PG8_SA(0, 1), a2, 1, gsel);
;             PG8_WAIT_V(8); PG8_WAIT_L(0); PG8_BAR; PG8_MMA(0, 0, At, B0); PG8_MMA(0, 1, At, B1); PG8_BAR; PG8_SCHED;
	s_setprio 1
	s_waitcnt lgkmcnt(0)
	v_mfma_f32_16x16x32_bf16 v[62:65], v[124:127], v[188:191], v[62:65]
	v_mfma_f32_16x16x32_bf16 v[58:61], v[132:135], v[188:191], v[58:61]
	v_mfma_f32_16x16x32_bf16 v[54:57], v[124:127], v[196:199], v[54:57]
	v_mfma_f32_16x16x32_bf16 v[42:45], v[132:135], v[196:199], v[42:45]
	v_mfma_f32_16x16x32_bf16 v[38:41], v[124:127], v[204:207], v[38:41]
	v_mfma_f32_16x16x32_bf16 v[26:29], v[132:135], v[204:207], v[26:29]
	v_mfma_f32_16x16x32_bf16 v[22:25], v[124:127], v[212:215], v[22:25]
	v_mfma_f32_16x16x32_bf16 v[10:13], v[132:135], v[212:215], v[10:13]
	v_mfma_f32_16x16x32_bf16 v[62:65], v[128:131], v[192:195], v[62:65]
	v_mfma_f32_16x16x32_bf16 v[58:61], v[164:167], v[192:195], v[58:61]
	v_mfma_f32_16x16x32_bf16 v[54:57], v[128:131], v[200:203], v[54:57]
	v_mfma_f32_16x16x32_bf16 v[42:45], v[164:167], v[200:203], v[42:45]
	v_mfma_f32_16x16x32_bf16 v[38:41], v[128:131], v[208:211], v[38:41]
	v_mfma_f32_16x16x32_bf16 v[26:29], v[164:167], v[208:211], v[26:29]
	v_mfma_f32_16x16x32_bf16 v[22:25], v[128:131], v[216:219], v[22:25]
	v_mfma_f32_16x16x32_bf16 v[10:13], v[164:167], v[216:219], v[10:13]
	s_setprio 0
	s_setprio 1
	v_mfma_f32_16x16x32_bf16 v[50:53], v[172:175], v[188:191], v[50:53]
	v_mfma_f32_16x16x32_bf16 v[46:49], v[180:183], v[188:191], v[46:49]
	v_mfma_f32_16x16x32_bf16 v[34:37], v[172:175], v[196:199], v[34:37]
	v_mfma_f32_16x16x32_bf16 v[30:33], v[180:183], v[196:199], v[30:33]
	v_mfma_f32_16x16x32_bf16 v[18:21], v[172:175], v[204:207], v[18:21]
	v_mfma_f32_16x16x32_bf16 v[14:17], v[180:183], v[204:207], v[14:17]
	v_mfma_f32_16x16x32_bf16 v[6:9], v[172:175], v[212:215], v[6:9]
	v_mfma_f32_16x16x32_bf16 v[2:5], v[180:183], v[212:215], v[2:5]
	v_mfma_f32_16x16x32_bf16 v[50:53], v[176:179], v[192:195], v[50:53]
	v_mfma_f32_16x16x32_bf16 v[46:49], v[184:187], v[192:195], v[46:49]
	v_mfma_f32_16x16x32_bf16 v[34:37], v[176:179], v[200:203], v[34:37]
	v_mfma_f32_16x16x32_bf16 v[30:33], v[184:187], v[200:203], v[30:33]
	v_mfma_f32_16x16x32_bf16 v[18:21], v[176:179], v[208:211], v[18:21]
	v_mfma_f32_16x16x32_bf16 v[14:17], v[184:187], v[208:211], v[14:17]
	v_mfma_f32_16x16x32_bf16 v[6:9], v[176:179], v[216:219], v[6:9]
	v_mfma_f32_16x16x32_bf16 v[2:5], v[184:187], v[216:219], v[2:5]
	s_setprio 0
	s_barrier
	s_add_i32 s90, 0, 0x18000
	v_add_u32_e32 v140, s90, v169
	s_add_i32 s91, 0, 0x1c000
	ds_read_b128 v[124:127], v140
	ds_read_b128 v[128:131], v140 offset:1024
	ds_read_b128 v[132:135], v140 offset:2048
	ds_read_b128 v[164:167], v140 offset:3072
	v_add_u32_e32 v140, s91, v169
	ds_read_b128 v[172:175], v140
	ds_read_b128 v[176:179], v140 offset:1024
	ds_read_b128 v[180:183], v140 offset:2048
	ds_read_b128 v[184:187], v140 offset:3072
	s_add_u32 s60, s60, 0x40000
	s_addc_u32 s61, s61, 0
	s_mov_b32 m0, s71
	v_lshl_add_u64 v[140:141], s[60:61], 0, v[152:153]
	ds_read_b128 v[188:191], v170 offset:32768
	ds_read_b128 v[192:195], v170 offset:33792
	ds_read_b128 v[196:199], v170 offset:34816
	ds_read_b128 v[200:203], v170 offset:35840
	ds_read_b128 v[204:207], v170 offset:36864
	ds_read_b128 v[208:211], v170 offset:37888
	ds_read_b128 v[212:215], v170 offset:38912
	ds_read_b128 v[216:219], v170 offset:39936
	global_load_lds_dwordx4 v[140:141], off
	v_lshl_add_u64 v[140:141], s[60:61], 0, v[148:149]
	s_mov_b32 m0, s72
	s_nop 0
	global_load_lds_dwordx4 v[140:141], off
	s_waitcnt vmcnt(8)
	s_waitcnt lgkmcnt(0)
	s_barrier
	s_setprio 1
	s_waitcnt lgkmcnt(0)
	v_mfma_f32_16x16x32_bf16 v[140:143], v[124:127], v[188:191], v[142:145]
	v_mfma_f32_16x16x32_bf16 v[136:139], v[132:135], v[188:191], v[136:139]
	v_mfma_f32_16x16x32_bf16 v[118:121], v[124:127], v[196:199], v[118:121]
	v_mfma_f32_16x16x32_bf16 v[106:109], v[132:135], v[196:199], v[106:109]
	v_mfma_f32_16x16x32_bf16 v[102:105], v[124:127], v[204:207], v[102:105]
	v_mfma_f32_16x16x32_bf16 v[90:93], v[132:135], v[204:207], v[90:93]
	v_mfma_f32_16x16x32_bf16 v[86:89], v[124:127], v[212:215], v[86:89]
	v_mfma_f32_16x16x32_bf16 v[74:77], v[132:135], v[212:215], v[74:77]
	v_mfma_f32_16x16x32_bf16 v[142:145], v[128:131], v[192:195], v[140:143]
	v_mfma_f32_16x16x32_bf16 v[138:141], v[164:167], v[192:195], v[136:139]
	v_mfma_f32_16x16x32_bf16 v[118:121], v[128:131], v[200:203], v[118:121]
	v_mfma_f32_16x16x32_bf16 v[106:109], v[164:167], v[200:203], v[106:109]
	v_mfma_f32_16x16x32_bf16 v[102:105], v[128:131], v[208:211], v[102:105]
	v_mfma_f32_16x16x32_bf16 v[90:93], v[164:167], v[208:211], v[90:93]
	v_mfma_f32_16x16x32_bf16 v[86:89], v[128:131], v[216:219], v[86:89]
	v_mfma_f32_16x16x32_bf16 v[74:77], v[164:167], v[216:219], v[74:77]
	s_setprio 0
	s_setprio 1
	v_mfma_f32_16x16x32_bf16 v[114:117], v[172:175], v[188:191], v[114:117]
	v_mfma_f32_16x16x32_bf16 v[110:113], v[180:183], v[188:191], v[110:113]
	v_mfma_f32_16x16x32_bf16 v[98:101], v[172:175], v[196:199], v[98:101]
	v_mfma_f32_16x16x32_bf16 v[94:97], v[180:183], v[196:199], v[94:97]
	v_mfma_f32_16x16x32_bf16 v[82:85], v[172:175], v[204:207], v[82:85]
	v_mfma_f32_16x16x32_bf16 v[78:81], v[180:183], v[204:207], v[78:81]
	v_mfma_f32_16x16x32_bf16 v[70:73], v[172:175], v[212:215], v[70:73]
	v_mfma_f32_16x16x32_bf16 v[66:69], v[180:183], v[212:215], v[66:69]
	v_mfma_f32_16x16x32_bf16 v[114:117], v[176:179], v[192:195], v[114:117]
	v_mfma_f32_16x16x32_bf16 v[110:113], v[184:187], v[192:195], v[110:113]
	v_mfma_f32_16x16x32_bf16 v[98:101], v[176:179], v[200:203], v[98:101]
	v_mfma_f32_16x16x32_bf16 v[94:97], v[184:187], v[200:203], v[94:97]
	v_mfma_f32_16x16x32_bf16 v[82:85], v[176:179], v[208:211], v[82:85]
	v_mfma_f32_16x16x32_bf16 v[78:81], v[184:187], v[208:211], v[78:81]
	v_mfma_f32_16x16x32_bf16 v[70:73], v[176:179], v[216:219], v[70:73]
	v_mfma_f32_16x16x32_bf16 v[66:69], v[184:187], v[216:219], v[66:69]
	s_setprio 0
	s_barrier
; #define PG8_STAGE(bufoff, gbase, voff) do { _Pragma("unroll") for (int _i = 0; _i < 2; ++_i) \
;         __builtin_amdgcn_global_load_lds((const unsigned*)((const char*)(gbase) + (voff)[_i]), (PG8_LAS unsigned*)(lds + (bufoff) + ldsw + _i * 8192), 16, 0, 0); } while (0)
; #define PG8_STAGE_A(bufoff, kbase, h, gv) do { if constexpr (GATHER) { PG8_STAGE(bufoff, kbase, (gv)[h]); } else { PG8_STAGE(bufoff, (kbase) + (h) * hstep, voffA); } } while (0)
; #define PG8_WAIT_V(n) asm volatile("s_waitcnt vmcnt(" #n ")" ::: "memory")
; #define PG8_WAIT_L(n) asm volatile("s_waitcnt lgkmcnt(" #n ")" ::: "memory")
; #define PG8_BAR __builtin_amdgcn_s_barrier()
; #define PG8_SCHED __builtin_amdgcn_sched_barrier(0)
; template <class Epi, class Sched, bool ALIGN_EPI = false, bool SP2 = false, bool FP8 = false, bool GATHER = false>
; __device__ __forceinline__ void gemm_phase(PG8_LAS unsigned char* lds, const Gemm g, const Sched& S, const Epi& E) {
;     ...
;             PG8_LDA(At, 1, 1); PG8_STAGE(PG8_SB(1, 0), b3, voffB); PG8_STAGE(PG8_SB(1, 1), b3 + hstep, voffB); PG8_STAGE_A(PG8_SA(1, 0), a3, 0, gsel);
;             PG8_WAIT_V(8); PG8_WAIT_L(0); PG8_BAR; PG8_MMA(1, 0, At, B0); PG8_MMA(1, 1, At, B1); PG8_BAR; PG8_SCHED;
;     __device__ __forceinline__ void pre(const pg8::Unit& u, int wid, int lane) const {
;         if (wid == 0) lds_dma16(gate + (size_t)(u.pm < 256 ? (u.pm >> 4) : 16) * (NMOD * DM) + u.pn * 256 + lane * 4, (unsigned)(uintptr_t)(lds + LDS_EPI)); }
	s_add_i32 s60, s90, s67
	v_lshl_add_u64 v[136:137], v[220:221], 0, s[18:19]
	s_mov_b32 m0, s60
	ds_read_b128 v[188:191], v170 offset:49152
	ds_read_b128 v[192:195], v170 offset:50176
	ds_read_b128 v[196:199], v170 offset:51200
	ds_read_b128 v[200:203], v170 offset:52224
	ds_read_b128 v[204:207], v170 offset:53248
	ds_read_b128 v[208:211], v170 offset:54272
	ds_read_b128 v[212:215], v170 offset:55296
	ds_read_b128 v[216:219], v170 offset:56320
	global_load_lds_dwordx4 v[136:137], off
	s_add_i32 m0, s60, 0x2000
	s_add_u32 s58, s58, 0x40080
	v_lshl_add_u64 v[136:137], v[222:223], 0, s[18:19]
	s_addc_u32 s59, s59, 0
	s_add_i32 s60, s91, s67
	global_load_lds_dwordx4 v[136:137], off
	v_lshl_add_u64 v[136:137], s[58:59], 0, v[150:151]
	s_mov_b32 m0, s60
	s_nop 0
	global_load_lds_dwordx4 v[136:137], off
	v_lshl_add_u64 v[136:137], s[58:59], 0, v[146:147]
	s_add_i32 m0, s60, 0x2000
	s_nop 0
	global_load_lds_dwordx4 v[136:137], off
	v_lshl_add_u64 v[136:137], v[224:225], 0, s[18:19]
	s_mov_b32 m0, s78
	s_nop 0
	global_load_lds_dwordx4 v[136:137], off
	v_lshl_add_u64 v[136:137], v[226:227], 0, s[18:19]
	s_mov_b32 m0, s79
	s_nop 0
	global_load_lds_dwordx4 v[136:137], off
	s_waitcnt vmcnt(8)
	s_waitcnt lgkmcnt(0)
	s_barrier
	s_setprio 1
	s_waitcnt lgkmcnt(0)
	v_mfma_f32_16x16x32_bf16 v[62:65], v[124:127], v[188:191], v[62:65]
	v_mfma_f32_16x16x32_bf16 v[58:61], v[132:135], v[188:191], v[58:61]
	v_mfma_f32_16x16x32_bf16 v[54:57], v[124:127], v[196:199], v[54:57]
	v_mfma_f32_16x16x32_bf16 v[42:45], v[132:135], v[196:199], v[42:45]
	v_mfma_f32_16x16x32_bf16 v[38:41], v[124:127], v[204:207], v[38:41]
	v_mfma_f32_16x16x32_bf16 v[26:29], v[132:135], v[204:207], v[26:29]
	v_mfma_f32_16x16x32_bf16 v[22:25], v[124:127], v[212:215], v[22:25]
	v_mfma_f32_16x16x32_bf16 v[10:13], v[132:135], v[212:215], v[10:13]
	v_mfma_f32_16x16x32_bf16 v[62:65], v[128:131], v[192:195], v[62:65]
	v_mfma_f32_16x16x32_bf16 v[58:61], v[164:167], v[192:195], v[58:61]
	v_mfma_f32_16x16x32_bf16 v[54:57], v[128:131], v[200:203], v[54:57]
	v_mfma_f32_16x16x32_bf16 v[42:45], v[164:167], v[200:203], v[42:45]
	v_mfma_f32_16x16x32_bf16 v[38:41], v[128:131], v[208:211], v[38:41]
	v_mfma_f32_16x16x32_bf16 v[26:29], v[164:167], v[208:211], v[26:29]
	v_mfma_f32_16x16x32_bf16 v[22:25], v[128:131], v[216:219], v[22:25]
	v_mfma_f32_16x16x32_bf16 v[10:13], v[164:167], v[216:219], v[10:13]
	s_setprio 0
	s_setprio 1
	v_mfma_f32_16x16x32_bf16 v[50:53], v[172:175], v[188:191], v[50:53]
	v_mfma_f32_16x16x32_bf16 v[46:49], v[180:183], v[188:191], v[46:49]
	v_mfma_f32_16x16x32_bf16 v[34:37], v[172:175], v[196:199], v[34:37]
	v_mfma_f32_16x16x32_bf16 v[30:33], v[180:183], v[196:199], v[30:33]
	v_mfma_f32_16x16x32_bf16 v[18:21], v[172:175], v[204:207], v[18:21]
	v_mfma_f32_16x16x32_bf16 v[14:17], v[180:183], v[204:207], v[14:17]
	v_mfma_f32_16x16x32_bf16 v[6:9], v[172:175], v[212:215], v[6:9]
	v_mfma_f32_16x16x32_bf16 v[2:5], v[180:183], v[212:215], v[2:5]
	v_mfma_f32_16x16x32_bf16 v[50:53], v[176:179], v[192:195], v[50:53]
	v_mfma_f32_16x16x32_bf16 v[46:49], v[184:187], v[192:195], v[46:49]
	v_mfma_f32_16x16x32_bf16 v[34:37], v[176:179], v[200:203], v[34:37]
	v_mfma_f32_16x16x32_bf16 v[30:33], v[184:187], v[200:203], v[30:33]
	v_mfma_f32_16x16x32_bf16 v[18:21], v[176:179], v[208:211], v[18:21]
	v_mfma_f32_16x16x32_bf16 v[14:17], v[184:187], v[208:211], v[14:17]
	v_mfma_f32_16x16x32_bf16 v[6:9], v[176:179], v[216:219], v[6:9]
	v_mfma_f32_16x16x32_bf16 v[2:5], v[184:187], v[216:219], v[2:5]
	s_setprio 0
	s_add_i32 s89, s89, 2
	s_add_u32 s56, s56, 0x100
	s_addc_u32 s57, s57, 0
	s_add_u32 s55, s55, 0x100
	s_addc_u32 s88, s88, 0
	s_cmp_gt_u32 s89, 13
	s_cbranch_scc1 .Lrot592_exit
	s_barrier
.LBB0_593:
	s_cmp_lg_u32 s89, 12
	s_cselect_b64 s[58:59], -1, 0
	s_or_b64 s[60:61], s[58:59], s[20:21]
	s_and_b64 vcc, exec, s[60:61]
	s_cbranch_vccnz .LBB0_592
	s_add_i32 s60, 0, 0x20000
	s_mov_b32 s61, m0
	s_mov_b32 m0, s60
	s_nop 0
	global_load_lds_dwordx4 v[122:123], off
	s_mov_b32 m0, s61
	s_branch .LBB0_592
.Lrot592_exit:
	s_barrier
.LBB0_595:
	s_and_b64 vcc, exec, s[22:23]
	s_cbranch_vccz .LBB0_597
	s_barrier

; #define PG8_STAGE(bufoff, gbase, voff) do { _Pragma("unroll") for (int _i = 0; _i < 2; ++_i) \
;         __builtin_amdgcn_global_load_lds((const unsigned*)((const char*)(gbase) + (voff)[_i]), (PG8_LAS unsigned*)(lds + (bufoff) + ldsw + _i * 8192), 16, 0, 0); } while (0)
; #define PG8_STAGE_A(bufoff, kbase, h, gv) do { if constexpr (GATHER) { PG8_STAGE(bufoff, kbase, (gv)[h]); } else { PG8_STAGE(bufoff, (kbase) + (h) * hstep, voffA); } } while (0)
; #define PG8_BAR __builtin_amdgcn_s_barrier()
; template <class Epi, class Sched, bool ALIGN_EPI = false, bool SP2 = false, bool FP8 = false, bool GATHER = false>
; __device__ __forceinline__ void gemm_phase(PG8_LAS unsigned char* lds, const Gemm g, const Sched& S, const Epi& E) {
;     ...
;         for (int t = 0; t < nt; t += 2) {
;             const bool last = (t == nt - 2);
;             const char* a1 = cA + (size_t)(t + 1) * kstep;
;             const char* a2 = last ? nA : cA + (size_t)(t + 2) * kstep; const char* b2 = last ? nB : cB + (size_t)(t + 2) * kstep;
;             const char* a3 = a2 + kstep; const char* b3 = b2 + kstep;
;             if (last && has_next) S.a_ready(nxt);
;             if (last) E.pre(cur, wid, lane);
;             if constexpr (GATHER) { if (t == nt - 4 && has_next) { _Pragma("unroll") for (int h_ = 0; h_ < 2; ++h_) _Pragma("unroll") for (int i_ = 0; i_ < 2; ++i_)
;                 asm volatile("global_load_dword %0, %1, off" : "+v"(graw[h_][i_]) : "v"(S.rowtok + (nxt.pm * BM + h_ * HALF + gR[i_])) : "memory"); } }
;             unsigned gsel[2][2];
;             if constexpr (GATHER) { _Pragma("unroll") for (int h_ = 0; h_ < 2; ++h_) _Pragma("unroll") for (int i_ = 0; i_ < 2; ++i_) { if (last && has_next) gnxt[h_][i_] = graw[h_][i_] * (unsigned)(K * 2) + gC[i_]; gsel[h_][i_] = (last && has_next) ? gnxt[h_][i_] : gcur[h_][i_]; } }
;             if constexpr (SP2) {
;             PG8_LDB(B0, 0, 0); PG8_LDB(B1, 0, 1); PG8_SCHED; PG8_LDA(At, 0, 0); PG8_STAGE_A(PG8_SA(1, 1), a1, 1, gcur);
;             PG8_WAIT_V(8); PG8_WAIT_L(0); PG8_BAR; PG8_MMA(0, 0, At, B0); PG8_MMA(0, 1, At, B1); PG8_BAR; PG8_SCHED;
;             PG8_LDA(At, 0, 1); PG8_STAGE(PG8_SB(0, 0), b2, voffB); PG8_STAGE(PG8_SB(0, 1), b2 + hstep, voffB); PG8_STAGE_A(PG8_SA(0, 0), a2, 0, gsel);
;             PG8_WAIT_V(8); PG8_WAIT_L(0); PG8_BAR; PG8_MMA(1, 0, At, B0); PG8_MMA(1, 1, At, B1); PG8_BAR; PG8_SCHED;
.Lpeel878_body:
	s_add_u32 s52, s8, s48
	s_addc_u32 s53, s9, s49
	s_add_u32 s54, s52, 0x19200100
	s_addc_u32 s55, s53, 0
	s_and_b64 s[52:53], s[56:57], exec
	s_cselect_b32 s55, s11, s55
	s_cselect_b32 s54, s10, s54
	s_add_u32 s86, s22, s48
	s_addc_u32 s87, s84, s49
	s_and_b64 s[52:53], s[56:57], exec
	s_cselect_b32 s53, s45, s87
	s_cselect_b32 s52, s44, s86
	v_lshl_add_u32 v2, v213, 10, v1
	s_and_b64 vcc, s[46:47], s[56:57]
	v_cndmask_b32_e32 v209, v209, v2, vcc
	v_cndmask_b32_e32 v170, v217, v2, vcc
	v_lshl_add_u32 v2, v214, 10, v204
	v_cndmask_b32_e32 v210, v210, v2, vcc
	v_cndmask_b32_e32 v200, v180, v2, vcc
	v_add_u32_e32 v2, s76, v206
	v_add_u32_e32 v14, s77, v206
	ds_read_b128 v[18:21], v2
	ds_read_b128 v[22:25], v2 offset:1024
	ds_read_b128 v[26:29], v2 offset:2048
	ds_read_b128 v[30:33], v2 offset:3072
	ds_read_b128 v[2:5], v14
	ds_read_b128 v[6:9], v14 offset:1024
	ds_read_b128 v[10:13], v14 offset:2048
	ds_read_b128 v[14:17], v14 offset:3072
	v_lshl_add_u32 v177, v215, 10, v1
	v_lshl_add_u32 v179, v216, 10, v204
	v_cndmask_b32_e32 v211, v211, v177, vcc
	v_cndmask_b32_e32 v212, v212, v179, vcc
	v_cndmask_b32_e32 v177, v178, v177, vcc
	v_cndmask_b32_e32 v179, v176, v179, vcc
	v_lshl_add_u64 v[196:197], v[194:195], 0, s[48:49]
	s_add_i32 m0, s63, 0xc000
	ds_read_b128 v[218:221], v207
	ds_read_b128 v[222:225], v207 offset:1024
	ds_read_b128 v[226:229], v207 offset:2048
	ds_read_b128 v[230:233], v207 offset:3072
	ds_read_b128 v[234:237], v207 offset:4096
	ds_read_b128 v[238:241], v207 offset:5120
	ds_read_b128 v[242:245], v207 offset:6144
	ds_read_b128 v[246:249], v207 offset:7168
	global_load_lds_dwordx4 v[196:197], off
	v_lshl_add_u64 v[196:197], v[192:193], 0, s[48:49]
	s_add_i32 m0, s63, 0xe000
	s_nop 0
	global_load_lds_dwordx4 v[196:197], off
	s_waitcnt vmcnt(8)
	s_waitcnt lgkmcnt(0)
	s_barrier
	s_setprio 1
	s_waitcnt lgkmcnt(0)
	v_mfma_f32_16x16x128_f8f6f4 v[158:161], v[18:25], v[218:225], 0
	v_mfma_f32_16x16x128_f8f6f4 v[150:153], v[26:33], v[218:225], 0
	v_mfma_f32_16x16x128_f8f6f4 v[142:145], v[18:25], v[226:233], 0
	v_mfma_f32_16x16x128_f8f6f4 v[134:137], v[26:33], v[226:233], 0
	v_mfma_f32_16x16x128_f8f6f4 v[126:129], v[18:25], v[234:241], 0
	v_mfma_f32_16x16x128_f8f6f4 v[118:121], v[26:33], v[234:241], 0
	v_mfma_f32_16x16x128_f8f6f4 v[110:113], v[18:25], v[242:249], 0
	v_mfma_f32_16x16x128_f8f6f4 v[102:105], v[26:33], v[242:249], 0
	s_setprio 0
	s_setprio 1
	v_mfma_f32_16x16x128_f8f6f4 v[154:157], v[2:9], v[218:225], 0
	v_mfma_f32_16x16x128_f8f6f4 v[146:149], v[10:17], v[218:225], 0
	v_mfma_f32_16x16x128_f8f6f4 v[138:141], v[2:9], v[226:233], 0
	v_mfma_f32_16x16x128_f8f6f4 v[130:133], v[10:17], v[226:233], 0
	v_mfma_f32_16x16x128_f8f6f4 v[122:125], v[2:9], v[234:241], 0
	v_mfma_f32_16x16x128_f8f6f4 v[114:117], v[10:17], v[234:241], 0
	v_mfma_f32_16x16x128_f8f6f4 v[106:109], v[2:9], v[242:249], 0
	v_mfma_f32_16x16x128_f8f6f4 v[98:101], v[10:17], v[242:249], 0
	s_setprio 0
	s_barrier
	s_add_i32 s56, s76, s60
	v_lshl_add_u64 v[196:197], s[52:53], 0, v[168:169]
	s_mov_b32 m0, s56
	ds_read_b128 v[218:221], v207 offset:16384
	ds_read_b128 v[222:225], v207 offset:17408
	ds_read_b128 v[226:229], v207 offset:18432
	ds_read_b128 v[230:233], v207 offset:19456
	ds_read_b128 v[234:237], v207 offset:20480
	ds_read_b128 v[238:241], v207 offset:21504
	ds_read_b128 v[242:245], v207 offset:22528
	ds_read_b128 v[246:249], v207 offset:23552
	global_load_lds_dwordx4 v[196:197], off
	s_add_i32 m0, s56, 0x2000
	s_add_u32 s56, s52, 0x20000
	v_lshl_add_u64 v[198:199], s[52:53], 0, v[166:167]
	s_addc_u32 s57, s53, 0
	s_add_i32 s86, s77, s60
	global_load_lds_dwordx4 v[198:199], off
	v_lshl_add_u64 v[202:203], s[56:57], 0, v[168:169]
	s_mov_b32 m0, s86
	v_mov_b32_e32 v201, v171
	global_load_lds_dwordx4 v[202:203], off
	v_lshl_add_u64 v[202:203], s[56:57], 0, v[166:167]
	s_add_i32 m0, s86, 0x2000
	s_nop 0
	global_load_lds_dwordx4 v[202:203], off
	s_mov_b32 m0, s63
	v_lshl_add_u64 v[202:203], s[54:55], 0, v[170:171]
	global_load_lds_dwordx4 v170, s[54:55]
	s_mov_b32 m0, s65
	s_nop 0
	global_load_lds_dwordx4 v200, s[54:55]
	s_waitcnt vmcnt(8)
	s_waitcnt lgkmcnt(0)
	v_lshl_add_u64 v[200:201], s[54:55], 0, v[200:201]
	s_barrier
	s_setprio 1
	s_waitcnt lgkmcnt(0)
	v_mfma_f32_16x16x128_f8f6f4 v[94:97], v[18:25], v[218:225], 0
	v_mfma_f32_16x16x128_f8f6f4 v[86:89], v[26:33], v[218:225], 0
	v_mfma_f32_16x16x128_f8f6f4 v[78:81], v[18:25], v[226:233], 0
	v_mfma_f32_16x16x128_f8f6f4 v[70:73], v[26:33], v[226:233], 0
	v_mfma_f32_16x16x128_f8f6f4 v[62:65], v[18:25], v[234:241], 0
	v_mfma_f32_16x16x128_f8f6f4 v[54:57], v[26:33], v[234:241], 0
	v_mfma_f32_16x16x128_f8f6f4 v[46:49], v[18:25], v[242:249], 0
	v_mfma_f32_16x16x128_f8f6f4 v[38:41], v[26:33], v[242:249], 0
	s_setprio 0
	s_setprio 1
	v_mfma_f32_16x16x128_f8f6f4 v[90:93], v[2:9], v[218:225], 0
	v_mfma_f32_16x16x128_f8f6f4 v[82:85], v[10:17], v[218:225], 0
	v_mfma_f32_16x16x128_f8f6f4 v[74:77], v[2:9], v[226:233], 0
	v_mfma_f32_16x16x128_f8f6f4 v[66:69], v[10:17], v[226:233], 0
	v_mfma_f32_16x16x128_f8f6f4 v[58:61], v[2:9], v[234:241], 0
	v_mfma_f32_16x16x128_f8f6f4 v[50:53], v[10:17], v[234:241], 0
	v_mfma_f32_16x16x128_f8f6f4 v[42:45], v[2:9], v[242:249], 0
	v_mfma_f32_16x16x128_f8f6f4 v[34:37], v[10:17], v[242:249], 0
	s_setprio 0
	s_barrier
; #define PG8_STAGE(bufoff, gbase, voff) do { _Pragma("unroll") for (int _i = 0; _i < 2; ++_i) \
;         __builtin_amdgcn_global_load_lds((const unsigned*)((const char*)(gbase) + (voff)[_i]), (PG8_LAS unsigned*)(lds + (bufoff) + ldsw + _i * 8192), 16, 0, 0); } while (0)
; #define PG8_STAGE_A(bufoff, kbase, h, gv) do { if constexpr (GATHER) { PG8_STAGE(bufoff, kbase, (gv)[h]); } else { PG8_STAGE(bufoff, (kbase) + (h) * hstep, voffA); } } while (0)
; #define PG8_WAIT_V(n) asm volatile("s_waitcnt vmcnt(" #n ")" ::: "memory")
; #define PG8_WAIT_L(n) asm volatile("s_waitcnt lgkmcnt(" #n ")" ::: "memory")
; #define PG8_BAR __builtin_amdgcn_s_barrier()
; #define PG8_SCHED __builtin_amdgcn_sched_barrier(0)
; template <class Epi, class Sched, bool ALIGN_EPI = false, bool SP2 = false, bool FP8 = false, bool GATHER = false>
; __device__ __forceinline__ void gemm_phase(PG8_LAS unsigned char* lds, const Gemm g, const Sched& S, const Epi& E) {
;     ...
;             PG8_LDB(B0, 1, 0); PG8_LDB(B1, 1, 1); PG8_SCHED; PG8_LDA(At, 1, 0); PG8_STAGE_A(PG8_SA(0, 1), a2, 1, gsel);
;             PG8_WAIT_V(8); PG8_WAIT_L(0); PG8_BAR; PG8_MMA(0, 0, At, B0); PG8_MMA(0, 1, At, B1); PG8_BAR; PG8_SCHED;
;             PG8_LDA(At, 1, 1); PG8_STAGE(PG8_SB(1, 0), b3, voffB); PG8_STAGE(PG8_SB(1, 1), b3 + hstep, voffB); PG8_STAGE_A(PG8_SA(1, 0), a3, 0, gsel);
;             PG8_WAIT_V(8); PG8_WAIT_L(0); PG8_BAR; PG8_MMA(1, 0, At, B0); PG8_MMA(1, 1, At, B1); PG8_BAR; PG8_SCHED;
	s_add_i32 s56, 0, 0x18000
	s_add_i32 s57, 0, 0x1c000
	v_add_u32_e32 v14, s56, v206
	v_add_u32_e32 v30, s57, v206
	ds_read_b128 v[2:5], v14
	ds_read_b128 v[6:9], v14 offset:1024
	ds_read_b128 v[10:13], v14 offset:2048
	ds_read_b128 v[14:17], v14 offset:3072
	ds_read_b128 v[18:21], v30
	ds_read_b128 v[22:25], v30 offset:1024
	ds_read_b128 v[26:29], v30 offset:2048
	ds_read_b128 v[30:33], v30 offset:3072
	s_mov_b32 m0, s66
	ds_read_b128 v[218:221], v207 offset:32768
	ds_read_b128 v[222:225], v207 offset:33792
	ds_read_b128 v[226:229], v207 offset:34816
	ds_read_b128 v[230:233], v207 offset:35840
	ds_read_b128 v[234:237], v207 offset:36864
	ds_read_b128 v[238:241], v207 offset:37888
	ds_read_b128 v[242:245], v207 offset:38912
	ds_read_b128 v[246:249], v207 offset:39936
	global_load_lds_dwordx4 v177, s[54:55]
	s_mov_b32 m0, s67
	s_nop 0
	global_load_lds_dwordx4 v179, s[54:55]
	s_waitcnt vmcnt(8)
	s_waitcnt lgkmcnt(0)
	s_barrier
	s_setprio 1
	s_waitcnt lgkmcnt(0)
	v_mfma_f32_16x16x128_f8f6f4 v[158:161], v[2:9], v[218:225], v[158:161]
	v_mfma_f32_16x16x128_f8f6f4 v[150:153], v[10:17], v[218:225], v[150:153]
	v_mfma_f32_16x16x128_f8f6f4 v[142:145], v[2:9], v[226:233], v[142:145]
	v_mfma_f32_16x16x128_f8f6f4 v[134:137], v[10:17], v[226:233], v[134:137]
	v_mfma_f32_16x16x128_f8f6f4 v[126:129], v[2:9], v[234:241], v[126:129]
	v_mfma_f32_16x16x128_f8f6f4 v[118:121], v[10:17], v[234:241], v[118:121]
	v_mfma_f32_16x16x128_f8f6f4 v[110:113], v[2:9], v[242:249], v[110:113]
	v_mfma_f32_16x16x128_f8f6f4 v[102:105], v[10:17], v[242:249], v[102:105]
	s_setprio 0
	s_setprio 1
	v_mfma_f32_16x16x128_f8f6f4 v[154:157], v[18:25], v[218:225], v[154:157]
	v_mfma_f32_16x16x128_f8f6f4 v[146:149], v[26:33], v[218:225], v[146:149]
	v_mfma_f32_16x16x128_f8f6f4 v[138:141], v[18:25], v[226:233], v[138:141]
	v_mfma_f32_16x16x128_f8f6f4 v[130:133], v[26:33], v[226:233], v[130:133]
	v_mfma_f32_16x16x128_f8f6f4 v[122:125], v[18:25], v[234:241], v[122:125]
	v_mfma_f32_16x16x128_f8f6f4 v[114:117], v[26:33], v[234:241], v[114:117]
	v_mfma_f32_16x16x128_f8f6f4 v[106:109], v[18:25], v[242:249], v[106:109]
	v_mfma_f32_16x16x128_f8f6f4 v[98:101], v[26:33], v[242:249], v[98:101]
	s_setprio 0
	s_barrier
	s_add_i32 s54, s56, s60
	v_lshl_add_u64 v[196:197], v[196:197], 0, s[18:19]
	s_mov_b32 m0, s54
	ds_read_b128 v[218:221], v207 offset:49152
	ds_read_b128 v[222:225], v207 offset:50176
	ds_read_b128 v[226:229], v207 offset:51200
	ds_read_b128 v[230:233], v207 offset:52224
	ds_read_b128 v[234:237], v207 offset:53248
	ds_read_b128 v[238:241], v207 offset:54272
	ds_read_b128 v[242:245], v207 offset:55296
	ds_read_b128 v[246:249], v207 offset:56320
	global_load_lds_dwordx4 v[196:197], off
	s_add_i32 m0, s54, 0x2000
	s_add_u32 s52, s52, 0x20080
	v_lshl_add_u64 v[196:197], v[198:199], 0, s[18:19]
	s_addc_u32 s53, s53, 0
	s_add_i32 s54, s57, s60
	global_load_lds_dwordx4 v[196:197], off
	v_lshl_add_u64 v[196:197], s[52:53], 0, v[168:169]
	s_mov_b32 m0, s54
	s_nop 0
	global_load_lds_dwordx4 v[196:197], off
	v_lshl_add_u64 v[196:197], s[52:53], 0, v[166:167]
	s_add_i32 m0, s54, 0x2000
	s_nop 0
	global_load_lds_dwordx4 v[196:197], off
	v_lshl_add_u64 v[196:197], v[202:203], 0, s[18:19]
	s_mov_b32 m0, s70
	s_nop 0
	global_load_lds_dwordx4 v[196:197], off
	v_lshl_add_u64 v[196:197], v[200:201], 0, s[18:19]
	s_mov_b32 m0, s71
	s_nop 0
	global_load_lds_dwordx4 v[196:197], off
	s_waitcnt vmcnt(8)
	s_waitcnt lgkmcnt(0)
	s_barrier
	s_setprio 1
	s_waitcnt lgkmcnt(0)
	v_mfma_f32_16x16x128_f8f6f4 v[94:97], v[2:9], v[218:225], v[94:97]
	v_mfma_f32_16x16x128_f8f6f4 v[86:89], v[10:17], v[218:225], v[86:89]
	v_mfma_f32_16x16x128_f8f6f4 v[78:81], v[2:9], v[226:233], v[78:81]
	v_mfma_f32_16x16x128_f8f6f4 v[70:73], v[10:17], v[226:233], v[70:73]
	v_mfma_f32_16x16x128_f8f6f4 v[62:65], v[2:9], v[234:241], v[62:65]
	v_mfma_f32_16x16x128_f8f6f4 v[54:57], v[10:17], v[234:241], v[54:57]
	v_mfma_f32_16x16x128_f8f6f4 v[46:49], v[2:9], v[242:249], v[46:49]
	v_mfma_f32_16x16x128_f8f6f4 v[38:41], v[10:17], v[242:249], v[38:41]
	s_setprio 0
	s_setprio 1
	v_mfma_f32_16x16x128_f8f6f4 v[90:93], v[18:25], v[218:225], v[90:93]
	v_mfma_f32_16x16x128_f8f6f4 v[82:85], v[26:33], v[218:225], v[82:85]
	v_mfma_f32_16x16x128_f8f6f4 v[74:77], v[18:25], v[226:233], v[74:77]
	v_mfma_f32_16x16x128_f8f6f4 v[66:69], v[26:33], v[226:233], v[66:69]
	v_mfma_f32_16x16x128_f8f6f4 v[58:61], v[18:25], v[234:241], v[58:61]
	v_mfma_f32_16x16x128_f8f6f4 v[50:53], v[26:33], v[234:241], v[50:53]
	v_mfma_f32_16x16x128_f8f6f4 v[42:45], v[18:25], v[242:249], v[42:45]
	v_mfma_f32_16x16x128_f8f6f4 v[34:37], v[26:33], v[242:249], v[34:37]
	s_setprio 0
	s_add_i32 s85, s85, 2
	s_add_u32 s48, s48, 0x100
	s_addc_u32 s49, s49, 0
	s_cmp_gt_u32 s85, 5
	s_cbranch_scc1 .Lrot878_exit
	s_barrier
	s_branch .LBB0_879
; #define PG8_STAGE(bufoff, gbase, voff) do { _Pragma("unroll") for (int _i = 0; _i < 2; ++_i) \
;         __builtin_amdgcn_global_load_lds((const unsigned*)((const char*)(gbase) + (voff)[_i]), (PG8_LAS unsigned*)(lds + (bufoff) + ldsw + _i * 8192), 16, 0, 0); } while (0)
; #define PG8_STAGE_A(bufoff, kbase, h, gv) do { if constexpr (GATHER) { PG8_STAGE(bufoff, kbase, (gv)[h]); } else { PG8_STAGE(bufoff, (kbase) + (h) * hstep, voffA); } } while (0)
; #define PG8_BAR __builtin_amdgcn_s_barrier()
; template <class Epi, class Sched, bool ALIGN_EPI = false, bool SP2 = false, bool FP8 = false, bool GATHER = false>
; __device__ __forceinline__ void gemm_phase(PG8_LAS unsigned char* lds, const Gemm g, const Sched& S, const Epi& E) {
;     ...
;         for (int t = 0; t < nt; t += 2) {
;             const bool last = (t == nt - 2);
;             const char* a1 = cA + (size_t)(t + 1) * kstep;
;             const char* a2 = last ? nA : cA + (size_t)(t + 2) * kstep; const char* b2 = last ? nB : cB + (size_t)(t + 2) * kstep;
;             const char* a3 = a2 + kstep; const char* b3 = b2 + kstep;
;             if (last && has_next) S.a_ready(nxt);
;             if (last) E.pre(cur, wid, lane);
;             if constexpr (GATHER) { if (t == nt - 4 && has_next) { _Pragma("unroll") for (int h_ = 0; h_ < 2; ++h_) _Pragma("unroll") for (int i_ = 0; i_ < 2; ++i_)
;                 asm volatile("global_load_dword %0, %1, off" : "+v"(graw[h_][i_]) : "v"(S.rowtok + (nxt.pm * BM + h_ * HALF + gR[i_])) : "memory"); } }
;             unsigned gsel[2][2];
;             if constexpr (GATHER) { _Pragma("unroll") for (int h_ = 0; h_ < 2; ++h_) _Pragma("unroll") for (int i_ = 0; i_ < 2; ++i_) { if (last && has_next) gnxt[h_][i_] = graw[h_][i_] * (unsigned)(K * 2) + gC[i_]; gsel[h_][i_] = (last && has_next) ? gnxt[h_][i_] : gcur[h_][i_]; } }
;             if constexpr (SP2) {
;             PG8_LDB(B0, 0, 0); PG8_LDB(B1, 0, 1); PG8_SCHED; PG8_LDA(At, 0, 0); PG8_STAGE_A(PG8_SA(1, 1), a1, 1, gcur);
;             PG8_WAIT_V(8); PG8_WAIT_L(0); PG8_BAR; PG8_MMA(0, 0, At, B0); PG8_MMA(0, 1, At, B1); PG8_BAR; PG8_SCHED;
;             PG8_LDA(At, 0, 1); PG8_STAGE(PG8_SB(0, 0), b2, voffB); PG8_STAGE(PG8_SB(0, 1), b2 + hstep, voffB); PG8_STAGE_A(PG8_SA(0, 0), a2, 0, gsel);
;             PG8_WAIT_V(8); PG8_WAIT_L(0); PG8_BAR; PG8_MMA(1, 0, At, B0); PG8_MMA(1, 1, At, B1); PG8_BAR; PG8_SCHED;
.LBB0_878:
	s_add_u32 s52, s8, s48
	s_addc_u32 s53, s9, s49
	s_add_u32 s54, s52, 0x19200100
	s_addc_u32 s55, s53, 0
	s_and_b64 s[52:53], s[56:57], exec
	s_cselect_b32 s55, s11, s55
	s_cselect_b32 s54, s10, s54
	s_add_u32 s86, s22, s48
	s_addc_u32 s87, s84, s49
	s_and_b64 s[52:53], s[56:57], exec
	s_cselect_b32 s53, s45, s87
	s_cselect_b32 s52, s44, s86
	v_lshl_add_u32 v2, v213, 10, v1
	s_and_b64 vcc, s[46:47], s[56:57]
	v_cndmask_b32_e32 v209, v209, v2, vcc
	v_cndmask_b32_e32 v170, v217, v2, vcc
	v_lshl_add_u32 v2, v214, 10, v204
	v_cndmask_b32_e32 v210, v210, v2, vcc
	v_cndmask_b32_e32 v200, v180, v2, vcc
	v_add_u32_e32 v2, s76, v206
	v_add_u32_e32 v14, s77, v206
	ds_read_b128 v[18:21], v2
	ds_read_b128 v[22:25], v2 offset:1024
	ds_read_b128 v[26:29], v2 offset:2048
	ds_read_b128 v[30:33], v2 offset:3072
	ds_read_b128 v[2:5], v14
	ds_read_b128 v[6:9], v14 offset:1024
	ds_read_b128 v[10:13], v14 offset:2048
	ds_read_b128 v[14:17], v14 offset:3072
	v_lshl_add_u32 v177, v215, 10, v1
	v_lshl_add_u32 v179, v216, 10, v204
	v_cndmask_b32_e32 v211, v211, v177, vcc
	v_cndmask_b32_e32 v212, v212, v179, vcc
	v_cndmask_b32_e32 v177, v178, v177, vcc
	v_cndmask_b32_e32 v179, v176, v179, vcc
	v_lshl_add_u64 v[196:197], v[194:195], 0, s[48:49]
	s_add_i32 m0, s63, 0xc000
	ds_read_b128 v[218:221], v207
	ds_read_b128 v[222:225], v207 offset:1024
	ds_read_b128 v[226:229], v207 offset:2048
	ds_read_b128 v[230:233], v207 offset:3072
	ds_read_b128 v[234:237], v207 offset:4096
	ds_read_b128 v[238:241], v207 offset:5120
	ds_read_b128 v[242:245], v207 offset:6144
	ds_read_b128 v[246:249], v207 offset:7168
	global_load_lds_dwordx4 v[196:197], off
	v_lshl_add_u64 v[196:197], v[192:193], 0, s[48:49]
	s_add_i32 m0, s63, 0xe000
	s_nop 0
	global_load_lds_dwordx4 v[196:197], off
	s_waitcnt vmcnt(8)
	s_waitcnt lgkmcnt(0)
	s_barrier
	s_setprio 1
	s_waitcnt lgkmcnt(0)
	v_mfma_f32_16x16x128_f8f6f4 v[158:161], v[18:25], v[218:225], v[158:161]
	v_mfma_f32_16x16x128_f8f6f4 v[150:153], v[26:33], v[218:225], v[150:153]
	v_mfma_f32_16x16x128_f8f6f4 v[142:145], v[18:25], v[226:233], v[142:145]
	v_mfma_f32_16x16x128_f8f6f4 v[134:137], v[26:33], v[226:233], v[134:137]
	v_mfma_f32_16x16x128_f8f6f4 v[126:129], v[18:25], v[234:241], v[126:129]
	v_mfma_f32_16x16x128_f8f6f4 v[118:121], v[26:33], v[234:241], v[118:121]
	v_mfma_f32_16x16x128_f8f6f4 v[110:113], v[18:25], v[242:249], v[110:113]
	v_mfma_f32_16x16x128_f8f6f4 v[102:105], v[26:33], v[242:249], v[102:105]
	s_setprio 0
	s_setprio 1
	v_mfma_f32_16x16x128_f8f6f4 v[154:157], v[2:9], v[218:225], v[154:157]
	v_mfma_f32_16x16x128_f8f6f4 v[146:149], v[10:17], v[218:225], v[146:149]
	v_mfma_f32_16x16x128_f8f6f4 v[138:141], v[2:9], v[226:233], v[138:141]
	v_mfma_f32_16x16x128_f8f6f4 v[130:133], v[10:17], v[226:233], v[130:133]
	v_mfma_f32_16x16x128_f8f6f4 v[122:125], v[2:9], v[234:241], v[122:125]
	v_mfma_f32_16x16x128_f8f6f4 v[114:117], v[10:17], v[234:241], v[114:117]
	v_mfma_f32_16x16x128_f8f6f4 v[106:109], v[2:9], v[242:249], v[106:109]
	v_mfma_f32_16x16x128_f8f6f4 v[98:101], v[10:17], v[242:249], v[98:101]
	s_setprio 0
	s_barrier
	s_add_i32 s56, s76, s60
	v_lshl_add_u64 v[196:197], s[52:53], 0, v[168:169]
	s_mov_b32 m0, s56
	ds_read_b128 v[218:221], v207 offset:16384
	ds_read_b128 v[222:225], v207 offset:17408
	ds_read_b128 v[226:229], v207 offset:18432
	ds_read_b128 v[230:233], v207 offset:19456
	ds_read_b128 v[234:237], v207 offset:20480
	ds_read_b128 v[238:241], v207 offset:21504
	ds_read_b128 v[242:245], v207 offset:22528
	ds_read_b128 v[246:249], v207 offset:23552
	global_load_lds_dwordx4 v[196:197], off
	s_add_i32 m0, s56, 0x2000
	s_add_u32 s56, s52, 0x20000
	v_lshl_add_u64 v[198:199], s[52:53], 0, v[166:167]
	s_addc_u32 s57, s53, 0
	s_add_i32 s86, s77, s60
	global_load_lds_dwordx4 v[198:199], off
	v_lshl_add_u64 v[202:203], s[56:57], 0, v[168:169]
	s_mov_b32 m0, s86
	v_mov_b32_e32 v201, v171
	global_load_lds_dwordx4 v[202:203], off
	v_lshl_add_u64 v[202:203], s[56:57], 0, v[166:167]
	s_add_i32 m0, s86, 0x2000
	s_nop 0
	global_load_lds_dwordx4 v[202:203], off
	s_mov_b32 m0, s63
	v_lshl_add_u64 v[202:203], s[54:55], 0, v[170:171]
	global_load_lds_dwordx4 v170, s[54:55]
	s_mov_b32 m0, s65
	s_nop 0
	global_load_lds_dwordx4 v200, s[54:55]
	s_waitcnt vmcnt(8)
	s_waitcnt lgkmcnt(0)
	v_lshl_add_u64 v[200:201], s[54:55], 0, v[200:201]
	s_barrier
	s_setprio 1
	s_waitcnt lgkmcnt(0)
	v_mfma_f32_16x16x128_f8f6f4 v[94:97], v[18:25], v[218:225], v[94:97]
	v_mfma_f32_16x16x128_f8f6f4 v[86:89], v[26:33], v[218:225], v[86:89]
	v_mfma_f32_16x16x128_f8f6f4 v[78:81], v[18:25], v[226:233], v[78:81]
	v_mfma_f32_16x16x128_f8f6f4 v[70:73], v[26:33], v[226:233], v[70:73]
	v_mfma_f32_16x16x128_f8f6f4 v[62:65], v[18:25], v[234:241], v[62:65]
	v_mfma_f32_16x16x128_f8f6f4 v[54:57], v[26:33], v[234:241], v[54:57]
	v_mfma_f32_16x16x128_f8f6f4 v[46:49], v[18:25], v[242:249], v[46:49]
	v_mfma_f32_16x16x128_f8f6f4 v[38:41], v[26:33], v[242:249], v[38:41]
	s_setprio 0
	s_setprio 1
	v_mfma_f32_16x16x128_f8f6f4 v[90:93], v[2:9], v[218:225], v[90:93]
	v_mfma_f32_16x16x128_f8f6f4 v[82:85], v[10:17], v[218:225], v[82:85]
	v_mfma_f32_16x16x128_f8f6f4 v[74:77], v[2:9], v[226:233], v[74:77]
	v_mfma_f32_16x16x128_f8f6f4 v[66:69], v[10:17], v[226:233], v[66:69]
	v_mfma_f32_16x16x128_f8f6f4 v[58:61], v[2:9], v[234:241], v[58:61]
	v_mfma_f32_16x16x128_f8f6f4 v[50:53], v[10:17], v[234:241], v[50:53]
	v_mfma_f32_16x16x128_f8f6f4 v[42:45], v[2:9], v[242:249], v[42:45]
	v_mfma_f32_16x16x128_f8f6f4 v[34:37], v[10:17], v[242:249], v[34:37]
	s_setprio 0
	s_barrier
; #define PG8_STAGE(bufoff, gbase, voff) do { _Pragma("unroll") for (int _i = 0; _i < 2; ++_i) \
;         __builtin_amdgcn_global_load_lds((const unsigned*)((const char*)(gbase) + (voff)[_i]), (PG8_LAS unsigned*)(lds + (bufoff) + ldsw + _i * 8192), 16, 0, 0); } while (0)
; #define PG8_STAGE_A(bufoff, kbase, h, gv) do { if constexpr (GATHER) { PG8_STAGE(bufoff, kbase, (gv)[h]); } else { PG8_STAGE(bufoff, (kbase) + (h) * hstep, voffA); } } while (0)
; #define PG8_WAIT_V(n) asm volatile("s_waitcnt vmcnt(" #n ")" ::: "memory")
; #define PG8_WAIT_L(n) asm volatile("s_waitcnt lgkmcnt(" #n ")" ::: "memory")
; #define PG8_BAR __builtin_amdgcn_s_barrier()
; #define PG8_SCHED __builtin_amdgcn_sched_barrier(0)
; template <class Epi, class Sched, bool ALIGN_EPI = false, bool SP2 = false, bool FP8 = false, bool GATHER = false>
; __device__ __forceinline__ void gemm_phase(PG8_LAS unsigned char* lds, const Gemm g, const Sched& S, const Epi& E) {
;     ...
;             PG8_LDB(B0, 1, 0); PG8_LDB(B1, 1, 1); PG8_SCHED; PG8_LDA(At, 1, 0); PG8_STAGE_A(PG8_SA(0, 1), a2, 1, gsel);
;             PG8_WAIT_V(8); PG8_WAIT_L(0); PG8_BAR; PG8_MMA(0, 0, At, B0); PG8_MMA(0, 1, At, B1); PG8_BAR; PG8_SCHED;
;             PG8_LDA(At, 1, 1); PG8_STAGE(PG8_SB(1, 0), b3, voffB); PG8_STAGE(PG8_SB(1, 1), b3 + hstep, voffB); PG8_STAGE_A(PG8_SA(1, 0), a3, 0, gsel);
;             PG8_WAIT_V(8); PG8_WAIT_L(0); PG8_BAR; PG8_MMA(1, 0, At, B0); PG8_MMA(1, 1, At, B1); PG8_BAR; PG8_SCHED;
	s_add_i32 s56, 0, 0x18000
	s_add_i32 s57, 0, 0x1c000
	v_add_u32_e32 v14, s56, v206
	v_add_u32_e32 v30, s57, v206
	ds_read_b128 v[2:5], v14
	ds_read_b128 v[6:9], v14 offset:1024
	ds_read_b128 v[10:13], v14 offset:2048
	ds_read_b128 v[14:17], v14 offset:3072
	ds_read_b128 v[18:21], v30
	ds_read_b128 v[22:25], v30 offset:1024
	ds_read_b128 v[26:29], v30 offset:2048
	ds_read_b128 v[30:33], v30 offset:3072
	s_mov_b32 m0, s66
	ds_read_b128 v[218:221], v207 offset:32768
	ds_read_b128 v[222:225], v207 offset:33792
	ds_read_b128 v[226:229], v207 offset:34816
	ds_read_b128 v[230:233], v207 offset:35840
	ds_read_b128 v[234:237], v207 offset:36864
	ds_read_b128 v[238:241], v207 offset:37888
	ds_read_b128 v[242:245], v207 offset:38912
	ds_read_b128 v[246:249], v207 offset:39936
	global_load_lds_dwordx4 v177, s[54:55]
	s_mov_b32 m0, s67
	s_nop 0
	global_load_lds_dwordx4 v179, s[54:55]
	s_waitcnt vmcnt(8)
	s_waitcnt lgkmcnt(0)
	s_barrier
	s_setprio 1
	s_waitcnt lgkmcnt(0)
	v_mfma_f32_16x16x128_f8f6f4 v[158:161], v[2:9], v[218:225], v[158:161]
	v_mfma_f32_16x16x128_f8f6f4 v[150:153], v[10:17], v[218:225], v[150:153]
	v_mfma_f32_16x16x128_f8f6f4 v[142:145], v[2:9], v[226:233], v[142:145]
	v_mfma_f32_16x16x128_f8f6f4 v[134:137], v[10:17], v[226:233], v[134:137]
	v_mfma_f32_16x16x128_f8f6f4 v[126:129], v[2:9], v[234:241], v[126:129]
	v_mfma_f32_16x16x128_f8f6f4 v[118:121], v[10:17], v[234:241], v[118:121]
	v_mfma_f32_16x16x128_f8f6f4 v[110:113], v[2:9], v[242:249], v[110:113]
	v_mfma_f32_16x16x128_f8f6f4 v[102:105], v[10:17], v[242:249], v[102:105]
	s_setprio 0
	s_setprio 1
	v_mfma_f32_16x16x128_f8f6f4 v[154:157], v[18:25], v[218:225], v[154:157]
	v_mfma_f32_16x16x128_f8f6f4 v[146:149], v[26:33], v[218:225], v[146:149]
	v_mfma_f32_16x16x128_f8f6f4 v[138:141], v[18:25], v[226:233], v[138:141]
	v_mfma_f32_16x16x128_f8f6f4 v[130:133], v[26:33], v[226:233], v[130:133]
	v_mfma_f32_16x16x128_f8f6f4 v[122:125], v[18:25], v[234:241], v[122:125]
	v_mfma_f32_16x16x128_f8f6f4 v[114:117], v[26:33], v[234:241], v[114:117]
	v_mfma_f32_16x16x128_f8f6f4 v[106:109], v[18:25], v[242:249], v[106:109]
	v_mfma_f32_16x16x128_f8f6f4 v[98:101], v[26:33], v[242:249], v[98:101]
	s_setprio 0
	s_barrier
	s_add_i32 s54, s56, s60
	v_lshl_add_u64 v[196:197], v[196:197], 0, s[18:19]
	s_mov_b32 m0, s54
	ds_read_b128 v[218:221], v207 offset:49152
	ds_read_b128 v[222:225], v207 offset:50176
	ds_read_b128 v[226:229], v207 offset:51200
	ds_read_b128 v[230:233], v207 offset:52224
	ds_read_b128 v[234:237], v207 offset:53248
	ds_read_b128 v[238:241], v207 offset:54272
	ds_read_b128 v[242:245], v207 offset:55296
	ds_read_b128 v[246:249], v207 offset:56320
	global_load_lds_dwordx4 v[196:197], off
	s_add_i32 m0, s54, 0x2000
	s_add_u32 s52, s52, 0x20080
	v_lshl_add_u64 v[196:197], v[198:199], 0, s[18:19]
	s_addc_u32 s53, s53, 0
	s_add_i32 s54, s57, s60
	global_load_lds_dwordx4 v[196:197], off
	v_lshl_add_u64 v[196:197], s[52:53], 0, v[168:169]
	s_mov_b32 m0, s54
	s_nop 0
	global_load_lds_dwordx4 v[196:197], off
	v_lshl_add_u64 v[196:197], s[52:53], 0, v[166:167]
	s_add_i32 m0, s54, 0x2000
	s_nop 0
	global_load_lds_dwordx4 v[196:197], off
	v_lshl_add_u64 v[196:197], v[202:203], 0, s[18:19]
	s_mov_b32 m0, s70
	s_nop 0
	global_load_lds_dwordx4 v[196:197], off
	v_lshl_add_u64 v[196:197], v[200:201], 0, s[18:19]
	s_mov_b32 m0, s71
	s_nop 0
	global_load_lds_dwordx4 v[196:197], off
	s_waitcnt vmcnt(8)
	s_waitcnt lgkmcnt(0)
	s_barrier
	s_setprio 1
	s_waitcnt lgkmcnt(0)
	v_mfma_f32_16x16x128_f8f6f4 v[94:97], v[2:9], v[218:225], v[94:97]
	v_mfma_f32_16x16x128_f8f6f4 v[86:89], v[10:17], v[218:225], v[86:89]
	v_mfma_f32_16x16x128_f8f6f4 v[78:81], v[2:9], v[226:233], v[78:81]
	v_mfma_f32_16x16x128_f8f6f4 v[70:73], v[10:17], v[226:233], v[70:73]
	v_mfma_f32_16x16x128_f8f6f4 v[62:65], v[2:9], v[234:241], v[62:65]
	v_mfma_f32_16x16x128_f8f6f4 v[54:57], v[10:17], v[234:241], v[54:57]
	v_mfma_f32_16x16x128_f8f6f4 v[46:49], v[2:9], v[242:249], v[46:49]
	v_mfma_f32_16x16x128_f8f6f4 v[38:41], v[10:17], v[242:249], v[38:41]
	s_setprio 0
	s_setprio 1
	v_mfma_f32_16x16x128_f8f6f4 v[90:93], v[18:25], v[218:225], v[90:93]
	v_mfma_f32_16x16x128_f8f6f4 v[82:85], v[26:33], v[218:225], v[82:85]
	v_mfma_f32_16x16x128_f8f6f4 v[74:77], v[18:25], v[226:233], v[74:77]
	v_mfma_f32_16x16x128_f8f6f4 v[66:69], v[26:33], v[226:233], v[66:69]
	v_mfma_f32_16x16x128_f8f6f4 v[58:61], v[18:25], v[234:241], v[58:61]
	v_mfma_f32_16x16x128_f8f6f4 v[50:53], v[26:33], v[234:241], v[50:53]
	v_mfma_f32_16x16x128_f8f6f4 v[42:45], v[18:25], v[242:249], v[42:45]
	v_mfma_f32_16x16x128_f8f6f4 v[34:37], v[26:33], v[242:249], v[34:37]
	s_setprio 0
	s_add_i32 s85, s85, 2
	s_add_u32 s48, s48, 0x100
	s_addc_u32 s49, s49, 0
	s_cmp_gt_u32 s85, 5
	s_cbranch_scc1 .Lrot878_exit
	s_barrier

; #define PG8_BAR __builtin_amdgcn_s_barrier()
; template <class Epi, class Sched, bool ALIGN_EPI = false, bool SP2 = false, bool FP8 = false, bool GATHER = false>
; __device__ __forceinline__ void gemm_phase(PG8_LAS unsigned char* lds, const Gemm g, const Sched& S, const Epi& E) {
;     ...
;             if constexpr (GATHER) { if (t == nt - 4 && has_next) { _Pragma("unroll") for (int h_ = 0; h_ < 2; ++h_) _Pragma("unroll") for (int i_ = 0; i_ < 2; ++i_)
;                 asm volatile("global_load_dword %0, %1, off" : "+v"(graw[h_][i_]) : "v"(S.rowtok + (nxt.pm * BM + h_ * HALF + gR[i_])) : "memory"); } }
;     ...
;         if constexpr (FP8) asm volatile("s_nop 15\n\ts_nop 15" ::: "memory");
;         if constexpr (ALIGN_EPI) { if (wr == 0) PG8_BAR; }
.LBB0_881:
	s_cmpk_lg_i32 s48, 0x200
	s_cselect_b64 s[52:53], -1, 0
	s_or_b64 s[52:53], s[50:51], s[52:53]
	s_and_b64 vcc, exec, s[52:53]
	s_cbranch_vccnz .LBB0_878
	global_load_dword v213, v[190:191], off
	global_load_dword v214, v[188:189], off
	global_load_dword v215, v[186:187], off
	global_load_dword v216, v[184:185], off
	s_branch .LBB0_878
.Lrot878_exit:
	s_barrier
.LBB0_883:
	s_nop 15
	s_nop 15
	s_and_b64 vcc, exec, s[26:27]
	s_cbranch_vccz .LBB0_885
	s_barrier

; #define PG8_STAGE(bufoff, gbase, voff) do { _Pragma("unroll") for (int _i = 0; _i < 2; ++_i) \
;         __builtin_amdgcn_global_load_lds((const unsigned*)((const char*)(gbase) + (voff)[_i]), (PG8_LAS unsigned*)(lds + (bufoff) + ldsw + _i * 8192), 16, 0, 0); } while (0)
; template <class Epi, class Sched, bool ALIGN_EPI = false, bool SP2 = false, bool FP8 = false, bool GATHER = false>
; __device__ __forceinline__ void gemm_phase(PG8_LAS unsigned char* lds, const Gemm g, const Sched& S, const Epi& E) {
;     ...
;         for (int t = 0; t < nt; t += 2) {
;             const bool last = (t == nt - 2);
;             const char* a1 = cA + (size_t)(t + 1) * kstep;
;             const char* a2 = last ? nA : cA + (size_t)(t + 2) * kstep; const char* b2 = last ? nB : cB + (size_t)(t + 2) * kstep;
;             const char* a3 = a2 + kstep; const char* b3 = b2 + kstep;
;             if (last && has_next) S.a_ready(nxt);
;             if (last) E.pre(cur, wid, lane);
;             if constexpr (GATHER) { if (t == nt - 4 && has_next) { _Pragma("unroll") for (int h_ = 0; h_ < 2; ++h_) _Pragma("unroll") for (int i_ = 0; i_ < 2; ++i_)
;                 asm volatile("global_load_dword %0, %1, off" : "+v"(graw[h_][i_]) : "v"(S.rowtok + (nxt.pm * BM + h_ * HALF + gR[i_])) : "memory"); } }
;             unsigned gsel[2][2];
;             if constexpr (GATHER) { _Pragma("unroll") for (int h_ = 0; h_ < 2; ++h_) _Pragma("unroll") for (int i_ = 0; i_ < 2; ++i_) { if (last && has_next) gnxt[h_][i_] = graw[h_][i_] * (unsigned)(K * 2) + gC[i_]; gsel[h_][i_] = (last && has_next) ? gnxt[h_][i_] : gcur[h_][i_]; } }
;             if constexpr (SP2) {
;             PG8_LDB(B0, 0, 0); PG8_LDB(B1, 0, 1); PG8_SCHED; PG8_LDA(At, 0, 0); PG8_STAGE_A(PG8_SA(1, 1), a1, 1, gcur);
;             PG8_WAIT_V(8); PG8_WAIT_L(0); PG8_BAR; PG8_MMA(0, 0, At, B0); PG8_MMA(0, 1, At, B1); PG8_BAR; PG8_SCHED;
;             PG8_LDA(At, 0, 1); PG8_STAGE(PG8_SB(0, 0), b2, voffB); PG8_STAGE(PG8_SB(0, 1), b2 + hstep, voffB); PG8_STAGE_A(PG8_SA(0, 0), a2, 0, gsel);
;             PG8_WAIT_V(8); PG8_WAIT_L(0); PG8_BAR; PG8_MMA(1, 0, At, B0); PG8_MMA(1, 1, At, B1); PG8_BAR; PG8_SCHED;
;             PG8_LDB(B0, 1, 0); PG8_LDB(B1, 1, 1); PG8_SCHED; PG8_LDA(At, 1, 0); PG8_STAGE_A(PG8_SA(0, 1), a2, 1, gsel);
;             PG8_WAIT_V(8); PG8_WAIT_L(0); PG8_BAR; PG8_MMA(0, 0, At, B0); PG8_MMA(0, 1, At, B1); PG8_BAR; PG8_SCHED;
.Lpeel953_body:
	v_add_u32_e32 v2, s76, v191
	v_add_u32_e32 v14, s77, v191
	ds_read_b128 v[18:21], v2
	ds_read_b128 v[22:25], v2 offset:1024
	ds_read_b128 v[26:29], v2 offset:2048
	ds_read_b128 v[30:33], v2 offset:3072
	ds_read_b128 v[2:5], v14
	ds_read_b128 v[6:9], v14 offset:1024
	ds_read_b128 v[10:13], v14 offset:2048
	ds_read_b128 v[14:17], v14 offset:3072
	s_add_u32 s52, s48, 0xfffe0080
	s_addc_u32 s53, s49, -1
	s_and_b64 s[50:51], s[50:51], exec
	s_cselect_b32 s53, s80, s53
	s_cselect_b32 s52, s81, s52
	s_cselect_b32 s51, s29, s82
	s_cselect_b32 s50, s28, s47
	v_lshl_add_u64 v[218:219], s[48:49], 0, v[172:173]
	s_add_i32 m0, s62, 0xc000
	ds_read_b128 v[182:185], v192
	ds_read_b128 v[186:189], v192 offset:1024
	ds_read_b128 v[194:197], v192 offset:2048
	ds_read_b128 v[198:201], v192 offset:3072
	ds_read_b128 v[202:205], v192 offset:4096
	ds_read_b128 v[206:209], v192 offset:5120
	ds_read_b128 v[210:213], v192 offset:6144
	ds_read_b128 v[214:217], v192 offset:7168
	global_load_lds_dwordx4 v[218:219], off
	v_lshl_add_u64 v[218:219], s[48:49], 0, v[174:175]
	s_add_i32 m0, s62, 0xe000
	s_nop 0
	global_load_lds_dwordx4 v[218:219], off
	s_waitcnt vmcnt(8)
	s_waitcnt lgkmcnt(0)
	s_barrier
	s_setprio 1
	s_waitcnt lgkmcnt(0)
	v_mfma_f32_16x16x128_f8f6f4 v[158:161], v[18:25], v[182:189], 0
	v_mfma_f32_16x16x128_f8f6f4 v[154:157], v[26:33], v[182:189], 0
	v_mfma_f32_16x16x128_f8f6f4 v[150:153], v[18:25], v[194:201], 0
	v_mfma_f32_16x16x128_f8f6f4 v[146:149], v[26:33], v[194:201], 0
	v_mfma_f32_16x16x128_f8f6f4 v[130:133], v[18:25], v[202:209], 0
	v_mfma_f32_16x16x128_f8f6f4 v[122:125], v[26:33], v[202:209], 0
	v_mfma_f32_16x16x128_f8f6f4 v[118:121], v[18:25], v[210:217], 0
	v_mfma_f32_16x16x128_f8f6f4 v[114:117], v[26:33], v[210:217], 0
	s_setprio 0
	s_setprio 1
	v_mfma_f32_16x16x128_f8f6f4 v[142:145], v[2:9], v[182:189], 0
	v_mfma_f32_16x16x128_f8f6f4 v[138:141], v[10:17], v[182:189], 0
	v_mfma_f32_16x16x128_f8f6f4 v[134:137], v[2:9], v[194:201], 0
	v_mfma_f32_16x16x128_f8f6f4 v[126:129], v[10:17], v[194:201], 0
	v_mfma_f32_16x16x128_f8f6f4 v[110:113], v[2:9], v[202:209], 0
	v_mfma_f32_16x16x128_f8f6f4 v[106:109], v[10:17], v[202:209], 0
	v_mfma_f32_16x16x128_f8f6f4 v[102:105], v[2:9], v[210:217], 0
	v_mfma_f32_16x16x128_f8f6f4 v[98:101], v[10:17], v[210:217], 0
	s_setprio 0
	s_barrier
	s_add_i32 s84, s76, s60
	v_lshl_add_u64 v[182:183], s[50:51], 0, v[166:167]
	s_mov_b32 m0, s84
	ds_read_b128 v[194:197], v192 offset:16384
	ds_read_b128 v[198:201], v192 offset:17408
	ds_read_b128 v[202:205], v192 offset:18432
	ds_read_b128 v[206:209], v192 offset:19456
	ds_read_b128 v[210:213], v192 offset:20480
	ds_read_b128 v[214:217], v192 offset:21504
	ds_read_b128 v[218:221], v192 offset:22528
	ds_read_b128 v[222:225], v192 offset:23552
	global_load_lds_dwordx4 v[182:183], off
	s_add_i32 m0, s84, 0x2000
	s_add_u32 s84, s50, 0x20000
	v_lshl_add_u64 v[184:185], s[50:51], 0, v[162:163]
	s_addc_u32 s85, s51, 0
	s_add_i32 s86, s77, s60
	global_load_lds_dwordx4 v[184:185], off
	v_lshl_add_u64 v[186:187], s[84:85], 0, v[166:167]
	s_mov_b32 m0, s86
	v_lshl_add_u64 v[188:189], s[52:53], 0, v[164:165]
	global_load_lds_dwordx4 v[186:187], off
	v_lshl_add_u64 v[186:187], s[84:85], 0, v[162:163]
	s_add_i32 m0, s86, 0x2000
	s_nop 0
	global_load_lds_dwordx4 v[186:187], off
	v_lshl_add_u64 v[186:187], s[52:53], 0, v[168:169]
	s_mov_b32 m0, s62
	s_nop 0
	global_load_lds_dwordx4 v[186:187], off
	s_mov_b32 m0, s63
	s_nop 0
	global_load_lds_dwordx4 v[188:189], off
	s_waitcnt vmcnt(8)
	s_waitcnt lgkmcnt(0)
	s_barrier
	s_setprio 1
	s_waitcnt lgkmcnt(0)
	v_mfma_f32_16x16x128_f8f6f4 v[94:97], v[18:25], v[194:201], 0
	v_mfma_f32_16x16x128_f8f6f4 v[90:93], v[26:33], v[194:201], 0
	v_mfma_f32_16x16x128_f8f6f4 v[86:89], v[18:25], v[202:209], 0
	v_mfma_f32_16x16x128_f8f6f4 v[82:85], v[26:33], v[202:209], 0
	v_mfma_f32_16x16x128_f8f6f4 v[66:69], v[18:25], v[210:217], 0
	v_mfma_f32_16x16x128_f8f6f4 v[58:61], v[26:33], v[210:217], 0
	v_mfma_f32_16x16x128_f8f6f4 v[54:57], v[18:25], v[218:225], 0
	v_mfma_f32_16x16x128_f8f6f4 v[50:53], v[26:33], v[218:225], 0
	s_setprio 0
	s_setprio 1
	v_mfma_f32_16x16x128_f8f6f4 v[78:81], v[2:9], v[194:201], 0
	v_mfma_f32_16x16x128_f8f6f4 v[74:77], v[10:17], v[194:201], 0
	v_mfma_f32_16x16x128_f8f6f4 v[70:73], v[2:9], v[202:209], 0
	v_mfma_f32_16x16x128_f8f6f4 v[62:65], v[10:17], v[202:209], 0
	v_mfma_f32_16x16x128_f8f6f4 v[46:49], v[2:9], v[210:217], 0
	v_mfma_f32_16x16x128_f8f6f4 v[42:45], v[10:17], v[210:217], 0
	v_mfma_f32_16x16x128_f8f6f4 v[38:41], v[2:9], v[218:225], 0
	v_mfma_f32_16x16x128_f8f6f4 v[34:37], v[10:17], v[218:225], 0
	s_setprio 0
	s_barrier
	s_add_i32 s84, 0, 0x18000
	s_add_i32 s85, 0, 0x1c000
	v_add_u32_e32 v14, s84, v191
	v_add_u32_e32 v30, s85, v191
	ds_read_b128 v[2:5], v14
	ds_read_b128 v[6:9], v14 offset:1024
	ds_read_b128 v[10:13], v14 offset:2048
	ds_read_b128 v[14:17], v14 offset:3072
	ds_read_b128 v[18:21], v30
	ds_read_b128 v[22:25], v30 offset:1024
	ds_read_b128 v[26:29], v30 offset:2048
	ds_read_b128 v[30:33], v30 offset:3072
	s_add_u32 s52, s52, 0x20000
	s_addc_u32 s53, s53, 0
	s_mov_b32 m0, s65
	v_lshl_add_u64 v[226:227], s[52:53], 0, v[168:169]
	ds_read_b128 v[194:197], v192 offset:32768
	ds_read_b128 v[198:201], v192 offset:33792
	ds_read_b128 v[202:205], v192 offset:34816
	ds_read_b128 v[206:209], v192 offset:35840
	ds_read_b128 v[210:213], v192 offset:36864
	ds_read_b128 v[214:217], v192 offset:37888
	ds_read_b128 v[218:221], v192 offset:38912
	ds_read_b128 v[222:225], v192 offset:39936
	global_load_lds_dwordx4 v[226:227], off
	v_lshl_add_u64 v[226:227], s[52:53], 0, v[164:165]
	s_mov_b32 m0, s66
	s_nop 0
	global_load_lds_dwordx4 v[226:227], off
	s_waitcnt vmcnt(8)
	s_waitcnt lgkmcnt(0)
	s_barrier
; #define PG8_STAGE(bufoff, gbase, voff) do { _Pragma("unroll") for (int _i = 0; _i < 2; ++_i) \
;         __builtin_amdgcn_global_load_lds((const unsigned*)((const char*)(gbase) + (voff)[_i]), (PG8_LAS unsigned*)(lds + (bufoff) + ldsw + _i * 8192), 16, 0, 0); } while (0)
; #define PG8_STAGE_A(bufoff, kbase, h, gv) do { if constexpr (GATHER) { PG8_STAGE(bufoff, kbase, (gv)[h]); } else { PG8_STAGE(bufoff, (kbase) + (h) * hstep, voffA); } } while (0)
; #define PG8_WAIT_V(n) asm volatile("s_waitcnt vmcnt(" #n ")" ::: "memory")
; #define PG8_WAIT_L(n) asm volatile("s_waitcnt lgkmcnt(" #n ")" ::: "memory")
; #define PG8_BAR __builtin_amdgcn_s_barrier()
; #define PG8_SCHED __builtin_amdgcn_sched_barrier(0)
; template <class Epi, class Sched, bool ALIGN_EPI = false, bool SP2 = false, bool FP8 = false, bool GATHER = false>
; __device__ __forceinline__ void gemm_phase(PG8_LAS unsigned char* lds, const Gemm g, const Sched& S, const Epi& E) {
;     ...
;             PG8_LDB(B0, 0, 0); PG8_LDB(B1, 0, 1); PG8_SCHED; PG8_LDA(At, 0, 0); PG8_STAGE_A(PG8_SA(1, 1), a1, 1, gcur);
;             PG8_WAIT_V(8); PG8_WAIT_L(0); PG8_BAR; PG8_MMA(0, 0, At, B0); PG8_MMA(0, 1, At, B1); PG8_BAR; PG8_SCHED;
;     ...
;             PG8_WAIT_V(8); PG8_WAIT_L(0); PG8_BAR; PG8_MMA(0, 0, At, B0); PG8_MMA(0, 1, At, B1); PG8_BAR; PG8_SCHED;
;             PG8_LDA(At, 1, 1); PG8_STAGE(PG8_SB(1, 0), b3, voffB); PG8_STAGE(PG8_SB(1, 1), b3 + hstep, voffB); PG8_STAGE_A(PG8_SA(1, 0), a3, 0, gsel);
;             PG8_WAIT_V(8); PG8_WAIT_L(0); PG8_BAR; PG8_MMA(1, 0, At, B0); PG8_MMA(1, 1, At, B1); PG8_BAR; PG8_SCHED;
	s_setprio 1
	s_waitcnt lgkmcnt(0)
	v_mfma_f32_16x16x128_f8f6f4 v[158:161], v[2:9], v[194:201], v[158:161]
	v_mfma_f32_16x16x128_f8f6f4 v[154:157], v[10:17], v[194:201], v[154:157]
	v_mfma_f32_16x16x128_f8f6f4 v[150:153], v[2:9], v[202:209], v[150:153]
	v_mfma_f32_16x16x128_f8f6f4 v[146:149], v[10:17], v[202:209], v[146:149]
	v_mfma_f32_16x16x128_f8f6f4 v[130:133], v[2:9], v[210:217], v[130:133]
	v_mfma_f32_16x16x128_f8f6f4 v[122:125], v[10:17], v[210:217], v[122:125]
	v_mfma_f32_16x16x128_f8f6f4 v[118:121], v[2:9], v[218:225], v[118:121]
	v_mfma_f32_16x16x128_f8f6f4 v[114:117], v[10:17], v[218:225], v[114:117]
	s_setprio 0
	s_setprio 1
	v_mfma_f32_16x16x128_f8f6f4 v[142:145], v[18:25], v[194:201], v[142:145]
	v_mfma_f32_16x16x128_f8f6f4 v[138:141], v[26:33], v[194:201], v[138:141]
	v_mfma_f32_16x16x128_f8f6f4 v[134:137], v[18:25], v[202:209], v[134:137]
	v_mfma_f32_16x16x128_f8f6f4 v[126:129], v[26:33], v[202:209], v[126:129]
	v_mfma_f32_16x16x128_f8f6f4 v[110:113], v[18:25], v[210:217], v[110:113]
	v_mfma_f32_16x16x128_f8f6f4 v[106:109], v[26:33], v[210:217], v[106:109]
	v_mfma_f32_16x16x128_f8f6f4 v[102:105], v[18:25], v[218:225], v[102:105]
	v_mfma_f32_16x16x128_f8f6f4 v[98:101], v[26:33], v[218:225], v[98:101]
	s_setprio 0
	s_barrier
	s_add_i32 s52, s84, s60
	v_lshl_add_u64 v[182:183], v[182:183], 0, s[18:19]
	s_mov_b32 m0, s52
	ds_read_b128 v[194:197], v192 offset:49152
	ds_read_b128 v[198:201], v192 offset:50176
	ds_read_b128 v[202:205], v192 offset:51200
	ds_read_b128 v[206:209], v192 offset:52224
	ds_read_b128 v[210:213], v192 offset:53248
	ds_read_b128 v[214:217], v192 offset:54272
	ds_read_b128 v[218:221], v192 offset:55296
	ds_read_b128 v[222:225], v192 offset:56320
	global_load_lds_dwordx4 v[182:183], off
	s_add_i32 m0, s52, 0x2000
	s_add_u32 s50, s50, 0x20080
	v_lshl_add_u64 v[182:183], v[184:185], 0, s[18:19]
	s_addc_u32 s51, s51, 0
	s_add_i32 s52, s85, s60
	global_load_lds_dwordx4 v[182:183], off
	v_lshl_add_u64 v[182:183], s[50:51], 0, v[166:167]
	s_mov_b32 m0, s52
	s_nop 0
	global_load_lds_dwordx4 v[182:183], off
	v_lshl_add_u64 v[182:183], s[50:51], 0, v[162:163]
	s_add_i32 m0, s52, 0x2000
	s_nop 0
	global_load_lds_dwordx4 v[182:183], off
	v_lshl_add_u64 v[182:183], v[186:187], 0, s[18:19]
	s_mov_b32 m0, s69
	s_nop 0
	global_load_lds_dwordx4 v[182:183], off
	v_lshl_add_u64 v[182:183], v[188:189], 0, s[18:19]
	s_mov_b32 m0, s70
	s_nop 0
	global_load_lds_dwordx4 v[182:183], off
	s_waitcnt vmcnt(8)
	s_waitcnt lgkmcnt(0)
	s_barrier
	s_setprio 1
	s_waitcnt lgkmcnt(0)
	v_mfma_f32_16x16x128_f8f6f4 v[94:97], v[2:9], v[194:201], v[94:97]
	v_mfma_f32_16x16x128_f8f6f4 v[90:93], v[10:17], v[194:201], v[90:93]
	v_mfma_f32_16x16x128_f8f6f4 v[86:89], v[2:9], v[202:209], v[86:89]
	v_mfma_f32_16x16x128_f8f6f4 v[82:85], v[10:17], v[202:209], v[82:85]
	v_mfma_f32_16x16x128_f8f6f4 v[66:69], v[2:9], v[210:217], v[66:69]
	v_mfma_f32_16x16x128_f8f6f4 v[58:61], v[10:17], v[210:217], v[58:61]
	v_mfma_f32_16x16x128_f8f6f4 v[54:57], v[2:9], v[218:225], v[54:57]
	v_mfma_f32_16x16x128_f8f6f4 v[50:53], v[10:17], v[218:225], v[50:53]
	s_setprio 0
	s_setprio 1
	v_mfma_f32_16x16x128_f8f6f4 v[78:81], v[18:25], v[194:201], v[78:81]
	v_mfma_f32_16x16x128_f8f6f4 v[74:77], v[26:33], v[194:201], v[74:77]
	v_mfma_f32_16x16x128_f8f6f4 v[70:73], v[18:25], v[202:209], v[70:73]
	v_mfma_f32_16x16x128_f8f6f4 v[62:65], v[26:33], v[202:209], v[62:65]
	v_mfma_f32_16x16x128_f8f6f4 v[46:49], v[18:25], v[210:217], v[46:49]
	v_mfma_f32_16x16x128_f8f6f4 v[42:45], v[26:33], v[210:217], v[42:45]
	v_mfma_f32_16x16x128_f8f6f4 v[38:41], v[18:25], v[218:225], v[38:41]
	v_mfma_f32_16x16x128_f8f6f4 v[34:37], v[26:33], v[218:225], v[34:37]
	s_setprio 0
	s_add_i32 s83, s83, 2
	s_add_u32 s48, s48, 0x100
	s_addc_u32 s49, s49, 0
	s_add_u32 s47, s47, 0x100
	s_addc_u32 s82, s82, 0
	s_cmp_gt_u32 s83, 5
	s_cbranch_scc1 .Lrot953_exit
	s_barrier
	s_branch .LBB0_954
.LBB0_953:
	v_add_u32_e32 v2, s76, v191
	v_add_u32_e32 v14, s77, v191
	ds_read_b128 v[18:21], v2
	ds_read_b128 v[22:25], v2 offset:1024
	ds_read_b128 v[26:29], v2 offset:2048
	ds_read_b128 v[30:33], v2 offset:3072
	ds_read_b128 v[2:5], v14
	ds_read_b128 v[6:9], v14 offset:1024
	ds_read_b128 v[10:13], v14 offset:2048
	ds_read_b128 v[14:17], v14 offset:3072
	s_add_u32 s52, s48, 0xfffe0080
	s_addc_u32 s53, s49, -1
	s_and_b64 s[50:51], s[50:51], exec
	s_cselect_b32 s53, s80, s53
	s_cselect_b32 s52, s81, s52
	s_cselect_b32 s51, s29, s82
	s_cselect_b32 s50, s28, s47
	v_lshl_add_u64 v[218:219], s[48:49], 0, v[172:173]
	s_add_i32 m0, s62, 0xc000
	ds_read_b128 v[182:185], v192
	ds_read_b128 v[186:189], v192 offset:1024
	ds_read_b128 v[194:197], v192 offset:2048
	ds_read_b128 v[198:201], v192 offset:3072
	ds_read_b128 v[202:205], v192 offset:4096
	ds_read_b128 v[206:209], v192 offset:5120
	ds_read_b128 v[210:213], v192 offset:6144
	ds_read_b128 v[214:217], v192 offset:7168
	global_load_lds_dwordx4 v[218:219], off
	v_lshl_add_u64 v[218:219], s[48:49], 0, v[174:175]
	s_add_i32 m0, s62, 0xe000
	s_nop 0
	global_load_lds_dwordx4 v[218:219], off
	s_waitcnt vmcnt(8)
	s_waitcnt lgkmcnt(0)
	s_barrier
; #define PG8_STAGE(bufoff, gbase, voff) do { _Pragma("unroll") for (int _i = 0; _i < 2; ++_i) \
;         __builtin_amdgcn_global_load_lds((const unsigned*)((const char*)(gbase) + (voff)[_i]), (PG8_LAS unsigned*)(lds + (bufoff) + ldsw + _i * 8192), 16, 0, 0); } while (0)
; #define PG8_STAGE_A(bufoff, kbase, h, gv) do { if constexpr (GATHER) { PG8_STAGE(bufoff, kbase, (gv)[h]); } else { PG8_STAGE(bufoff, (kbase) + (h) * hstep, voffA); } } while (0)
; #define PG8_WAIT_V(n) asm volatile("s_waitcnt vmcnt(" #n ")" ::: "memory")
; #define PG8_WAIT_L(n) asm volatile("s_waitcnt lgkmcnt(" #n ")" ::: "memory")
; #define PG8_BAR __builtin_amdgcn_s_barrier()
; #define PG8_SCHED __builtin_amdgcn_sched_barrier(0)
; template <class Epi, class Sched, bool ALIGN_EPI = false, bool SP2 = false, bool FP8 = false, bool GATHER = false>
; __device__ __forceinline__ void gemm_phase(PG8_LAS unsigned char* lds, const Gemm g, const Sched& S, const Epi& E) {
;     ...
;             PG8_WAIT_V(8); PG8_WAIT_L(0); PG8_BAR; PG8_MMA(0, 0, At, B0); PG8_MMA(0, 1, At, B1); PG8_BAR; PG8_SCHED;
;             PG8_LDA(At, 0, 1); PG8_STAGE(PG8_SB(0, 0), b2, voffB); PG8_STAGE(PG8_SB(0, 1), b2 + hstep, voffB); PG8_STAGE_A(PG8_SA(0, 0), a2, 0, gsel);
;             PG8_WAIT_V(8); PG8_WAIT_L(0); PG8_BAR; PG8_MMA(1, 0, At, B0); PG8_MMA(1, 1, At, B1); PG8_BAR; PG8_SCHED;
;             PG8_LDB(B0, 1, 0); PG8_LDB(B1, 1, 1); PG8_SCHED; PG8_LDA(At, 1, 0); PG8_STAGE_A(PG8_SA(0, 1), a2, 1, gsel);
;             PG8_WAIT_V(8); PG8_WAIT_L(0); PG8_BAR; PG8_MMA(0, 0, At, B0); PG8_MMA(0, 1, At, B1); PG8_BAR; PG8_SCHED;
	s_setprio 1
	s_waitcnt lgkmcnt(0)
	v_mfma_f32_16x16x128_f8f6f4 v[158:161], v[18:25], v[182:189], v[158:161]
	v_mfma_f32_16x16x128_f8f6f4 v[154:157], v[26:33], v[182:189], v[154:157]
	v_mfma_f32_16x16x128_f8f6f4 v[150:153], v[18:25], v[194:201], v[150:153]
	v_mfma_f32_16x16x128_f8f6f4 v[146:149], v[26:33], v[194:201], v[146:149]
	v_mfma_f32_16x16x128_f8f6f4 v[130:133], v[18:25], v[202:209], v[130:133]
	v_mfma_f32_16x16x128_f8f6f4 v[122:125], v[26:33], v[202:209], v[122:125]
	v_mfma_f32_16x16x128_f8f6f4 v[118:121], v[18:25], v[210:217], v[118:121]
	v_mfma_f32_16x16x128_f8f6f4 v[114:117], v[26:33], v[210:217], v[114:117]
	s_setprio 0
	s_setprio 1
	v_mfma_f32_16x16x128_f8f6f4 v[142:145], v[2:9], v[182:189], v[142:145]
	v_mfma_f32_16x16x128_f8f6f4 v[138:141], v[10:17], v[182:189], v[138:141]
	v_mfma_f32_16x16x128_f8f6f4 v[134:137], v[2:9], v[194:201], v[134:137]
	v_mfma_f32_16x16x128_f8f6f4 v[126:129], v[10:17], v[194:201], v[126:129]
	v_mfma_f32_16x16x128_f8f6f4 v[110:113], v[2:9], v[202:209], v[110:113]
	v_mfma_f32_16x16x128_f8f6f4 v[106:109], v[10:17], v[202:209], v[106:109]
	v_mfma_f32_16x16x128_f8f6f4 v[102:105], v[2:9], v[210:217], v[102:105]
	v_mfma_f32_16x16x128_f8f6f4 v[98:101], v[10:17], v[210:217], v[98:101]
	s_setprio 0
	s_barrier
	s_add_i32 s84, s76, s60
	v_lshl_add_u64 v[182:183], s[50:51], 0, v[166:167]
	s_mov_b32 m0, s84
	ds_read_b128 v[194:197], v192 offset:16384
	ds_read_b128 v[198:201], v192 offset:17408
	ds_read_b128 v[202:205], v192 offset:18432
	ds_read_b128 v[206:209], v192 offset:19456
	ds_read_b128 v[210:213], v192 offset:20480
	ds_read_b128 v[214:217], v192 offset:21504
	ds_read_b128 v[218:221], v192 offset:22528
	ds_read_b128 v[222:225], v192 offset:23552
	global_load_lds_dwordx4 v[182:183], off
	s_add_i32 m0, s84, 0x2000
	s_add_u32 s84, s50, 0x20000
	v_lshl_add_u64 v[184:185], s[50:51], 0, v[162:163]
	s_addc_u32 s85, s51, 0
	s_add_i32 s86, s77, s60
	global_load_lds_dwordx4 v[184:185], off
	v_lshl_add_u64 v[186:187], s[84:85], 0, v[166:167]
	s_mov_b32 m0, s86
	v_lshl_add_u64 v[188:189], s[52:53], 0, v[164:165]
	global_load_lds_dwordx4 v[186:187], off
	v_lshl_add_u64 v[186:187], s[84:85], 0, v[162:163]
	s_add_i32 m0, s86, 0x2000
	s_nop 0
	global_load_lds_dwordx4 v[186:187], off
	v_lshl_add_u64 v[186:187], s[52:53], 0, v[168:169]
	s_mov_b32 m0, s62
	s_nop 0
	global_load_lds_dwordx4 v[186:187], off
	s_mov_b32 m0, s63
	s_nop 0
	global_load_lds_dwordx4 v[188:189], off
	s_waitcnt vmcnt(8)
	s_waitcnt lgkmcnt(0)
	s_barrier
	s_setprio 1
	s_waitcnt lgkmcnt(0)
	v_mfma_f32_16x16x128_f8f6f4 v[94:97], v[18:25], v[194:201], v[94:97]
	v_mfma_f32_16x16x128_f8f6f4 v[90:93], v[26:33], v[194:201], v[90:93]
	v_mfma_f32_16x16x128_f8f6f4 v[86:89], v[18:25], v[202:209], v[86:89]
	v_mfma_f32_16x16x128_f8f6f4 v[82:85], v[26:33], v[202:209], v[82:85]
	v_mfma_f32_16x16x128_f8f6f4 v[66:69], v[18:25], v[210:217], v[66:69]
	v_mfma_f32_16x16x128_f8f6f4 v[58:61], v[26:33], v[210:217], v[58:61]
	v_mfma_f32_16x16x128_f8f6f4 v[54:57], v[18:25], v[218:225], v[54:57]
	v_mfma_f32_16x16x128_f8f6f4 v[50:53], v[26:33], v[218:225], v[50:53]
	s_setprio 0
	s_setprio 1
	v_mfma_f32_16x16x128_f8f6f4 v[78:81], v[2:9], v[194:201], v[78:81]
	v_mfma_f32_16x16x128_f8f6f4 v[74:77], v[10:17], v[194:201], v[74:77]
	v_mfma_f32_16x16x128_f8f6f4 v[70:73], v[2:9], v[202:209], v[70:73]
	v_mfma_f32_16x16x128_f8f6f4 v[62:65], v[10:17], v[202:209], v[62:65]
	v_mfma_f32_16x16x128_f8f6f4 v[46:49], v[2:9], v[210:217], v[46:49]
	v_mfma_f32_16x16x128_f8f6f4 v[42:45], v[10:17], v[210:217], v[42:45]
	v_mfma_f32_16x16x128_f8f6f4 v[38:41], v[2:9], v[218:225], v[38:41]
	v_mfma_f32_16x16x128_f8f6f4 v[34:37], v[10:17], v[218:225], v[34:37]
	s_setprio 0
	s_barrier
	s_add_i32 s84, 0, 0x18000
	s_add_i32 s85, 0, 0x1c000
	v_add_u32_e32 v14, s84, v191
	v_add_u32_e32 v30, s85, v191
	ds_read_b128 v[2:5], v14
	ds_read_b128 v[6:9], v14 offset:1024
	ds_read_b128 v[10:13], v14 offset:2048
	ds_read_b128 v[14:17], v14 offset:3072
	ds_read_b128 v[18:21], v30
	ds_read_b128 v[22:25], v30 offset:1024
	ds_read_b128 v[26:29], v30 offset:2048
	ds_read_b128 v[30:33], v30 offset:3072
	s_add_u32 s52, s52, 0x20000
	s_addc_u32 s53, s53, 0
	s_mov_b32 m0, s65
	v_lshl_add_u64 v[226:227], s[52:53], 0, v[168:169]
	ds_read_b128 v[194:197], v192 offset:32768
	ds_read_b128 v[198:201], v192 offset:33792
	ds_read_b128 v[202:205], v192 offset:34816
	ds_read_b128 v[206:209], v192 offset:35840
	ds_read_b128 v[210:213], v192 offset:36864
	ds_read_b128 v[214:217], v192 offset:37888
	ds_read_b128 v[218:221], v192 offset:38912
	ds_read_b128 v[222:225], v192 offset:39936
	global_load_lds_dwordx4 v[226:227], off
	v_lshl_add_u64 v[226:227], s[52:53], 0, v[164:165]
	s_mov_b32 m0, s66
	s_nop 0
	global_load_lds_dwordx4 v[226:227], off
	s_waitcnt vmcnt(8)
	s_waitcnt lgkmcnt(0)
	s_barrier
; #define PG8_STAGE(bufoff, gbase, voff) do { _Pragma("unroll") for (int _i = 0; _i < 2; ++_i) \
;         __builtin_amdgcn_global_load_lds((const unsigned*)((const char*)(gbase) + (voff)[_i]), (PG8_LAS unsigned*)(lds + (bufoff) + ldsw + _i * 8192), 16, 0, 0); } while (0)
; #define PG8_STAGE_A(bufoff, kbase, h, gv) do { if constexpr (GATHER) { PG8_STAGE(bufoff, kbase, (gv)[h]); } else { PG8_STAGE(bufoff, (kbase) + (h) * hstep, voffA); } } while (0)
; #define PG8_WAIT_V(n) asm volatile("s_waitcnt vmcnt(" #n ")" ::: "memory")
; #define PG8_WAIT_L(n) asm volatile("s_waitcnt lgkmcnt(" #n ")" ::: "memory")
; #define PG8_BAR __builtin_amdgcn_s_barrier()
; #define PG8_SCHED __builtin_amdgcn_sched_barrier(0)
; template <class Epi, class Sched, bool ALIGN_EPI = false, bool SP2 = false, bool FP8 = false, bool GATHER = false>
; __device__ __forceinline__ void gemm_phase(PG8_LAS unsigned char* lds, const Gemm g, const Sched& S, const Epi& E) {
;     ...
;             PG8_WAIT_V(8); PG8_WAIT_L(0); PG8_BAR; PG8_MMA(0, 0, At, B0); PG8_MMA(0, 1, At, B1); PG8_BAR; PG8_SCHED;
;             PG8_LDA(At, 1, 1); PG8_STAGE(PG8_SB(1, 0), b3, voffB); PG8_STAGE(PG8_SB(1, 1), b3 + hstep, voffB); PG8_STAGE_A(PG8_SA(1, 0), a3, 0, gsel);
;             PG8_WAIT_V(8); PG8_WAIT_L(0); PG8_BAR; PG8_MMA(1, 0, At, B0); PG8_MMA(1, 1, At, B1); PG8_BAR; PG8_SCHED;
	s_setprio 1
	s_waitcnt lgkmcnt(0)
	v_mfma_f32_16x16x128_f8f6f4 v[158:161], v[2:9], v[194:201], v[158:161]
	v_mfma_f32_16x16x128_f8f6f4 v[154:157], v[10:17], v[194:201], v[154:157]
	v_mfma_f32_16x16x128_f8f6f4 v[150:153], v[2:9], v[202:209], v[150:153]
	v_mfma_f32_16x16x128_f8f6f4 v[146:149], v[10:17], v[202:209], v[146:149]
	v_mfma_f32_16x16x128_f8f6f4 v[130:133], v[2:9], v[210:217], v[130:133]
	v_mfma_f32_16x16x128_f8f6f4 v[122:125], v[10:17], v[210:217], v[122:125]
	v_mfma_f32_16x16x128_f8f6f4 v[118:121], v[2:9], v[218:225], v[118:121]
	v_mfma_f32_16x16x128_f8f6f4 v[114:117], v[10:17], v[218:225], v[114:117]
	s_setprio 0
	s_setprio 1
	v_mfma_f32_16x16x128_f8f6f4 v[142:145], v[18:25], v[194:201], v[142:145]
	v_mfma_f32_16x16x128_f8f6f4 v[138:141], v[26:33], v[194:201], v[138:141]
	v_mfma_f32_16x16x128_f8f6f4 v[134:137], v[18:25], v[202:209], v[134:137]
	v_mfma_f32_16x16x128_f8f6f4 v[126:129], v[26:33], v[202:209], v[126:129]
	v_mfma_f32_16x16x128_f8f6f4 v[110:113], v[18:25], v[210:217], v[110:113]
	v_mfma_f32_16x16x128_f8f6f4 v[106:109], v[26:33], v[210:217], v[106:109]
	v_mfma_f32_16x16x128_f8f6f4 v[102:105], v[18:25], v[218:225], v[102:105]
	v_mfma_f32_16x16x128_f8f6f4 v[98:101], v[26:33], v[218:225], v[98:101]
	s_setprio 0
	s_barrier
	s_add_i32 s52, s84, s60
	v_lshl_add_u64 v[182:183], v[182:183], 0, s[18:19]
	s_mov_b32 m0, s52
	ds_read_b128 v[194:197], v192 offset:49152
	ds_read_b128 v[198:201], v192 offset:50176
	ds_read_b128 v[202:205], v192 offset:51200
	ds_read_b128 v[206:209], v192 offset:52224
	ds_read_b128 v[210:213], v192 offset:53248
	ds_read_b128 v[214:217], v192 offset:54272
	ds_read_b128 v[218:221], v192 offset:55296
	ds_read_b128 v[222:225], v192 offset:56320
	global_load_lds_dwordx4 v[182:183], off
	s_add_i32 m0, s52, 0x2000
	s_add_u32 s50, s50, 0x20080
	v_lshl_add_u64 v[182:183], v[184:185], 0, s[18:19]
	s_addc_u32 s51, s51, 0
	s_add_i32 s52, s85, s60
	global_load_lds_dwordx4 v[182:183], off
	v_lshl_add_u64 v[182:183], s[50:51], 0, v[166:167]
	s_mov_b32 m0, s52
	s_nop 0
	global_load_lds_dwordx4 v[182:183], off
	v_lshl_add_u64 v[182:183], s[50:51], 0, v[162:163]
	s_add_i32 m0, s52, 0x2000
	s_nop 0
	global_load_lds_dwordx4 v[182:183], off
	v_lshl_add_u64 v[182:183], v[186:187], 0, s[18:19]
	s_mov_b32 m0, s69
	s_nop 0
	global_load_lds_dwordx4 v[182:183], off
	v_lshl_add_u64 v[182:183], v[188:189], 0, s[18:19]
	s_mov_b32 m0, s70
	s_nop 0
	global_load_lds_dwordx4 v[182:183], off
	s_waitcnt vmcnt(8)
	s_waitcnt lgkmcnt(0)
	s_barrier
	s_setprio 1
	s_waitcnt lgkmcnt(0)
	v_mfma_f32_16x16x128_f8f6f4 v[94:97], v[2:9], v[194:201], v[94:97]
	v_mfma_f32_16x16x128_f8f6f4 v[90:93], v[10:17], v[194:201], v[90:93]
	v_mfma_f32_16x16x128_f8f6f4 v[86:89], v[2:9], v[202:209], v[86:89]
	v_mfma_f32_16x16x128_f8f6f4 v[82:85], v[10:17], v[202:209], v[82:85]
	v_mfma_f32_16x16x128_f8f6f4 v[66:69], v[2:9], v[210:217], v[66:69]
	v_mfma_f32_16x16x128_f8f6f4 v[58:61], v[10:17], v[210:217], v[58:61]
	v_mfma_f32_16x16x128_f8f6f4 v[54:57], v[2:9], v[218:225], v[54:57]
	v_mfma_f32_16x16x128_f8f6f4 v[50:53], v[10:17], v[218:225], v[50:53]
	s_setprio 0
	s_setprio 1
	v_mfma_f32_16x16x128_f8f6f4 v[78:81], v[18:25], v[194:201], v[78:81]
	v_mfma_f32_16x16x128_f8f6f4 v[74:77], v[26:33], v[194:201], v[74:77]
	v_mfma_f32_16x16x128_f8f6f4 v[70:73], v[18:25], v[202:209], v[70:73]
	v_mfma_f32_16x16x128_f8f6f4 v[62:65], v[26:33], v[202:209], v[62:65]
	v_mfma_f32_16x16x128_f8f6f4 v[46:49], v[18:25], v[210:217], v[46:49]
	v_mfma_f32_16x16x128_f8f6f4 v[42:45], v[26:33], v[210:217], v[42:45]
	v_mfma_f32_16x16x128_f8f6f4 v[38:41], v[18:25], v[218:225], v[38:41]
	v_mfma_f32_16x16x128_f8f6f4 v[34:37], v[26:33], v[218:225], v[34:37]
	s_setprio 0
	s_add_i32 s83, s83, 2
	s_add_u32 s48, s48, 0x100
	s_addc_u32 s49, s49, 0
	s_add_u32 s47, s47, 0x100
	s_addc_u32 s82, s82, 0
	s_cmp_gt_u32 s83, 5
	s_cbranch_scc1 .Lrot953_exit
	s_barrier

; #define PG8_BAR __builtin_amdgcn_s_barrier()
; template <class Epi, class Sched, bool ALIGN_EPI = false, bool SP2 = false, bool FP8 = false, bool GATHER = false>
; __device__ __forceinline__ void gemm_phase(PG8_LAS unsigned char* lds, const Gemm g, const Sched& S, const Epi& E) {
;     ...
;         if constexpr (FP8) asm volatile("s_nop 15\n\ts_nop 15" ::: "memory");
;         if constexpr (ALIGN_EPI) { if (wr == 0) PG8_BAR; }
;     __device__ __forceinline__ void pre(const pg8::Unit& u, int wid, int lane) const {
;         if (wid == 0) lds_dma16(bias + (size_t)(u.pn >> 8) * 1024 + (u.pn & 255) * 256 + lane * 4, (unsigned)(uintptr_t)(lds + LDS_EPI));
;         if (wid == 1) lds_dma16(row_w + (size_t)u.pm * 256 + lane * 4, (unsigned)(uintptr_t)(lds + LDS_EPI + 1024)); }
.LBB0_959:
	s_andn2_b64 vcc, exec, s[52:53]
	s_cbranch_vccnz .LBB0_953
	s_cmp_lg_u32 s59, 0
	s_cbranch_scc1 .LBB0_953
	s_add_i32 s52, 0, 0x20000
	s_mov_b32 s53, m0
	s_mov_b32 m0, s52
	s_nop 0
	global_load_lds_dwordx4 v[180:181], off
	s_mov_b32 m0, s53
	s_branch .LBB0_953
.Lrot953_exit:
	s_barrier
.LBB0_962:
	s_nop 15
	s_nop 15
	s_and_b64 vcc, exec, s[20:21]
	s_cbranch_vccz .LBB0_964
	s_barrier

; #define PG8_STAGE(bufoff, gbase, voff) do { _Pragma("unroll") for (int _i = 0; _i < 2; ++_i) \
;         __builtin_amdgcn_global_load_lds((const unsigned*)((const char*)(gbase) + (voff)[_i]), (PG8_LAS unsigned*)(lds + (bufoff) + ldsw + _i * 8192), 16, 0, 0); } while (0)
; template <class Epi, class Sched, bool ALIGN_EPI = false, bool SP2 = false, bool FP8 = false, bool GATHER = false>
; __device__ __forceinline__ void gemm_phase(PG8_LAS unsigned char* lds, const Gemm g, const Sched& S, const Epi& E) {
;     ...
;         const char* nA = (has_next && !GATHER) ? (const char*)g.A + (size_t)nxt.pm * tstep : cA; const char* nB = has_next ? (const char*)g.Bt + (size_t)S.brow(nxt) * (size_t)K * 2 : cB;
; #pragma nounroll
;         for (int t = 0; t < nt; t += 2) {
;             const bool last = (t == nt - 2);
;             const char* a1 = cA + (size_t)(t + 1) * kstep;
;             const char* a2 = last ? nA : cA + (size_t)(t + 2) * kstep; const char* b2 = last ? nB : cB + (size_t)(t + 2) * kstep;
;             const char* a3 = a2 + kstep; const char* b3 = b2 + kstep;
;             if (last && has_next) S.a_ready(nxt);
;             if (last) E.pre(cur, wid, lane);
;             if constexpr (GATHER) { if (t == nt - 4 && has_next) { _Pragma("unroll") for (int h_ = 0; h_ < 2; ++h_) _Pragma("unroll") for (int i_ = 0; i_ < 2; ++i_)
;                 asm volatile("global_load_dword %0, %1, off" : "+v"(graw[h_][i_]) : "v"(S.rowtok + (nxt.pm * BM + h_ * HALF + gR[i_])) : "memory"); } }
;             unsigned gsel[2][2];
;             if constexpr (GATHER) { _Pragma("unroll") for (int h_ = 0; h_ < 2; ++h_) _Pragma("unroll") for (int i_ = 0; i_ < 2; ++i_) { if (last && has_next) gnxt[h_][i_] = graw[h_][i_] * (unsigned)(K * 2) + gC[i_]; gsel[h_][i_] = (last && has_next) ? gnxt[h_][i_] : gcur[h_][i_]; } }
;             if constexpr (SP2) {
;             PG8_LDB(B0, 0, 0); PG8_LDB(B1, 0, 1); PG8_SCHED; PG8_LDA(At, 0, 0); PG8_STAGE_A(PG8_SA(1, 1), a1, 1, gcur);
;             PG8_WAIT_V(8); PG8_WAIT_L(0); PG8_BAR; PG8_MMA(0, 0, At, B0); PG8_MMA(0, 1, At, B1); PG8_BAR; PG8_SCHED;
;             PG8_LDA(At, 0, 1); PG8_STAGE(PG8_SB(0, 0), b2, voffB); PG8_STAGE(PG8_SB(0, 1), b2 + hstep, voffB); PG8_STAGE_A(PG8_SA(0, 0), a2, 0, gsel);
;             PG8_WAIT_V(8); PG8_WAIT_L(0); PG8_BAR; PG8_MMA(1, 0, At, B0); PG8_MMA(1, 1, At, B1); PG8_BAR; PG8_SCHED;
.LBB0_1127:
	s_mov_b32 s46, s7
	s_ashr_i32 s47, s7, 31
	s_lshl_b64 s[12:13], s[46:47], 19
	s_add_u32 s50, s65, s12
	s_addc_u32 s51, s66, s13
	s_mov_b32 s95, s14
	s_and_b64 s[12:13], s[48:49], exec
	s_cselect_b32 s7, s51, s9
	s_cselect_b32 s14, s50, s8
	s_lshl_b32 s12, s95, 8
	s_ashr_i32 s13, s12, 31
	s_lshl_b64 s[12:13], s[12:13], 11
	s_add_u32 s52, s67, s12
	s_addc_u32 s53, s68, s13
	s_and_b64 s[12:13], s[48:49], exec
	s_cselect_b32 s15, s53, s11
	s_cselect_b32 s16, s52, s10
	s_add_u32 s8, s8, 0x40080
	s_addc_u32 s9, s9, 0
	s_add_u32 s17, s10, 0x100
	s_addc_u32 s18, s11, 0
	s_mov_b32 s47, -2
	ds_read_b128 v[74:77], v164
	ds_read_b128 v[78:81], v164 offset:1024
	ds_read_b128 v[152:155], v164 offset:2048
	ds_read_b128 v[156:159], v164 offset:3072
	ds_read_b128 v[170:173], v165
	ds_read_b128 v[174:177], v165 offset:1024
	ds_read_b128 v[178:181], v165 offset:2048
	ds_read_b128 v[182:185], v165 offset:3072
	s_add_u32 s10, s8, 0xfffc0080
	s_addc_u32 s11, s9, -1
	s_cmp_eq_u32 s47, 12
	s_cselect_b32 s13, s7, s11
	s_cselect_b32 s12, s14, s10
	s_cselect_b32 s11, s15, s18
	s_cselect_b32 s10, s16, s17
	v_lshl_add_u64 v[160:161], s[8:9], 0, v[146:147]
	s_add_i32 m0, s69, 0xc000
	ds_read_b128 v[186:189], v166
	ds_read_b128 v[190:193], v166 offset:1024
	ds_read_b128 v[194:197], v166 offset:2048
	ds_read_b128 v[198:201], v166 offset:3072
	ds_read_b128 v[202:205], v166 offset:4096
	ds_read_b128 v[206:209], v166 offset:5120
	ds_read_b128 v[210:213], v166 offset:6144
	ds_read_b128 v[214:217], v166 offset:7168
	global_load_lds_dwordx4 v[160:161], off
	v_lshl_add_u64 v[160:161], s[8:9], 0, v[148:149]
	s_add_i32 m0, s69, 0xe000
	s_nop 0
	global_load_lds_dwordx4 v[160:161], off
	s_waitcnt vmcnt(8)
	s_waitcnt lgkmcnt(0)
	s_barrier
	s_setprio 1
	s_waitcnt lgkmcnt(0)
	v_mfma_f32_16x16x32_bf16 v[134:137], v[74:77], v[186:189], 0
	v_mfma_f32_16x16x32_bf16 v[130:133], v[152:155], v[186:189], 0
	v_mfma_f32_16x16x32_bf16 v[126:129], v[74:77], v[194:197], 0
	v_mfma_f32_16x16x32_bf16 v[122:125], v[152:155], v[194:197], 0
	v_mfma_f32_16x16x32_bf16 v[118:121], v[74:77], v[202:205], 0
	v_mfma_f32_16x16x32_bf16 v[114:117], v[152:155], v[202:205], 0
	v_mfma_f32_16x16x32_bf16 v[110:113], v[74:77], v[210:213], 0
	v_mfma_f32_16x16x32_bf16 v[106:109], v[152:155], v[210:213], 0
	v_mfma_f32_16x16x32_bf16 v[134:137], v[78:81], v[190:193], v[134:137]
	v_mfma_f32_16x16x32_bf16 v[130:133], v[156:159], v[190:193], v[130:133]
	v_mfma_f32_16x16x32_bf16 v[126:129], v[78:81], v[198:201], v[126:129]
	v_mfma_f32_16x16x32_bf16 v[122:125], v[156:159], v[198:201], v[122:125]
	v_mfma_f32_16x16x32_bf16 v[118:121], v[78:81], v[206:209], v[118:121]
	v_mfma_f32_16x16x32_bf16 v[114:117], v[156:159], v[206:209], v[114:117]
	v_mfma_f32_16x16x32_bf16 v[110:113], v[78:81], v[214:217], v[110:113]
	v_mfma_f32_16x16x32_bf16 v[106:109], v[156:159], v[214:217], v[106:109]
	s_setprio 0
	s_setprio 1
	v_mfma_f32_16x16x32_bf16 v[62:65], v[170:173], v[186:189], 0
	v_mfma_f32_16x16x32_bf16 v[58:61], v[178:181], v[186:189], 0
	v_mfma_f32_16x16x32_bf16 v[54:57], v[170:173], v[194:197], 0
	v_mfma_f32_16x16x32_bf16 v[50:53], v[178:181], v[194:197], 0
	v_mfma_f32_16x16x32_bf16 v[46:49], v[170:173], v[202:205], 0
	v_mfma_f32_16x16x32_bf16 v[42:45], v[178:181], v[202:205], 0
	v_mfma_f32_16x16x32_bf16 v[38:41], v[170:173], v[210:213], 0
	v_mfma_f32_16x16x32_bf16 v[34:37], v[178:181], v[210:213], 0
	v_mfma_f32_16x16x32_bf16 v[62:65], v[174:177], v[190:193], v[62:65]
	v_mfma_f32_16x16x32_bf16 v[58:61], v[182:185], v[190:193], v[58:61]
	v_mfma_f32_16x16x32_bf16 v[54:57], v[174:177], v[198:201], v[54:57]
	v_mfma_f32_16x16x32_bf16 v[50:53], v[182:185], v[198:201], v[50:53]
	v_mfma_f32_16x16x32_bf16 v[46:49], v[174:177], v[206:209], v[46:49]
	v_mfma_f32_16x16x32_bf16 v[42:45], v[182:185], v[206:209], v[42:45]
	v_mfma_f32_16x16x32_bf16 v[38:41], v[174:177], v[214:217], v[38:41]
	v_mfma_f32_16x16x32_bf16 v[34:37], v[182:185], v[214:217], v[34:37]
	s_setprio 0
	s_barrier
	s_add_i32 s55, s87, s45
	v_lshl_add_u64 v[160:161], s[10:11], 0, v[140:141]
	s_mov_b32 m0, s55
	ds_read_b128 v[186:189], v166 offset:16384
	ds_read_b128 v[190:193], v166 offset:17408
	ds_read_b128 v[194:197], v166 offset:18432
	ds_read_b128 v[198:201], v166 offset:19456
	ds_read_b128 v[202:205], v166 offset:20480
	ds_read_b128 v[206:209], v166 offset:21504
	ds_read_b128 v[210:213], v166 offset:22528
	ds_read_b128 v[214:217], v166 offset:23552
	global_load_lds_dwordx4 v[160:161], off
	s_add_i32 m0, s55, 0x2000
	s_add_u32 s56, s10, 0x40000
	v_lshl_add_u64 v[218:219], s[10:11], 0, v[144:145]
	s_addc_u32 s57, s11, 0
	s_add_i32 s55, s88, s45
	global_load_lds_dwordx4 v[218:219], off
	v_lshl_add_u64 v[220:221], s[56:57], 0, v[140:141]
	s_mov_b32 m0, s55
	v_lshl_add_u64 v[222:223], s[12:13], 0, v[142:143]
	global_load_lds_dwordx4 v[220:221], off
	v_lshl_add_u64 v[220:221], s[56:57], 0, v[144:145]
	s_add_i32 m0, s55, 0x2000
	s_nop 0
	global_load_lds_dwordx4 v[220:221], off
	v_lshl_add_u64 v[220:221], s[12:13], 0, v[138:139]
	s_mov_b32 m0, s69
	s_nop 0
	global_load_lds_dwordx4 v[220:221], off
	s_mov_b32 m0, s70
	s_nop 0
	global_load_lds_dwordx4 v[222:223], off
	s_waitcnt vmcnt(8)
	s_waitcnt lgkmcnt(0)
	s_barrier
; #define PG8_STAGE_A(bufoff, kbase, h, gv) do { if constexpr (GATHER) { PG8_STAGE(bufoff, kbase, (gv)[h]); } else { PG8_STAGE(bufoff, (kbase) + (h) * hstep, voffA); } } while (0)
; #define PG8_WAIT_V(n) asm volatile("s_waitcnt vmcnt(" #n ")" ::: "memory")
; #define PG8_WAIT_L(n) asm volatile("s_waitcnt lgkmcnt(" #n ")" ::: "memory")
; #define PG8_BAR __builtin_amdgcn_s_barrier()
; #define PG8_SCHED __builtin_amdgcn_sched_barrier(0)
; template <class Epi, class Sched, bool ALIGN_EPI = false, bool SP2 = false, bool FP8 = false, bool GATHER = false>
; __device__ __forceinline__ void gemm_phase(PG8_LAS unsigned char* lds, const Gemm g, const Sched& S, const Epi& E) {
;     ...
;             PG8_WAIT_V(8); PG8_WAIT_L(0); PG8_BAR; PG8_MMA(1, 0, At, B0); PG8_MMA(1, 1, At, B1); PG8_BAR; PG8_SCHED;
;             PG8_LDB(B0, 1, 0); PG8_LDB(B1, 1, 1); PG8_SCHED; PG8_LDA(At, 1, 0); PG8_STAGE_A(PG8_SA(0, 1), a2, 1, gsel);
;             PG8_WAIT_V(8); PG8_WAIT_L(0); PG8_BAR; PG8_MMA(0, 0, At, B0); PG8_MMA(0, 1, At, B1); PG8_BAR; PG8_SCHED;
	s_setprio 1
	s_waitcnt lgkmcnt(0)
	v_mfma_f32_16x16x32_bf16 v[102:105], v[74:77], v[186:189], 0
	v_mfma_f32_16x16x32_bf16 v[98:101], v[152:155], v[186:189], 0
	v_mfma_f32_16x16x32_bf16 v[94:97], v[74:77], v[194:197], 0
	v_mfma_f32_16x16x32_bf16 v[90:93], v[152:155], v[194:197], 0
	v_mfma_f32_16x16x32_bf16 v[86:89], v[74:77], v[202:205], 0
	v_mfma_f32_16x16x32_bf16 v[82:85], v[152:155], v[202:205], 0
	v_mfma_f32_16x16x32_bf16 v[70:73], v[74:77], v[210:213], 0
	v_mfma_f32_16x16x32_bf16 v[66:69], v[152:155], v[210:213], 0
	v_mfma_f32_16x16x32_bf16 v[102:105], v[78:81], v[190:193], v[102:105]
	v_mfma_f32_16x16x32_bf16 v[98:101], v[156:159], v[190:193], v[98:101]
	v_mfma_f32_16x16x32_bf16 v[94:97], v[78:81], v[198:201], v[94:97]
	v_mfma_f32_16x16x32_bf16 v[90:93], v[156:159], v[198:201], v[90:93]
	v_mfma_f32_16x16x32_bf16 v[86:89], v[78:81], v[206:209], v[86:89]
	v_mfma_f32_16x16x32_bf16 v[82:85], v[156:159], v[206:209], v[82:85]
	v_mfma_f32_16x16x32_bf16 v[70:73], v[78:81], v[214:217], v[70:73]
	v_mfma_f32_16x16x32_bf16 v[66:69], v[156:159], v[214:217], v[66:69]
	s_setprio 0
	s_setprio 1
	v_mfma_f32_16x16x32_bf16 v[30:33], v[170:173], v[186:189], 0
	v_mfma_f32_16x16x32_bf16 v[26:29], v[178:181], v[186:189], 0
	v_mfma_f32_16x16x32_bf16 v[22:25], v[170:173], v[194:197], 0
	v_mfma_f32_16x16x32_bf16 v[18:21], v[178:181], v[194:197], 0
	v_mfma_f32_16x16x32_bf16 v[14:17], v[170:173], v[202:205], 0
	v_mfma_f32_16x16x32_bf16 v[10:13], v[178:181], v[202:205], 0
	v_mfma_f32_16x16x32_bf16 v[6:9], v[170:173], v[210:213], 0
	v_mfma_f32_16x16x32_bf16 v[2:5], v[178:181], v[210:213], 0
	v_mfma_f32_16x16x32_bf16 v[30:33], v[174:177], v[190:193], v[30:33]
	v_mfma_f32_16x16x32_bf16 v[26:29], v[182:185], v[190:193], v[26:29]
	v_mfma_f32_16x16x32_bf16 v[22:25], v[174:177], v[198:201], v[22:25]
	v_mfma_f32_16x16x32_bf16 v[18:21], v[182:185], v[198:201], v[18:21]
	v_mfma_f32_16x16x32_bf16 v[14:17], v[174:177], v[206:209], v[14:17]
	v_mfma_f32_16x16x32_bf16 v[10:13], v[182:185], v[206:209], v[10:13]
	v_mfma_f32_16x16x32_bf16 v[6:9], v[174:177], v[214:217], v[6:9]
	v_mfma_f32_16x16x32_bf16 v[2:5], v[182:185], v[214:217], v[2:5]
	s_setprio 0
	s_barrier
	s_add_i32 s55, 0, 0x18000
	s_add_i32 s56, 0, 0x1c000
	v_add_u32_e32 v156, s55, v163
	v_add_u32_e32 v182, s56, v163
	ds_read_b128 v[74:77], v156
	ds_read_b128 v[78:81], v156 offset:1024
	ds_read_b128 v[152:155], v156 offset:2048
	ds_read_b128 v[156:159], v156 offset:3072
	ds_read_b128 v[170:173], v182
	ds_read_b128 v[174:177], v182 offset:1024
	ds_read_b128 v[178:181], v182 offset:2048
	ds_read_b128 v[182:185], v182 offset:3072
	s_add_u32 s12, s12, 0x40000
	s_addc_u32 s13, s13, 0
	s_mov_b32 m0, s71
	v_lshl_add_u64 v[224:225], s[12:13], 0, v[138:139]
	ds_read_b128 v[186:189], v166 offset:32768
	ds_read_b128 v[190:193], v166 offset:33792
	ds_read_b128 v[194:197], v166 offset:34816
	ds_read_b128 v[198:201], v166 offset:35840
	ds_read_b128 v[202:205], v166 offset:36864
	ds_read_b128 v[206:209], v166 offset:37888
	ds_read_b128 v[210:213], v166 offset:38912
	ds_read_b128 v[214:217], v166 offset:39936
	global_load_lds_dwordx4 v[224:225], off
	v_lshl_add_u64 v[224:225], s[12:13], 0, v[142:143]
	s_mov_b32 m0, s72
	s_nop 0
	global_load_lds_dwordx4 v[224:225], off
	s_waitcnt vmcnt(8)
	s_waitcnt lgkmcnt(0)
	s_barrier
	s_setprio 1
	s_waitcnt lgkmcnt(0)
	v_mfma_f32_16x16x32_bf16 v[134:137], v[74:77], v[186:189], v[134:137]
	v_mfma_f32_16x16x32_bf16 v[130:133], v[152:155], v[186:189], v[130:133]
	v_mfma_f32_16x16x32_bf16 v[126:129], v[74:77], v[194:197], v[126:129]
	v_mfma_f32_16x16x32_bf16 v[122:125], v[152:155], v[194:197], v[122:125]
	v_mfma_f32_16x16x32_bf16 v[118:121], v[74:77], v[202:205], v[118:121]
	v_mfma_f32_16x16x32_bf16 v[114:117], v[152:155], v[202:205], v[114:117]
	v_mfma_f32_16x16x32_bf16 v[110:113], v[74:77], v[210:213], v[110:113]
	v_mfma_f32_16x16x32_bf16 v[106:109], v[152:155], v[210:213], v[106:109]
	v_mfma_f32_16x16x32_bf16 v[134:137], v[78:81], v[190:193], v[134:137]
	v_mfma_f32_16x16x32_bf16 v[130:133], v[156:159], v[190:193], v[130:133]
	v_mfma_f32_16x16x32_bf16 v[126:129], v[78:81], v[198:201], v[126:129]
	v_mfma_f32_16x16x32_bf16 v[122:125], v[156:159], v[198:201], v[122:125]
	v_mfma_f32_16x16x32_bf16 v[118:121], v[78:81], v[206:209], v[118:121]
	v_mfma_f32_16x16x32_bf16 v[114:117], v[156:159], v[206:209], v[114:117]
	v_mfma_f32_16x16x32_bf16 v[110:113], v[78:81], v[214:217], v[110:113]
	v_mfma_f32_16x16x32_bf16 v[106:109], v[156:159], v[214:217], v[106:109]
	s_setprio 0
	s_setprio 1
	v_mfma_f32_16x16x32_bf16 v[62:65], v[170:173], v[186:189], v[62:65]
	v_mfma_f32_16x16x32_bf16 v[58:61], v[178:181], v[186:189], v[58:61]
	v_mfma_f32_16x16x32_bf16 v[54:57], v[170:173], v[194:197], v[54:57]
	v_mfma_f32_16x16x32_bf16 v[50:53], v[178:181], v[194:197], v[50:53]
	v_mfma_f32_16x16x32_bf16 v[46:49], v[170:173], v[202:205], v[46:49]
	v_mfma_f32_16x16x32_bf16 v[42:45], v[178:181], v[202:205], v[42:45]
	v_mfma_f32_16x16x32_bf16 v[38:41], v[170:173], v[210:213], v[38:41]
	v_mfma_f32_16x16x32_bf16 v[34:37], v[178:181], v[210:213], v[34:37]
	v_mfma_f32_16x16x32_bf16 v[62:65], v[174:177], v[190:193], v[62:65]
	v_mfma_f32_16x16x32_bf16 v[58:61], v[182:185], v[190:193], v[58:61]
	v_mfma_f32_16x16x32_bf16 v[54:57], v[174:177], v[198:201], v[54:57]
	v_mfma_f32_16x16x32_bf16 v[50:53], v[182:185], v[198:201], v[50:53]
	v_mfma_f32_16x16x32_bf16 v[46:49], v[174:177], v[206:209], v[46:49]
	v_mfma_f32_16x16x32_bf16 v[42:45], v[182:185], v[206:209], v[42:45]
	v_mfma_f32_16x16x32_bf16 v[38:41], v[174:177], v[214:217], v[38:41]
	v_mfma_f32_16x16x32_bf16 v[34:37], v[182:185], v[214:217], v[34:37]
	s_setprio 0
	s_barrier
; #define PG8_STAGE(bufoff, gbase, voff) do { _Pragma("unroll") for (int _i = 0; _i < 2; ++_i) \
;         __builtin_amdgcn_global_load_lds((const unsigned*)((const char*)(gbase) + (voff)[_i]), (PG8_LAS unsigned*)(lds + (bufoff) + ldsw + _i * 8192), 16, 0, 0); } while (0)
; #define PG8_STAGE_A(bufoff, kbase, h, gv) do { if constexpr (GATHER) { PG8_STAGE(bufoff, kbase, (gv)[h]); } else { PG8_STAGE(bufoff, (kbase) + (h) * hstep, voffA); } } while (0)
; #define PG8_WAIT_V(n) asm volatile("s_waitcnt vmcnt(" #n ")" ::: "memory")
; #define PG8_WAIT_L(n) asm volatile("s_waitcnt lgkmcnt(" #n ")" ::: "memory")
; #define PG8_BAR __builtin_amdgcn_s_barrier()
; #define PG8_SCHED __builtin_amdgcn_sched_barrier(0)
; template <class Epi, class Sched, bool ALIGN_EPI = false, bool SP2 = false, bool FP8 = false, bool GATHER = false>
; __device__ __forceinline__ void gemm_phase(PG8_LAS unsigned char* lds, const Gemm g, const Sched& S, const Epi& E) {
;     ...
;             PG8_LDB(B0, 0, 0); PG8_LDB(B1, 0, 1); PG8_SCHED; PG8_LDA(At, 0, 0); PG8_STAGE_A(PG8_SA(1, 1), a1, 1, gcur);
;             PG8_WAIT_V(8); PG8_WAIT_L(0); PG8_BAR; PG8_MMA(0, 0, At, B0); PG8_MMA(0, 1, At, B1); PG8_BAR; PG8_SCHED;
;     ...
;             PG8_LDA(At, 1, 1); PG8_STAGE(PG8_SB(1, 0), b3, voffB); PG8_STAGE(PG8_SB(1, 1), b3 + hstep, voffB); PG8_STAGE_A(PG8_SA(1, 0), a3, 0, gsel);
;             PG8_WAIT_V(8); PG8_WAIT_L(0); PG8_BAR; PG8_MMA(1, 0, At, B0); PG8_MMA(1, 1, At, B1); PG8_BAR; PG8_SCHED;
	s_add_i32 s12, s55, s45
	v_lshl_add_u64 v[160:161], v[160:161], 0, s[28:29]
	s_mov_b32 m0, s12
	ds_read_b128 v[186:189], v166 offset:49152
	ds_read_b128 v[190:193], v166 offset:50176
	ds_read_b128 v[194:197], v166 offset:51200
	ds_read_b128 v[198:201], v166 offset:52224
	ds_read_b128 v[202:205], v166 offset:53248
	ds_read_b128 v[206:209], v166 offset:54272
	ds_read_b128 v[210:213], v166 offset:55296
	ds_read_b128 v[214:217], v166 offset:56320
	global_load_lds_dwordx4 v[160:161], off
	s_add_i32 m0, s12, 0x2000
	s_add_u32 s10, s10, 0x40080
	v_lshl_add_u64 v[160:161], v[218:219], 0, s[28:29]
	s_addc_u32 s11, s11, 0
	s_add_i32 s12, s56, s45
	global_load_lds_dwordx4 v[160:161], off
	v_lshl_add_u64 v[160:161], s[10:11], 0, v[140:141]
	s_mov_b32 m0, s12
	s_nop 0
	global_load_lds_dwordx4 v[160:161], off
	v_lshl_add_u64 v[160:161], s[10:11], 0, v[144:145]
	s_add_i32 m0, s12, 0x2000
	s_nop 0
	global_load_lds_dwordx4 v[160:161], off
	v_lshl_add_u64 v[160:161], v[220:221], 0, s[28:29]
	s_mov_b32 m0, s79
	s_nop 0
	global_load_lds_dwordx4 v[160:161], off
	v_lshl_add_u64 v[160:161], v[222:223], 0, s[28:29]
	s_mov_b32 m0, s80
	s_nop 0
	global_load_lds_dwordx4 v[160:161], off
	s_waitcnt vmcnt(8)
	s_waitcnt lgkmcnt(0)
	s_barrier
	s_setprio 1
	s_waitcnt lgkmcnt(0)
	v_mfma_f32_16x16x32_bf16 v[102:105], v[74:77], v[186:189], v[102:105]
	v_mfma_f32_16x16x32_bf16 v[98:101], v[152:155], v[186:189], v[98:101]
	v_mfma_f32_16x16x32_bf16 v[94:97], v[74:77], v[194:197], v[94:97]
	v_mfma_f32_16x16x32_bf16 v[90:93], v[152:155], v[194:197], v[90:93]
	v_mfma_f32_16x16x32_bf16 v[86:89], v[74:77], v[202:205], v[86:89]
	v_mfma_f32_16x16x32_bf16 v[82:85], v[152:155], v[202:205], v[82:85]
	v_mfma_f32_16x16x32_bf16 v[70:73], v[74:77], v[210:213], v[70:73]
	v_mfma_f32_16x16x32_bf16 v[66:69], v[152:155], v[210:213], v[66:69]
	v_mfma_f32_16x16x32_bf16 v[102:105], v[78:81], v[190:193], v[102:105]
	v_mfma_f32_16x16x32_bf16 v[98:101], v[156:159], v[190:193], v[98:101]
	v_mfma_f32_16x16x32_bf16 v[94:97], v[78:81], v[198:201], v[94:97]
	v_mfma_f32_16x16x32_bf16 v[90:93], v[156:159], v[198:201], v[90:93]
	v_mfma_f32_16x16x32_bf16 v[86:89], v[78:81], v[206:209], v[86:89]
	v_mfma_f32_16x16x32_bf16 v[82:85], v[156:159], v[206:209], v[82:85]
	v_mfma_f32_16x16x32_bf16 v[70:73], v[78:81], v[214:217], v[70:73]
	v_mfma_f32_16x16x32_bf16 v[66:69], v[156:159], v[214:217], v[66:69]
	s_setprio 0
	s_setprio 1
	v_mfma_f32_16x16x32_bf16 v[30:33], v[170:173], v[186:189], v[30:33]
	v_mfma_f32_16x16x32_bf16 v[26:29], v[178:181], v[186:189], v[26:29]
	v_mfma_f32_16x16x32_bf16 v[22:25], v[170:173], v[194:197], v[22:25]
	v_mfma_f32_16x16x32_bf16 v[18:21], v[178:181], v[194:197], v[18:21]
	v_mfma_f32_16x16x32_bf16 v[14:17], v[170:173], v[202:205], v[14:17]
	v_mfma_f32_16x16x32_bf16 v[10:13], v[178:181], v[202:205], v[10:13]
	v_mfma_f32_16x16x32_bf16 v[6:9], v[170:173], v[210:213], v[6:9]
	v_mfma_f32_16x16x32_bf16 v[2:5], v[178:181], v[210:213], v[2:5]
	v_mfma_f32_16x16x32_bf16 v[30:33], v[174:177], v[190:193], v[30:33]
	v_mfma_f32_16x16x32_bf16 v[26:29], v[182:185], v[190:193], v[26:29]
	v_mfma_f32_16x16x32_bf16 v[22:25], v[174:177], v[198:201], v[22:25]
	v_mfma_f32_16x16x32_bf16 v[18:21], v[182:185], v[198:201], v[18:21]
	v_mfma_f32_16x16x32_bf16 v[14:17], v[174:177], v[206:209], v[14:17]
	v_mfma_f32_16x16x32_bf16 v[10:13], v[182:185], v[206:209], v[10:13]
	v_mfma_f32_16x16x32_bf16 v[6:9], v[174:177], v[214:217], v[6:9]
	v_mfma_f32_16x16x32_bf16 v[2:5], v[182:185], v[214:217], v[2:5]
	s_setprio 0
	s_add_i32 s47, s47, 2
	s_add_u32 s8, s8, 0x100
	s_addc_u32 s9, s9, 0
	s_add_u32 s17, s17, 0x100
	s_addc_u32 s18, s18, 0
	s_cmp_gt_u32 s47, 13
.LBB0_1128:
	s_barrier
	ds_read_b128 v[74:77], v164
	ds_read_b128 v[78:81], v164 offset:1024
	ds_read_b128 v[152:155], v164 offset:2048
	ds_read_b128 v[156:159], v164 offset:3072
	ds_read_b128 v[170:173], v165
	ds_read_b128 v[174:177], v165 offset:1024
	ds_read_b128 v[178:181], v165 offset:2048
	ds_read_b128 v[182:185], v165 offset:3072
	s_add_u32 s10, s8, 0xfffc0080
	s_addc_u32 s11, s9, -1
	s_cmp_eq_u32 s47, 12
	s_cselect_b32 s13, s7, s11
	s_cselect_b32 s12, s14, s10
	s_cselect_b32 s11, s15, s18
	s_cselect_b32 s10, s16, s17
	v_lshl_add_u64 v[160:161], s[8:9], 0, v[146:147]
	s_add_i32 m0, s69, 0xc000
	ds_read_b128 v[186:189], v166
	ds_read_b128 v[190:193], v166 offset:1024
	ds_read_b128 v[194:197], v166 offset:2048
	ds_read_b128 v[198:201], v166 offset:3072
	ds_read_b128 v[202:205], v166 offset:4096
	ds_read_b128 v[206:209], v166 offset:5120
	ds_read_b128 v[210:213], v166 offset:6144
	ds_read_b128 v[214:217], v166 offset:7168
	global_load_lds_dwordx4 v[160:161], off
	v_lshl_add_u64 v[160:161], s[8:9], 0, v[148:149]
	s_add_i32 m0, s69, 0xe000
	s_nop 0
	global_load_lds_dwordx4 v[160:161], off
	s_waitcnt vmcnt(8)
	s_waitcnt lgkmcnt(0)
	s_barrier
; #define PG8_STAGE(bufoff, gbase, voff) do { _Pragma("unroll") for (int _i = 0; _i < 2; ++_i) \
;         __builtin_amdgcn_global_load_lds((const unsigned*)((const char*)(gbase) + (voff)[_i]), (PG8_LAS unsigned*)(lds + (bufoff) + ldsw + _i * 8192), 16, 0, 0); } while (0)
; #define PG8_STAGE_A(bufoff, kbase, h, gv) do { if constexpr (GATHER) { PG8_STAGE(bufoff, kbase, (gv)[h]); } else { PG8_STAGE(bufoff, (kbase) + (h) * hstep, voffA); } } while (0)
; #define PG8_WAIT_V(n) asm volatile("s_waitcnt vmcnt(" #n ")" ::: "memory")
; #define PG8_WAIT_L(n) asm volatile("s_waitcnt lgkmcnt(" #n ")" ::: "memory")
; #define PG8_BAR __builtin_amdgcn_s_barrier()
; #define PG8_SCHED __builtin_amdgcn_sched_barrier(0)
; template <class Epi, class Sched, bool ALIGN_EPI = false, bool SP2 = false, bool FP8 = false, bool GATHER = false>
; __device__ __forceinline__ void gemm_phase(PG8_LAS unsigned char* lds, const Gemm g, const Sched& S, const Epi& E) {
;     ...
;             PG8_WAIT_V(8); PG8_WAIT_L(0); PG8_BAR; PG8_MMA(0, 0, At, B0); PG8_MMA(0, 1, At, B1); PG8_BAR; PG8_SCHED;
;             PG8_LDA(At, 0, 1); PG8_STAGE(PG8_SB(0, 0), b2, voffB); PG8_STAGE(PG8_SB(0, 1), b2 + hstep, voffB); PG8_STAGE_A(PG8_SA(0, 0), a2, 0, gsel);
;             PG8_WAIT_V(8); PG8_WAIT_L(0); PG8_BAR; PG8_MMA(1, 0, At, B0); PG8_MMA(1, 1, At, B1); PG8_BAR; PG8_SCHED;
	s_setprio 1
	s_waitcnt lgkmcnt(0)
	v_mfma_f32_16x16x32_bf16 v[134:137], v[74:77], v[186:189], v[134:137]
	v_mfma_f32_16x16x32_bf16 v[130:133], v[152:155], v[186:189], v[130:133]
	v_mfma_f32_16x16x32_bf16 v[126:129], v[74:77], v[194:197], v[126:129]
	v_mfma_f32_16x16x32_bf16 v[122:125], v[152:155], v[194:197], v[122:125]
	v_mfma_f32_16x16x32_bf16 v[118:121], v[74:77], v[202:205], v[118:121]
	v_mfma_f32_16x16x32_bf16 v[114:117], v[152:155], v[202:205], v[114:117]
	v_mfma_f32_16x16x32_bf16 v[110:113], v[74:77], v[210:213], v[110:113]
	v_mfma_f32_16x16x32_bf16 v[106:109], v[152:155], v[210:213], v[106:109]
	v_mfma_f32_16x16x32_bf16 v[134:137], v[78:81], v[190:193], v[134:137]
	v_mfma_f32_16x16x32_bf16 v[130:133], v[156:159], v[190:193], v[130:133]
	v_mfma_f32_16x16x32_bf16 v[126:129], v[78:81], v[198:201], v[126:129]
	v_mfma_f32_16x16x32_bf16 v[122:125], v[156:159], v[198:201], v[122:125]
	v_mfma_f32_16x16x32_bf16 v[118:121], v[78:81], v[206:209], v[118:121]
	v_mfma_f32_16x16x32_bf16 v[114:117], v[156:159], v[206:209], v[114:117]
	v_mfma_f32_16x16x32_bf16 v[110:113], v[78:81], v[214:217], v[110:113]
	v_mfma_f32_16x16x32_bf16 v[106:109], v[156:159], v[214:217], v[106:109]
	s_setprio 0
	s_setprio 1
	v_mfma_f32_16x16x32_bf16 v[62:65], v[170:173], v[186:189], v[62:65]
	v_mfma_f32_16x16x32_bf16 v[58:61], v[178:181], v[186:189], v[58:61]
	v_mfma_f32_16x16x32_bf16 v[54:57], v[170:173], v[194:197], v[54:57]
	v_mfma_f32_16x16x32_bf16 v[50:53], v[178:181], v[194:197], v[50:53]
	v_mfma_f32_16x16x32_bf16 v[46:49], v[170:173], v[202:205], v[46:49]
	v_mfma_f32_16x16x32_bf16 v[42:45], v[178:181], v[202:205], v[42:45]
	v_mfma_f32_16x16x32_bf16 v[38:41], v[170:173], v[210:213], v[38:41]
	v_mfma_f32_16x16x32_bf16 v[34:37], v[178:181], v[210:213], v[34:37]
	v_mfma_f32_16x16x32_bf16 v[62:65], v[174:177], v[190:193], v[62:65]
	v_mfma_f32_16x16x32_bf16 v[58:61], v[182:185], v[190:193], v[58:61]
	v_mfma_f32_16x16x32_bf16 v[54:57], v[174:177], v[198:201], v[54:57]
	v_mfma_f32_16x16x32_bf16 v[50:53], v[182:185], v[198:201], v[50:53]
	v_mfma_f32_16x16x32_bf16 v[46:49], v[174:177], v[206:209], v[46:49]
	v_mfma_f32_16x16x32_bf16 v[42:45], v[182:185], v[206:209], v[42:45]
	v_mfma_f32_16x16x32_bf16 v[38:41], v[174:177], v[214:217], v[38:41]
	v_mfma_f32_16x16x32_bf16 v[34:37], v[182:185], v[214:217], v[34:37]
	s_setprio 0
	s_barrier
	s_add_i32 s55, s87, s45
	v_lshl_add_u64 v[160:161], s[10:11], 0, v[140:141]
	s_mov_b32 m0, s55
	ds_read_b128 v[186:189], v166 offset:16384
	ds_read_b128 v[190:193], v166 offset:17408
	ds_read_b128 v[194:197], v166 offset:18432
	ds_read_b128 v[198:201], v166 offset:19456
	ds_read_b128 v[202:205], v166 offset:20480
	ds_read_b128 v[206:209], v166 offset:21504
	ds_read_b128 v[210:213], v166 offset:22528
	ds_read_b128 v[214:217], v166 offset:23552
	global_load_lds_dwordx4 v[160:161], off
	s_add_i32 m0, s55, 0x2000
	s_add_u32 s56, s10, 0x40000
	v_lshl_add_u64 v[218:219], s[10:11], 0, v[144:145]
	s_addc_u32 s57, s11, 0
	s_add_i32 s55, s88, s45
	global_load_lds_dwordx4 v[218:219], off
	v_lshl_add_u64 v[220:221], s[56:57], 0, v[140:141]
	s_mov_b32 m0, s55
	v_lshl_add_u64 v[222:223], s[12:13], 0, v[142:143]
	global_load_lds_dwordx4 v[220:221], off
	v_lshl_add_u64 v[220:221], s[56:57], 0, v[144:145]
	s_add_i32 m0, s55, 0x2000
	s_nop 0
	global_load_lds_dwordx4 v[220:221], off
	v_lshl_add_u64 v[220:221], s[12:13], 0, v[138:139]
	s_mov_b32 m0, s69
	s_nop 0
	global_load_lds_dwordx4 v[220:221], off
	s_mov_b32 m0, s70
	s_nop 0
	global_load_lds_dwordx4 v[222:223], off
	s_waitcnt vmcnt(8)
	s_waitcnt lgkmcnt(0)
	s_barrier
	s_setprio 1
	s_waitcnt lgkmcnt(0)
	v_mfma_f32_16x16x32_bf16 v[102:105], v[74:77], v[186:189], v[102:105]
	v_mfma_f32_16x16x32_bf16 v[98:101], v[152:155], v[186:189], v[98:101]
	v_mfma_f32_16x16x32_bf16 v[94:97], v[74:77], v[194:197], v[94:97]
	v_mfma_f32_16x16x32_bf16 v[90:93], v[152:155], v[194:197], v[90:93]
	v_mfma_f32_16x16x32_bf16 v[86:89], v[74:77], v[202:205], v[86:89]
	v_mfma_f32_16x16x32_bf16 v[82:85], v[152:155], v[202:205], v[82:85]
	v_mfma_f32_16x16x32_bf16 v[70:73], v[74:77], v[210:213], v[70:73]
	v_mfma_f32_16x16x32_bf16 v[66:69], v[152:155], v[210:213], v[66:69]
	v_mfma_f32_16x16x32_bf16 v[102:105], v[78:81], v[190:193], v[102:105]
	v_mfma_f32_16x16x32_bf16 v[98:101], v[156:159], v[190:193], v[98:101]
	v_mfma_f32_16x16x32_bf16 v[94:97], v[78:81], v[198:201], v[94:97]
	v_mfma_f32_16x16x32_bf16 v[90:93], v[156:159], v[198:201], v[90:93]
	v_mfma_f32_16x16x32_bf16 v[86:89], v[78:81], v[206:209], v[86:89]
	v_mfma_f32_16x16x32_bf16 v[82:85], v[156:159], v[206:209], v[82:85]
	v_mfma_f32_16x16x32_bf16 v[70:73], v[78:81], v[214:217], v[70:73]
	v_mfma_f32_16x16x32_bf16 v[66:69], v[156:159], v[214:217], v[66:69]
	s_setprio 0
	s_setprio 1
	v_mfma_f32_16x16x32_bf16 v[30:33], v[170:173], v[186:189], v[30:33]
	v_mfma_f32_16x16x32_bf16 v[26:29], v[178:181], v[186:189], v[26:29]
	v_mfma_f32_16x16x32_bf16 v[22:25], v[170:173], v[194:197], v[22:25]
	v_mfma_f32_16x16x32_bf16 v[18:21], v[178:181], v[194:197], v[18:21]
	v_mfma_f32_16x16x32_bf16 v[14:17], v[170:173], v[202:205], v[14:17]
	v_mfma_f32_16x16x32_bf16 v[10:13], v[178:181], v[202:205], v[10:13]
	v_mfma_f32_16x16x32_bf16 v[6:9], v[170:173], v[210:213], v[6:9]
	v_mfma_f32_16x16x32_bf16 v[2:5], v[178:181], v[210:213], v[2:5]
	v_mfma_f32_16x16x32_bf16 v[30:33], v[174:177], v[190:193], v[30:33]
	v_mfma_f32_16x16x32_bf16 v[26:29], v[182:185], v[190:193], v[26:29]
	v_mfma_f32_16x16x32_bf16 v[22:25], v[174:177], v[198:201], v[22:25]
	v_mfma_f32_16x16x32_bf16 v[18:21], v[182:185], v[198:201], v[18:21]
	v_mfma_f32_16x16x32_bf16 v[14:17], v[174:177], v[206:209], v[14:17]
	v_mfma_f32_16x16x32_bf16 v[10:13], v[182:185], v[206:209], v[10:13]
	v_mfma_f32_16x16x32_bf16 v[6:9], v[174:177], v[214:217], v[6:9]
	v_mfma_f32_16x16x32_bf16 v[2:5], v[182:185], v[214:217], v[2:5]
	s_setprio 0
	s_barrier
; #define PG8_STAGE_A(bufoff, kbase, h, gv) do { if constexpr (GATHER) { PG8_STAGE(bufoff, kbase, (gv)[h]); } else { PG8_STAGE(bufoff, (kbase) + (h) * hstep, voffA); } } while (0)
; #define PG8_WAIT_V(n) asm volatile("s_waitcnt vmcnt(" #n ")" ::: "memory")
; #define PG8_WAIT_L(n) asm volatile("s_waitcnt lgkmcnt(" #n ")" ::: "memory")
; #define PG8_BAR __builtin_amdgcn_s_barrier()
; #define PG8_SCHED __builtin_amdgcn_sched_barrier(0)
; template <class Epi, class Sched, bool ALIGN_EPI = false, bool SP2 = false, bool FP8 = false, bool GATHER = false>
; __device__ __forceinline__ void gemm_phase(PG8_LAS unsigned char* lds, const Gemm g, const Sched& S, const Epi& E) {
;     ...
;             PG8_LDB(B0, 1, 0); PG8_LDB(B1, 1, 1); PG8_SCHED; PG8_LDA(At, 1, 0); PG8_STAGE_A(PG8_SA(0, 1), a2, 1, gsel);
;             PG8_WAIT_V(8); PG8_WAIT_L(0); PG8_BAR; PG8_MMA(0, 0, At, B0); PG8_MMA(0, 1, At, B1); PG8_BAR; PG8_SCHED;
	s_add_i32 s55, 0, 0x18000
	s_add_i32 s56, 0, 0x1c000
	v_add_u32_e32 v156, s55, v163
	v_add_u32_e32 v182, s56, v163
	ds_read_b128 v[74:77], v156
	ds_read_b128 v[78:81], v156 offset:1024
	ds_read_b128 v[152:155], v156 offset:2048
	ds_read_b128 v[156:159], v156 offset:3072
	ds_read_b128 v[170:173], v182
	ds_read_b128 v[174:177], v182 offset:1024
	ds_read_b128 v[178:181], v182 offset:2048
	ds_read_b128 v[182:185], v182 offset:3072
	s_add_u32 s12, s12, 0x40000
	s_addc_u32 s13, s13, 0
	s_mov_b32 m0, s71
	v_lshl_add_u64 v[224:225], s[12:13], 0, v[138:139]
	ds_read_b128 v[186:189], v166 offset:32768
	ds_read_b128 v[190:193], v166 offset:33792
	ds_read_b128 v[194:197], v166 offset:34816
	ds_read_b128 v[198:201], v166 offset:35840
	ds_read_b128 v[202:205], v166 offset:36864
	ds_read_b128 v[206:209], v166 offset:37888
	ds_read_b128 v[210:213], v166 offset:38912
	ds_read_b128 v[214:217], v166 offset:39936
	global_load_lds_dwordx4 v[224:225], off
	v_lshl_add_u64 v[224:225], s[12:13], 0, v[142:143]
	s_mov_b32 m0, s72
	s_nop 0
	global_load_lds_dwordx4 v[224:225], off
	s_waitcnt vmcnt(8)
	s_waitcnt lgkmcnt(0)
	s_barrier
	s_setprio 1
	s_waitcnt lgkmcnt(0)
	v_mfma_f32_16x16x32_bf16 v[134:137], v[74:77], v[186:189], v[134:137]
	v_mfma_f32_16x16x32_bf16 v[130:133], v[152:155], v[186:189], v[130:133]
	v_mfma_f32_16x16x32_bf16 v[126:129], v[74:77], v[194:197], v[126:129]
	v_mfma_f32_16x16x32_bf16 v[122:125], v[152:155], v[194:197], v[122:125]
	v_mfma_f32_16x16x32_bf16 v[118:121], v[74:77], v[202:205], v[118:121]
	v_mfma_f32_16x16x32_bf16 v[114:117], v[152:155], v[202:205], v[114:117]
	v_mfma_f32_16x16x32_bf16 v[110:113], v[74:77], v[210:213], v[110:113]
	v_mfma_f32_16x16x32_bf16 v[106:109], v[152:155], v[210:213], v[106:109]
	v_mfma_f32_16x16x32_bf16 v[134:137], v[78:81], v[190:193], v[134:137]
	v_mfma_f32_16x16x32_bf16 v[130:133], v[156:159], v[190:193], v[130:133]
	v_mfma_f32_16x16x32_bf16 v[126:129], v[78:81], v[198:201], v[126:129]
	v_mfma_f32_16x16x32_bf16 v[122:125], v[156:159], v[198:201], v[122:125]
	v_mfma_f32_16x16x32_bf16 v[118:121], v[78:81], v[206:209], v[118:121]
	v_mfma_f32_16x16x32_bf16 v[114:117], v[156:159], v[206:209], v[114:117]
	v_mfma_f32_16x16x32_bf16 v[110:113], v[78:81], v[214:217], v[110:113]
	v_mfma_f32_16x16x32_bf16 v[106:109], v[156:159], v[214:217], v[106:109]
	s_setprio 0
	s_setprio 1
	v_mfma_f32_16x16x32_bf16 v[62:65], v[170:173], v[186:189], v[62:65]
	v_mfma_f32_16x16x32_bf16 v[58:61], v[178:181], v[186:189], v[58:61]
	v_mfma_f32_16x16x32_bf16 v[54:57], v[170:173], v[194:197], v[54:57]
	v_mfma_f32_16x16x32_bf16 v[50:53], v[178:181], v[194:197], v[50:53]
	v_mfma_f32_16x16x32_bf16 v[46:49], v[170:173], v[202:205], v[46:49]
	v_mfma_f32_16x16x32_bf16 v[42:45], v[178:181], v[202:205], v[42:45]
	v_mfma_f32_16x16x32_bf16 v[38:41], v[170:173], v[210:213], v[38:41]
	v_mfma_f32_16x16x32_bf16 v[34:37], v[178:181], v[210:213], v[34:37]
	v_mfma_f32_16x16x32_bf16 v[62:65], v[174:177], v[190:193], v[62:65]
	v_mfma_f32_16x16x32_bf16 v[58:61], v[182:185], v[190:193], v[58:61]
	v_mfma_f32_16x16x32_bf16 v[54:57], v[174:177], v[198:201], v[54:57]
	v_mfma_f32_16x16x32_bf16 v[50:53], v[182:185], v[198:201], v[50:53]
	v_mfma_f32_16x16x32_bf16 v[46:49], v[174:177], v[206:209], v[46:49]
	v_mfma_f32_16x16x32_bf16 v[42:45], v[182:185], v[206:209], v[42:45]
	v_mfma_f32_16x16x32_bf16 v[38:41], v[174:177], v[214:217], v[38:41]
	v_mfma_f32_16x16x32_bf16 v[34:37], v[182:185], v[214:217], v[34:37]
	s_setprio 0
	s_barrier
; #define PG8_STAGE(bufoff, gbase, voff) do { _Pragma("unroll") for (int _i = 0; _i < 2; ++_i) \
;         __builtin_amdgcn_global_load_lds((const unsigned*)((const char*)(gbase) + (voff)[_i]), (PG8_LAS unsigned*)(lds + (bufoff) + ldsw + _i * 8192), 16, 0, 0); } while (0)
; #define PG8_STAGE_A(bufoff, kbase, h, gv) do { if constexpr (GATHER) { PG8_STAGE(bufoff, kbase, (gv)[h]); } else { PG8_STAGE(bufoff, (kbase) + (h) * hstep, voffA); } } while (0)
; #define PG8_WAIT_V(n) asm volatile("s_waitcnt vmcnt(" #n ")" ::: "memory")
; #define PG8_WAIT_L(n) asm volatile("s_waitcnt lgkmcnt(" #n ")" ::: "memory")
; #define PG8_BAR __builtin_amdgcn_s_barrier()
; #define PG8_SCHED __builtin_amdgcn_sched_barrier(0)
; template <class Epi, class Sched, bool ALIGN_EPI = false, bool SP2 = false, bool FP8 = false, bool GATHER = false>
; __device__ __forceinline__ void gemm_phase(PG8_LAS unsigned char* lds, const Gemm g, const Sched& S, const Epi& E) {
;     ...
;             PG8_LDA(At, 1, 1); PG8_STAGE(PG8_SB(1, 0), b3, voffB); PG8_STAGE(PG8_SB(1, 1), b3 + hstep, voffB); PG8_STAGE_A(PG8_SA(1, 0), a3, 0, gsel);
;             PG8_WAIT_V(8); PG8_WAIT_L(0); PG8_BAR; PG8_MMA(1, 0, At, B0); PG8_MMA(1, 1, At, B1); PG8_BAR; PG8_SCHED;
;     ...
;         if constexpr (ALIGN_EPI) { if (wr == 0) PG8_BAR; }
	s_add_i32 s12, s55, s45
	v_lshl_add_u64 v[160:161], v[160:161], 0, s[28:29]
	s_mov_b32 m0, s12
	ds_read_b128 v[186:189], v166 offset:49152
	ds_read_b128 v[190:193], v166 offset:50176
	ds_read_b128 v[194:197], v166 offset:51200
	ds_read_b128 v[198:201], v166 offset:52224
	ds_read_b128 v[202:205], v166 offset:53248
	ds_read_b128 v[206:209], v166 offset:54272
	ds_read_b128 v[210:213], v166 offset:55296
	ds_read_b128 v[214:217], v166 offset:56320
	global_load_lds_dwordx4 v[160:161], off
	s_add_i32 m0, s12, 0x2000
	s_add_u32 s10, s10, 0x40080
	v_lshl_add_u64 v[160:161], v[218:219], 0, s[28:29]
	s_addc_u32 s11, s11, 0
	s_add_i32 s12, s56, s45
	global_load_lds_dwordx4 v[160:161], off
	v_lshl_add_u64 v[160:161], s[10:11], 0, v[140:141]
	s_mov_b32 m0, s12
	s_nop 0
	global_load_lds_dwordx4 v[160:161], off
	v_lshl_add_u64 v[160:161], s[10:11], 0, v[144:145]
	s_add_i32 m0, s12, 0x2000
	s_nop 0
	global_load_lds_dwordx4 v[160:161], off
	v_lshl_add_u64 v[160:161], v[220:221], 0, s[28:29]
	s_mov_b32 m0, s79
	s_nop 0
	global_load_lds_dwordx4 v[160:161], off
	v_lshl_add_u64 v[160:161], v[222:223], 0, s[28:29]
	s_mov_b32 m0, s80
	s_nop 0
	global_load_lds_dwordx4 v[160:161], off
	s_waitcnt vmcnt(8)
	s_waitcnt lgkmcnt(0)
	s_barrier
	s_setprio 1
	s_waitcnt lgkmcnt(0)
	v_mfma_f32_16x16x32_bf16 v[102:105], v[74:77], v[186:189], v[102:105]
	v_mfma_f32_16x16x32_bf16 v[98:101], v[152:155], v[186:189], v[98:101]
	v_mfma_f32_16x16x32_bf16 v[94:97], v[74:77], v[194:197], v[94:97]
	v_mfma_f32_16x16x32_bf16 v[90:93], v[152:155], v[194:197], v[90:93]
	v_mfma_f32_16x16x32_bf16 v[86:89], v[74:77], v[202:205], v[86:89]
	v_mfma_f32_16x16x32_bf16 v[82:85], v[152:155], v[202:205], v[82:85]
	v_mfma_f32_16x16x32_bf16 v[70:73], v[74:77], v[210:213], v[70:73]
	v_mfma_f32_16x16x32_bf16 v[66:69], v[152:155], v[210:213], v[66:69]
	v_mfma_f32_16x16x32_bf16 v[102:105], v[78:81], v[190:193], v[102:105]
	v_mfma_f32_16x16x32_bf16 v[98:101], v[156:159], v[190:193], v[98:101]
	v_mfma_f32_16x16x32_bf16 v[94:97], v[78:81], v[198:201], v[94:97]
	v_mfma_f32_16x16x32_bf16 v[90:93], v[156:159], v[198:201], v[90:93]
	v_mfma_f32_16x16x32_bf16 v[86:89], v[78:81], v[206:209], v[86:89]
	v_mfma_f32_16x16x32_bf16 v[82:85], v[156:159], v[206:209], v[82:85]
	v_mfma_f32_16x16x32_bf16 v[70:73], v[78:81], v[214:217], v[70:73]
	v_mfma_f32_16x16x32_bf16 v[66:69], v[156:159], v[214:217], v[66:69]
	s_setprio 0
	s_setprio 1
	v_mfma_f32_16x16x32_bf16 v[30:33], v[170:173], v[186:189], v[30:33]
	v_mfma_f32_16x16x32_bf16 v[26:29], v[178:181], v[186:189], v[26:29]
	v_mfma_f32_16x16x32_bf16 v[22:25], v[170:173], v[194:197], v[22:25]
	v_mfma_f32_16x16x32_bf16 v[18:21], v[178:181], v[194:197], v[18:21]
	v_mfma_f32_16x16x32_bf16 v[14:17], v[170:173], v[202:205], v[14:17]
	v_mfma_f32_16x16x32_bf16 v[10:13], v[178:181], v[202:205], v[10:13]
	v_mfma_f32_16x16x32_bf16 v[6:9], v[170:173], v[210:213], v[6:9]
	v_mfma_f32_16x16x32_bf16 v[2:5], v[178:181], v[210:213], v[2:5]
	v_mfma_f32_16x16x32_bf16 v[30:33], v[174:177], v[190:193], v[30:33]
	v_mfma_f32_16x16x32_bf16 v[26:29], v[182:185], v[190:193], v[26:29]
	v_mfma_f32_16x16x32_bf16 v[22:25], v[174:177], v[198:201], v[22:25]
	v_mfma_f32_16x16x32_bf16 v[18:21], v[182:185], v[198:201], v[18:21]
	v_mfma_f32_16x16x32_bf16 v[14:17], v[174:177], v[206:209], v[14:17]
	v_mfma_f32_16x16x32_bf16 v[10:13], v[182:185], v[206:209], v[10:13]
	v_mfma_f32_16x16x32_bf16 v[6:9], v[174:177], v[214:217], v[6:9]
	v_mfma_f32_16x16x32_bf16 v[2:5], v[182:185], v[214:217], v[2:5]
	s_setprio 0
	s_add_i32 s47, s47, 2
	s_add_u32 s8, s8, 0x100
	s_addc_u32 s9, s9, 0
	s_add_u32 s17, s17, 0x100
	s_addc_u32 s18, s18, 0
	s_cmp_gt_u32 s47, 13
	s_cbranch_scc0 .LBB0_1128
	s_barrier
	s_and_b64 vcc, exec, s[30:31]
	s_cbranch_vccz .LBB0_1131
	s_barrier

; #define PG8_STAGE(bufoff, gbase, voff) do { _Pragma("unroll") for (int _i = 0; _i < 2; ++_i) \
;         __builtin_amdgcn_global_load_lds((const unsigned*)((const char*)(gbase) + (voff)[_i]), (PG8_LAS unsigned*)(lds + (bufoff) + ldsw + _i * 8192), 16, 0, 0); } while (0)
; #define PG8_STAGE_A(bufoff, kbase, h, gv) do { if constexpr (GATHER) { PG8_STAGE(bufoff, kbase, (gv)[h]); } else { PG8_STAGE(bufoff, (kbase) + (h) * hstep, voffA); } } while (0)
; #define PG8_WAIT_V(n) asm volatile("s_waitcnt vmcnt(" #n ")" ::: "memory")
; #define PG8_WAIT_L(n) asm volatile("s_waitcnt lgkmcnt(" #n ")" ::: "memory")
; #define PG8_BAR __builtin_amdgcn_s_barrier()
; #define PG8_SCHED __builtin_amdgcn_sched_barrier(0)
; template <class Epi, class Sched, bool ALIGN_EPI = false, bool SP2 = false, bool FP8 = false, bool GATHER = false>
; __device__ __forceinline__ void gemm_phase(PG8_LAS unsigned char* lds, const Gemm g, const Sched& S, const Epi& E) {
;     ...
;             PG8_LDB(B0, 0, 0); PG8_LDB(B1, 0, 1); PG8_SCHED; PG8_LDA(At, 0, 0); PG8_STAGE_A(PG8_SA(1, 1), a1, 1, gcur);
;             PG8_WAIT_V(8); PG8_WAIT_L(0); PG8_BAR; PG8_MMA(0, 0, At, B0); PG8_MMA(0, 1, At, B1); PG8_BAR; PG8_SCHED;
;             PG8_LDA(At, 0, 1); PG8_STAGE(PG8_SB(0, 0), b2, voffB); PG8_STAGE(PG8_SB(0, 1), b2 + hstep, voffB); PG8_STAGE_A(PG8_SA(0, 0), a2, 0, gsel);
.LBB0_1497:
	v_add_u32_e32 v136, s79, v169
	ds_read_b128 v[124:127], v136
	ds_read_b128 v[128:131], v136 offset:1024
	ds_read_b128 v[132:135], v136 offset:2048
	ds_read_b128 v[164:167], v136 offset:3072
	v_add_u32_e32 v136, s80, v169
	ds_read_b128 v[172:175], v136
	ds_read_b128 v[176:179], v136 offset:1024
	ds_read_b128 v[180:183], v136 offset:2048
	ds_read_b128 v[184:187], v136 offset:3072
	s_add_u32 s58, s54, 0xfffc0080
	s_addc_u32 s59, s55, -1
	s_and_b64 s[56:57], s[56:57], exec
	s_cselect_b32 s59, s59, s45
	s_cselect_b32 s58, s58, s82
	s_cselect_b32 s57, s85, s83
	s_cselect_b32 s56, s53, s84
	v_lshl_add_u64 v[136:137], s[54:55], 0, v[154:155]
	s_add_i32 m0, s51, 0xc000
	ds_read_b128 v[188:191], v170
	ds_read_b128 v[192:195], v170 offset:1024
	ds_read_b128 v[196:199], v170 offset:2048
	ds_read_b128 v[200:203], v170 offset:3072
	ds_read_b128 v[204:207], v170 offset:4096
	ds_read_b128 v[208:211], v170 offset:5120
	ds_read_b128 v[212:215], v170 offset:6144
	ds_read_b128 v[216:219], v170 offset:7168
	global_load_lds_dwordx4 v[136:137], off
	v_lshl_add_u64 v[136:137], s[54:55], 0, v[156:157]
	s_add_i32 m0, s51, 0xe000
	s_nop 0
	global_load_lds_dwordx4 v[136:137], off
	s_waitcnt vmcnt(8)
	s_waitcnt lgkmcnt(0)
	s_barrier
	s_setprio 1
	s_waitcnt lgkmcnt(0)
	v_mfma_f32_16x16x32_bf16 v[142:145], v[124:127], v[188:191], v[142:145]
	v_mfma_f32_16x16x32_bf16 v[136:139], v[132:135], v[188:191], v[138:141]
	v_mfma_f32_16x16x32_bf16 v[118:121], v[124:127], v[196:199], v[118:121]
	v_mfma_f32_16x16x32_bf16 v[106:109], v[132:135], v[196:199], v[106:109]
	v_mfma_f32_16x16x32_bf16 v[102:105], v[124:127], v[204:207], v[102:105]
	v_mfma_f32_16x16x32_bf16 v[90:93], v[132:135], v[204:207], v[90:93]
	v_mfma_f32_16x16x32_bf16 v[86:89], v[124:127], v[212:215], v[86:89]
	v_mfma_f32_16x16x32_bf16 v[74:77], v[132:135], v[212:215], v[74:77]
	v_mfma_f32_16x16x32_bf16 v[142:145], v[128:131], v[192:195], v[142:145]
	v_mfma_f32_16x16x32_bf16 v[136:139], v[164:167], v[192:195], v[136:139]
	v_mfma_f32_16x16x32_bf16 v[118:121], v[128:131], v[200:203], v[118:121]
	v_mfma_f32_16x16x32_bf16 v[106:109], v[164:167], v[200:203], v[106:109]
	v_mfma_f32_16x16x32_bf16 v[102:105], v[128:131], v[208:211], v[102:105]
	v_mfma_f32_16x16x32_bf16 v[90:93], v[164:167], v[208:211], v[90:93]
	v_mfma_f32_16x16x32_bf16 v[86:89], v[128:131], v[216:219], v[86:89]
	v_mfma_f32_16x16x32_bf16 v[74:77], v[164:167], v[216:219], v[74:77]
	s_setprio 0
	s_setprio 1
	v_mfma_f32_16x16x32_bf16 v[114:117], v[172:175], v[188:191], v[114:117]
	v_mfma_f32_16x16x32_bf16 v[110:113], v[180:183], v[188:191], v[110:113]
	v_mfma_f32_16x16x32_bf16 v[98:101], v[172:175], v[196:199], v[98:101]
	v_mfma_f32_16x16x32_bf16 v[94:97], v[180:183], v[196:199], v[94:97]
	v_mfma_f32_16x16x32_bf16 v[82:85], v[172:175], v[204:207], v[82:85]
	v_mfma_f32_16x16x32_bf16 v[78:81], v[180:183], v[204:207], v[78:81]
	v_mfma_f32_16x16x32_bf16 v[70:73], v[172:175], v[212:215], v[70:73]
	v_mfma_f32_16x16x32_bf16 v[66:69], v[180:183], v[212:215], v[66:69]
	v_mfma_f32_16x16x32_bf16 v[114:117], v[176:179], v[192:195], v[114:117]
	v_mfma_f32_16x16x32_bf16 v[110:113], v[184:187], v[192:195], v[110:113]
	v_mfma_f32_16x16x32_bf16 v[98:101], v[176:179], v[200:203], v[98:101]
	v_mfma_f32_16x16x32_bf16 v[94:97], v[184:187], v[200:203], v[94:97]
	v_mfma_f32_16x16x32_bf16 v[82:85], v[176:179], v[208:211], v[82:85]
	v_mfma_f32_16x16x32_bf16 v[78:81], v[184:187], v[208:211], v[78:81]
	v_mfma_f32_16x16x32_bf16 v[70:73], v[176:179], v[216:219], v[70:73]
	v_mfma_f32_16x16x32_bf16 v[66:69], v[184:187], v[216:219], v[66:69]
	s_setprio 0
	s_barrier
	s_add_i32 s87, s79, s66
	v_lshl_add_u64 v[220:221], s[56:57], 0, v[148:149]
	s_mov_b32 m0, s87
	ds_read_b128 v[188:191], v170 offset:16384
	ds_read_b128 v[192:195], v170 offset:17408
	ds_read_b128 v[196:199], v170 offset:18432
	ds_read_b128 v[200:203], v170 offset:19456
	ds_read_b128 v[204:207], v170 offset:20480
	ds_read_b128 v[208:211], v170 offset:21504
	ds_read_b128 v[212:215], v170 offset:22528
	ds_read_b128 v[216:219], v170 offset:23552
	global_load_lds_dwordx4 v[220:221], off
	s_add_i32 m0, s87, 0x2000
	s_add_u32 s88, s56, 0x40000
	v_lshl_add_u64 v[222:223], s[56:57], 0, v[152:153]
	s_addc_u32 s89, s57, 0
	s_add_i32 s87, s80, s66
	global_load_lds_dwordx4 v[222:223], off
	v_lshl_add_u64 v[140:141], s[88:89], 0, v[148:149]
	s_mov_b32 m0, s87
	v_lshl_add_u64 v[224:225], s[58:59], 0, v[146:147]
	global_load_lds_dwordx4 v[140:141], off
	v_lshl_add_u64 v[140:141], s[88:89], 0, v[152:153]
	s_add_i32 m0, s87, 0x2000
	v_lshl_add_u64 v[226:227], s[58:59], 0, v[150:151]
	global_load_lds_dwordx4 v[140:141], off
	s_mov_b32 m0, s51
	s_nop 0
	global_load_lds_dwordx4 v[224:225], off
	s_mov_b32 m0, s67
	s_nop 0
	global_load_lds_dwordx4 v[226:227], off
	s_waitcnt vmcnt(8)
	s_waitcnt lgkmcnt(0)
	s_barrier
; #define PG8_STAGE_A(bufoff, kbase, h, gv) do { if constexpr (GATHER) { PG8_STAGE(bufoff, kbase, (gv)[h]); } else { PG8_STAGE(bufoff, (kbase) + (h) * hstep, voffA); } } while (0)
; #define PG8_WAIT_V(n) asm volatile("s_waitcnt vmcnt(" #n ")" ::: "memory")
; #define PG8_WAIT_L(n) asm volatile("s_waitcnt lgkmcnt(" #n ")" ::: "memory")
; #define PG8_BAR __builtin_amdgcn_s_barrier()
; #define PG8_SCHED __builtin_amdgcn_sched_barrier(0)
; template <class Epi, class Sched, bool ALIGN_EPI = false, bool SP2 = false, bool FP8 = false, bool GATHER = false>
; __device__ __forceinline__ void gemm_phase(PG8_LAS unsigned char* lds, const Gemm g, const Sched& S, const Epi& E) {
;     ...
;             PG8_WAIT_V(8); PG8_WAIT_L(0); PG8_BAR; PG8_MMA(1, 0, At, B0); PG8_MMA(1, 1, At, B1); PG8_BAR; PG8_SCHED;
;             PG8_LDB(B0, 1, 0); PG8_LDB(B1, 1, 1); PG8_SCHED; PG8_LDA(At, 1, 0); PG8_STAGE_A(PG8_SA(0, 1), a2, 1, gsel);
;             PG8_WAIT_V(8); PG8_WAIT_L(0); PG8_BAR; PG8_MMA(0, 0, At, B0); PG8_MMA(0, 1, At, B1); PG8_BAR; PG8_SCHED;
	s_setprio 1
	s_waitcnt lgkmcnt(0)
	v_mfma_f32_16x16x32_bf16 v[62:65], v[124:127], v[188:191], v[62:65]
	v_mfma_f32_16x16x32_bf16 v[58:61], v[132:135], v[188:191], v[58:61]
	v_mfma_f32_16x16x32_bf16 v[54:57], v[124:127], v[196:199], v[54:57]
	v_mfma_f32_16x16x32_bf16 v[42:45], v[132:135], v[196:199], v[42:45]
	v_mfma_f32_16x16x32_bf16 v[38:41], v[124:127], v[204:207], v[38:41]
	v_mfma_f32_16x16x32_bf16 v[26:29], v[132:135], v[204:207], v[26:29]
	v_mfma_f32_16x16x32_bf16 v[22:25], v[124:127], v[212:215], v[22:25]
	v_mfma_f32_16x16x32_bf16 v[10:13], v[132:135], v[212:215], v[10:13]
	v_mfma_f32_16x16x32_bf16 v[62:65], v[128:131], v[192:195], v[62:65]
	v_mfma_f32_16x16x32_bf16 v[58:61], v[164:167], v[192:195], v[58:61]
	v_mfma_f32_16x16x32_bf16 v[54:57], v[128:131], v[200:203], v[54:57]
	v_mfma_f32_16x16x32_bf16 v[42:45], v[164:167], v[200:203], v[42:45]
	v_mfma_f32_16x16x32_bf16 v[38:41], v[128:131], v[208:211], v[38:41]
	v_mfma_f32_16x16x32_bf16 v[26:29], v[164:167], v[208:211], v[26:29]
	v_mfma_f32_16x16x32_bf16 v[22:25], v[128:131], v[216:219], v[22:25]
	v_mfma_f32_16x16x32_bf16 v[10:13], v[164:167], v[216:219], v[10:13]
	s_setprio 0
	s_setprio 1
	v_mfma_f32_16x16x32_bf16 v[50:53], v[172:175], v[188:191], v[50:53]
	v_mfma_f32_16x16x32_bf16 v[46:49], v[180:183], v[188:191], v[46:49]
	v_mfma_f32_16x16x32_bf16 v[34:37], v[172:175], v[196:199], v[34:37]
	v_mfma_f32_16x16x32_bf16 v[30:33], v[180:183], v[196:199], v[30:33]
	v_mfma_f32_16x16x32_bf16 v[18:21], v[172:175], v[204:207], v[18:21]
	v_mfma_f32_16x16x32_bf16 v[14:17], v[180:183], v[204:207], v[14:17]
	v_mfma_f32_16x16x32_bf16 v[6:9], v[172:175], v[212:215], v[6:9]
	v_mfma_f32_16x16x32_bf16 v[2:5], v[180:183], v[212:215], v[2:5]
	v_mfma_f32_16x16x32_bf16 v[50:53], v[176:179], v[192:195], v[50:53]
	v_mfma_f32_16x16x32_bf16 v[46:49], v[184:187], v[192:195], v[46:49]
	v_mfma_f32_16x16x32_bf16 v[34:37], v[176:179], v[200:203], v[34:37]
	v_mfma_f32_16x16x32_bf16 v[30:33], v[184:187], v[200:203], v[30:33]
	v_mfma_f32_16x16x32_bf16 v[18:21], v[176:179], v[208:211], v[18:21]
	v_mfma_f32_16x16x32_bf16 v[14:17], v[184:187], v[208:211], v[14:17]
	v_mfma_f32_16x16x32_bf16 v[6:9], v[176:179], v[216:219], v[6:9]
	v_mfma_f32_16x16x32_bf16 v[2:5], v[184:187], v[216:219], v[2:5]
	s_setprio 0
	s_barrier
	s_add_i32 s87, 0, 0x18000
	v_add_u32_e32 v140, s87, v169
	s_add_i32 s88, 0, 0x1c000
	ds_read_b128 v[124:127], v140
	ds_read_b128 v[128:131], v140 offset:1024
	ds_read_b128 v[132:135], v140 offset:2048
	ds_read_b128 v[164:167], v140 offset:3072
	v_add_u32_e32 v140, s88, v169
	ds_read_b128 v[172:175], v140
	ds_read_b128 v[176:179], v140 offset:1024
	ds_read_b128 v[180:183], v140 offset:2048
	ds_read_b128 v[184:187], v140 offset:3072
	s_add_u32 s58, s58, 0x40000
	s_addc_u32 s59, s59, 0
	s_mov_b32 m0, s68
	v_lshl_add_u64 v[140:141], s[58:59], 0, v[146:147]
	ds_read_b128 v[188:191], v170 offset:32768
	ds_read_b128 v[192:195], v170 offset:33792
	ds_read_b128 v[196:199], v170 offset:34816
	ds_read_b128 v[200:203], v170 offset:35840
	ds_read_b128 v[204:207], v170 offset:36864
	ds_read_b128 v[208:211], v170 offset:37888
	ds_read_b128 v[212:215], v170 offset:38912
	ds_read_b128 v[216:219], v170 offset:39936
	global_load_lds_dwordx4 v[140:141], off
	v_lshl_add_u64 v[140:141], s[58:59], 0, v[150:151]
	s_mov_b32 m0, s69
	s_nop 0
	global_load_lds_dwordx4 v[140:141], off
	s_waitcnt vmcnt(8)
	s_waitcnt lgkmcnt(0)
	s_barrier
	s_setprio 1
	s_waitcnt lgkmcnt(0)
	v_mfma_f32_16x16x32_bf16 v[140:143], v[124:127], v[188:191], v[142:145]
	v_mfma_f32_16x16x32_bf16 v[136:139], v[132:135], v[188:191], v[136:139]
	v_mfma_f32_16x16x32_bf16 v[118:121], v[124:127], v[196:199], v[118:121]
	v_mfma_f32_16x16x32_bf16 v[106:109], v[132:135], v[196:199], v[106:109]
	v_mfma_f32_16x16x32_bf16 v[102:105], v[124:127], v[204:207], v[102:105]
	v_mfma_f32_16x16x32_bf16 v[90:93], v[132:135], v[204:207], v[90:93]
	v_mfma_f32_16x16x32_bf16 v[86:89], v[124:127], v[212:215], v[86:89]
	v_mfma_f32_16x16x32_bf16 v[74:77], v[132:135], v[212:215], v[74:77]
	v_mfma_f32_16x16x32_bf16 v[142:145], v[128:131], v[192:195], v[140:143]
	v_mfma_f32_16x16x32_bf16 v[138:141], v[164:167], v[192:195], v[136:139]
	v_mfma_f32_16x16x32_bf16 v[118:121], v[128:131], v[200:203], v[118:121]
	v_mfma_f32_16x16x32_bf16 v[106:109], v[164:167], v[200:203], v[106:109]
	v_mfma_f32_16x16x32_bf16 v[102:105], v[128:131], v[208:211], v[102:105]
	v_mfma_f32_16x16x32_bf16 v[90:93], v[164:167], v[208:211], v[90:93]
	v_mfma_f32_16x16x32_bf16 v[86:89], v[128:131], v[216:219], v[86:89]
	v_mfma_f32_16x16x32_bf16 v[74:77], v[164:167], v[216:219], v[74:77]
	s_setprio 0
	s_setprio 1
	v_mfma_f32_16x16x32_bf16 v[114:117], v[172:175], v[188:191], v[114:117]
	v_mfma_f32_16x16x32_bf16 v[110:113], v[180:183], v[188:191], v[110:113]
	v_mfma_f32_16x16x32_bf16 v[98:101], v[172:175], v[196:199], v[98:101]
	v_mfma_f32_16x16x32_bf16 v[94:97], v[180:183], v[196:199], v[94:97]
	v_mfma_f32_16x16x32_bf16 v[82:85], v[172:175], v[204:207], v[82:85]
	v_mfma_f32_16x16x32_bf16 v[78:81], v[180:183], v[204:207], v[78:81]
	v_mfma_f32_16x16x32_bf16 v[70:73], v[172:175], v[212:215], v[70:73]
	v_mfma_f32_16x16x32_bf16 v[66:69], v[180:183], v[212:215], v[66:69]
	v_mfma_f32_16x16x32_bf16 v[114:117], v[176:179], v[192:195], v[114:117]
	v_mfma_f32_16x16x32_bf16 v[110:113], v[184:187], v[192:195], v[110:113]
	v_mfma_f32_16x16x32_bf16 v[98:101], v[176:179], v[200:203], v[98:101]
	v_mfma_f32_16x16x32_bf16 v[94:97], v[184:187], v[200:203], v[94:97]
	v_mfma_f32_16x16x32_bf16 v[82:85], v[176:179], v[208:211], v[82:85]
	v_mfma_f32_16x16x32_bf16 v[78:81], v[184:187], v[208:211], v[78:81]
	v_mfma_f32_16x16x32_bf16 v[70:73], v[176:179], v[216:219], v[70:73]
	v_mfma_f32_16x16x32_bf16 v[66:69], v[184:187], v[216:219], v[66:69]
	s_setprio 0
	s_barrier
; #define PG8_STAGE(bufoff, gbase, voff) do { _Pragma("unroll") for (int _i = 0; _i < 2; ++_i) \
;         __builtin_amdgcn_global_load_lds((const unsigned*)((const char*)(gbase) + (voff)[_i]), (PG8_LAS unsigned*)(lds + (bufoff) + ldsw + _i * 8192), 16, 0, 0); } while (0)
; #define PG8_STAGE_A(bufoff, kbase, h, gv) do { if constexpr (GATHER) { PG8_STAGE(bufoff, kbase, (gv)[h]); } else { PG8_STAGE(bufoff, (kbase) + (h) * hstep, voffA); } } while (0)
; #define PG8_WAIT_V(n) asm volatile("s_waitcnt vmcnt(" #n ")" ::: "memory")
; #define PG8_WAIT_L(n) asm volatile("s_waitcnt lgkmcnt(" #n ")" ::: "memory")
; #define PG8_BAR __builtin_amdgcn_s_barrier()
; #define PG8_SCHED __builtin_amdgcn_sched_barrier(0)
; template <class Epi, class Sched, bool ALIGN_EPI = false, bool SP2 = false, bool FP8 = false, bool GATHER = false>
; __device__ __forceinline__ void gemm_phase(PG8_LAS unsigned char* lds, const Gemm g, const Sched& S, const Epi& E) {
;     ...
;             PG8_LDA(At, 1, 1); PG8_STAGE(PG8_SB(1, 0), b3, voffB); PG8_STAGE(PG8_SB(1, 1), b3 + hstep, voffB); PG8_STAGE_A(PG8_SA(1, 0), a3, 0, gsel);
;             PG8_WAIT_V(8); PG8_WAIT_L(0); PG8_BAR; PG8_MMA(1, 0, At, B0); PG8_MMA(1, 1, At, B1); PG8_BAR; PG8_SCHED;
;     __device__ __forceinline__ void pre(const pg8::Unit& u, int wid, int lane) const {
;         if (wid == 0) lds_dma16(gate + (size_t)(u.pm < 256 ? (u.pm >> 4) : 16) * (NMOD * DM) + u.pn * 256 + lane * 4, (unsigned)(uintptr_t)(lds + LDS_EPI)); }
	s_add_i32 s58, s87, s66
	v_lshl_add_u64 v[136:137], v[220:221], 0, s[16:17]
	s_mov_b32 m0, s58
	ds_read_b128 v[188:191], v170 offset:49152
	ds_read_b128 v[192:195], v170 offset:50176
	ds_read_b128 v[196:199], v170 offset:51200
	ds_read_b128 v[200:203], v170 offset:52224
	ds_read_b128 v[204:207], v170 offset:53248
	ds_read_b128 v[208:211], v170 offset:54272
	ds_read_b128 v[212:215], v170 offset:55296
	ds_read_b128 v[216:219], v170 offset:56320
	global_load_lds_dwordx4 v[136:137], off
	s_add_i32 m0, s58, 0x2000
	s_add_u32 s56, s56, 0x40080
	v_lshl_add_u64 v[136:137], v[222:223], 0, s[16:17]
	s_addc_u32 s57, s57, 0
	s_add_i32 s58, s88, s66
	global_load_lds_dwordx4 v[136:137], off
	v_lshl_add_u64 v[136:137], s[56:57], 0, v[148:149]
	s_mov_b32 m0, s58
	s_nop 0
	global_load_lds_dwordx4 v[136:137], off
	v_lshl_add_u64 v[136:137], s[56:57], 0, v[152:153]
	s_add_i32 m0, s58, 0x2000
	s_nop 0
	global_load_lds_dwordx4 v[136:137], off
	v_lshl_add_u64 v[136:137], v[224:225], 0, s[16:17]
	s_mov_b32 m0, s75
	s_nop 0
	global_load_lds_dwordx4 v[136:137], off
	v_lshl_add_u64 v[136:137], v[226:227], 0, s[16:17]
	s_mov_b32 m0, s76
	s_nop 0
	global_load_lds_dwordx4 v[136:137], off
	s_waitcnt vmcnt(8)
	s_waitcnt lgkmcnt(0)
	s_barrier
	s_setprio 1
	s_waitcnt lgkmcnt(0)
	v_mfma_f32_16x16x32_bf16 v[62:65], v[124:127], v[188:191], v[62:65]
	v_mfma_f32_16x16x32_bf16 v[58:61], v[132:135], v[188:191], v[58:61]
	v_mfma_f32_16x16x32_bf16 v[54:57], v[124:127], v[196:199], v[54:57]
	v_mfma_f32_16x16x32_bf16 v[42:45], v[132:135], v[196:199], v[42:45]
	v_mfma_f32_16x16x32_bf16 v[38:41], v[124:127], v[204:207], v[38:41]
	v_mfma_f32_16x16x32_bf16 v[26:29], v[132:135], v[204:207], v[26:29]
	v_mfma_f32_16x16x32_bf16 v[22:25], v[124:127], v[212:215], v[22:25]
	v_mfma_f32_16x16x32_bf16 v[10:13], v[132:135], v[212:215], v[10:13]
	v_mfma_f32_16x16x32_bf16 v[62:65], v[128:131], v[192:195], v[62:65]
	v_mfma_f32_16x16x32_bf16 v[58:61], v[164:167], v[192:195], v[58:61]
	v_mfma_f32_16x16x32_bf16 v[54:57], v[128:131], v[200:203], v[54:57]
	v_mfma_f32_16x16x32_bf16 v[42:45], v[164:167], v[200:203], v[42:45]
	v_mfma_f32_16x16x32_bf16 v[38:41], v[128:131], v[208:211], v[38:41]
	v_mfma_f32_16x16x32_bf16 v[26:29], v[164:167], v[208:211], v[26:29]
	v_mfma_f32_16x16x32_bf16 v[22:25], v[128:131], v[216:219], v[22:25]
	v_mfma_f32_16x16x32_bf16 v[10:13], v[164:167], v[216:219], v[10:13]
	s_setprio 0
	s_setprio 1
	v_mfma_f32_16x16x32_bf16 v[50:53], v[172:175], v[188:191], v[50:53]
	v_mfma_f32_16x16x32_bf16 v[46:49], v[180:183], v[188:191], v[46:49]
	v_mfma_f32_16x16x32_bf16 v[34:37], v[172:175], v[196:199], v[34:37]
	v_mfma_f32_16x16x32_bf16 v[30:33], v[180:183], v[196:199], v[30:33]
	v_mfma_f32_16x16x32_bf16 v[18:21], v[172:175], v[204:207], v[18:21]
	v_mfma_f32_16x16x32_bf16 v[14:17], v[180:183], v[204:207], v[14:17]
	v_mfma_f32_16x16x32_bf16 v[6:9], v[172:175], v[212:215], v[6:9]
	v_mfma_f32_16x16x32_bf16 v[2:5], v[180:183], v[212:215], v[2:5]
	v_mfma_f32_16x16x32_bf16 v[50:53], v[176:179], v[192:195], v[50:53]
	v_mfma_f32_16x16x32_bf16 v[46:49], v[184:187], v[192:195], v[46:49]
	v_mfma_f32_16x16x32_bf16 v[34:37], v[176:179], v[200:203], v[34:37]
	v_mfma_f32_16x16x32_bf16 v[30:33], v[184:187], v[200:203], v[30:33]
	v_mfma_f32_16x16x32_bf16 v[18:21], v[176:179], v[208:211], v[18:21]
	v_mfma_f32_16x16x32_bf16 v[14:17], v[184:187], v[208:211], v[14:17]
	v_mfma_f32_16x16x32_bf16 v[6:9], v[176:179], v[216:219], v[6:9]
	v_mfma_f32_16x16x32_bf16 v[2:5], v[184:187], v[216:219], v[2:5]
	s_setprio 0
	s_add_i32 s86, s86, 2
	s_add_u32 s54, s54, 0x100
	s_addc_u32 s55, s55, 0
	s_add_u32 s53, s53, 0x100
	s_addc_u32 s85, s85, 0
	s_cmp_gt_u32 s86, 13
	s_cbranch_scc1 .Lrot1497_exit
	s_barrier
.LBB0_1498:
	s_cmp_lg_u32 s86, 12
	s_cselect_b64 s[56:57], -1, 0
	s_or_b64 s[58:59], s[56:57], s[18:19]
	s_and_b64 vcc, exec, s[58:59]
	s_cbranch_vccnz .LBB0_1497
	s_add_i32 s58, 0, 0x20000
	s_mov_b32 s59, m0
	s_mov_b32 m0, s58
	s_nop 0
	global_load_lds_dwordx4 v[122:123], off
	s_mov_b32 m0, s59
	s_branch .LBB0_1497
.Lrot1497_exit:
	s_barrier
.LBB0_1500:
	s_and_b64 vcc, exec, s[20:21]
	s_cbranch_vccz .LBB0_1502
	s_barrier

; #define PG8_STAGE(bufoff, gbase, voff) do { _Pragma("unroll") for (int _i = 0; _i < 2; ++_i) \
;         __builtin_amdgcn_global_load_lds((const unsigned*)((const char*)(gbase) + (voff)[_i]), (PG8_LAS unsigned*)(lds + (bufoff) + ldsw + _i * 8192), 16, 0, 0); } while (0)
; #define PG8_STAGE_A(bufoff, kbase, h, gv) do { if constexpr (GATHER) { PG8_STAGE(bufoff, kbase, (gv)[h]); } else { PG8_STAGE(bufoff, (kbase) + (h) * hstep, voffA); } } while (0)
; #define PG8_BAR __builtin_amdgcn_s_barrier()
; template <class Epi, class Sched, bool ALIGN_EPI = false, bool SP2 = false, bool FP8 = false, bool GATHER = false>
; __device__ __forceinline__ void gemm_phase(PG8_LAS unsigned char* lds, const Gemm g, const Sched& S, const Epi& E) {
;     ...
;         for (int t = 0; t < nt; t += 2) {
;             const bool last = (t == nt - 2);
;             const char* a1 = cA + (size_t)(t + 1) * kstep;
;             const char* a2 = last ? nA : cA + (size_t)(t + 2) * kstep; const char* b2 = last ? nB : cB + (size_t)(t + 2) * kstep;
;             const char* a3 = a2 + kstep; const char* b3 = b2 + kstep;
;             if (last && has_next) S.a_ready(nxt);
;             if (last) E.pre(cur, wid, lane);
;             if constexpr (GATHER) { if (t == nt - 4 && has_next) { _Pragma("unroll") for (int h_ = 0; h_ < 2; ++h_) _Pragma("unroll") for (int i_ = 0; i_ < 2; ++i_)
;                 asm volatile("global_load_dword %0, %1, off" : "+v"(graw[h_][i_]) : "v"(S.rowtok + (nxt.pm * BM + h_ * HALF + gR[i_])) : "memory"); } }
;             unsigned gsel[2][2];
;             if constexpr (GATHER) { _Pragma("unroll") for (int h_ = 0; h_ < 2; ++h_) _Pragma("unroll") for (int i_ = 0; i_ < 2; ++i_) { if (last && has_next) gnxt[h_][i_] = graw[h_][i_] * (unsigned)(K * 2) + gC[i_]; gsel[h_][i_] = (last && has_next) ? gnxt[h_][i_] : gcur[h_][i_]; } }
;             if constexpr (SP2) {
;             PG8_LDB(B0, 0, 0); PG8_LDB(B1, 0, 1); PG8_SCHED; PG8_LDA(At, 0, 0); PG8_STAGE_A(PG8_SA(1, 1), a1, 1, gcur);
;             PG8_WAIT_V(8); PG8_WAIT_L(0); PG8_BAR; PG8_MMA(0, 0, At, B0); PG8_MMA(0, 1, At, B1); PG8_BAR; PG8_SCHED;
;             PG8_LDA(At, 0, 1); PG8_STAGE(PG8_SB(0, 0), b2, voffB); PG8_STAGE(PG8_SB(0, 1), b2 + hstep, voffB); PG8_STAGE_A(PG8_SA(0, 0), a2, 0, gsel);
;             PG8_WAIT_V(8); PG8_WAIT_L(0); PG8_BAR; PG8_MMA(1, 0, At, B0); PG8_MMA(1, 1, At, B1); PG8_BAR; PG8_SCHED;
.Lpeel1781_body:
	s_add_u32 s50, s6, s46
	s_addc_u32 s51, s7, s47
	s_add_u32 s52, s50, 0x19200100
	s_addc_u32 s53, s51, 0
	s_and_b64 s[50:51], s[54:55], exec
	s_cselect_b32 s53, s9, s53
	s_cselect_b32 s52, s8, s52
	s_add_u32 s84, s20, s46
	s_addc_u32 s85, s82, s47
	s_and_b64 s[50:51], s[54:55], exec
	s_cselect_b32 s51, s35, s85
	s_cselect_b32 s50, s34, s84
	v_lshl_add_u32 v2, v213, 10, v1
	s_and_b64 vcc, s[44:45], s[54:55]
	v_cndmask_b32_e32 v209, v209, v2, vcc
	v_cndmask_b32_e32 v170, v217, v2, vcc
	v_lshl_add_u32 v2, v214, 10, v204
	v_cndmask_b32_e32 v210, v210, v2, vcc
	v_cndmask_b32_e32 v200, v180, v2, vcc
	v_add_u32_e32 v2, s74, v206
	v_add_u32_e32 v14, s75, v206
	ds_read_b128 v[18:21], v2
	ds_read_b128 v[22:25], v2 offset:1024
	ds_read_b128 v[26:29], v2 offset:2048
	ds_read_b128 v[30:33], v2 offset:3072
	ds_read_b128 v[2:5], v14
	ds_read_b128 v[6:9], v14 offset:1024
	ds_read_b128 v[10:13], v14 offset:2048
	ds_read_b128 v[14:17], v14 offset:3072
	v_lshl_add_u32 v177, v215, 10, v1
	v_lshl_add_u32 v179, v216, 10, v204
	v_cndmask_b32_e32 v211, v211, v177, vcc
	v_cndmask_b32_e32 v212, v212, v179, vcc
	v_cndmask_b32_e32 v177, v178, v177, vcc
	v_cndmask_b32_e32 v179, v176, v179, vcc
	v_lshl_add_u64 v[196:197], v[194:195], 0, s[46:47]
	s_add_i32 m0, s61, 0xc000
	ds_read_b128 v[218:221], v207
	ds_read_b128 v[222:225], v207 offset:1024
	ds_read_b128 v[226:229], v207 offset:2048
	ds_read_b128 v[230:233], v207 offset:3072
	ds_read_b128 v[234:237], v207 offset:4096
	ds_read_b128 v[238:241], v207 offset:5120
	ds_read_b128 v[242:245], v207 offset:6144
	ds_read_b128 v[246:249], v207 offset:7168
	global_load_lds_dwordx4 v[196:197], off
	v_lshl_add_u64 v[196:197], v[192:193], 0, s[46:47]
	s_add_i32 m0, s61, 0xe000
	s_nop 0
	global_load_lds_dwordx4 v[196:197], off
	s_waitcnt vmcnt(8)
	s_waitcnt lgkmcnt(0)
	s_barrier
	s_setprio 1
	s_waitcnt lgkmcnt(0)
	v_mfma_f32_16x16x128_f8f6f4 v[158:161], v[18:25], v[218:225], 0
	v_mfma_f32_16x16x128_f8f6f4 v[150:153], v[26:33], v[218:225], 0
	v_mfma_f32_16x16x128_f8f6f4 v[142:145], v[18:25], v[226:233], 0
	v_mfma_f32_16x16x128_f8f6f4 v[134:137], v[26:33], v[226:233], 0
	v_mfma_f32_16x16x128_f8f6f4 v[126:129], v[18:25], v[234:241], 0
	v_mfma_f32_16x16x128_f8f6f4 v[118:121], v[26:33], v[234:241], 0
	v_mfma_f32_16x16x128_f8f6f4 v[110:113], v[18:25], v[242:249], 0
	v_mfma_f32_16x16x128_f8f6f4 v[102:105], v[26:33], v[242:249], 0
	s_setprio 0
	s_setprio 1
	v_mfma_f32_16x16x128_f8f6f4 v[154:157], v[2:9], v[218:225], 0
	v_mfma_f32_16x16x128_f8f6f4 v[146:149], v[10:17], v[218:225], 0
	v_mfma_f32_16x16x128_f8f6f4 v[138:141], v[2:9], v[226:233], 0
	v_mfma_f32_16x16x128_f8f6f4 v[130:133], v[10:17], v[226:233], 0
	v_mfma_f32_16x16x128_f8f6f4 v[122:125], v[2:9], v[234:241], 0
	v_mfma_f32_16x16x128_f8f6f4 v[114:117], v[10:17], v[234:241], 0
	v_mfma_f32_16x16x128_f8f6f4 v[106:109], v[2:9], v[242:249], 0
	v_mfma_f32_16x16x128_f8f6f4 v[98:101], v[10:17], v[242:249], 0
	s_setprio 0
	s_barrier
	s_add_i32 s54, s74, s58
	v_lshl_add_u64 v[196:197], s[50:51], 0, v[168:169]
	s_mov_b32 m0, s54
	ds_read_b128 v[218:221], v207 offset:16384
	ds_read_b128 v[222:225], v207 offset:17408
	ds_read_b128 v[226:229], v207 offset:18432
	ds_read_b128 v[230:233], v207 offset:19456
	ds_read_b128 v[234:237], v207 offset:20480
	ds_read_b128 v[238:241], v207 offset:21504
	ds_read_b128 v[242:245], v207 offset:22528
	ds_read_b128 v[246:249], v207 offset:23552
	global_load_lds_dwordx4 v[196:197], off
	s_add_i32 m0, s54, 0x2000
	s_add_u32 s54, s50, 0x20000
	v_lshl_add_u64 v[198:199], s[50:51], 0, v[166:167]
	s_addc_u32 s55, s51, 0
	s_add_i32 s84, s75, s58
	global_load_lds_dwordx4 v[198:199], off
	v_lshl_add_u64 v[202:203], s[54:55], 0, v[168:169]
	s_mov_b32 m0, s84
	v_mov_b32_e32 v201, v171
	global_load_lds_dwordx4 v[202:203], off
	v_lshl_add_u64 v[202:203], s[54:55], 0, v[166:167]
	s_add_i32 m0, s84, 0x2000
	s_nop 0
	global_load_lds_dwordx4 v[202:203], off
	s_mov_b32 m0, s61
	v_lshl_add_u64 v[202:203], s[52:53], 0, v[170:171]
	global_load_lds_dwordx4 v170, s[52:53]
	s_mov_b32 m0, s62
	s_nop 0
	global_load_lds_dwordx4 v200, s[52:53]
	s_waitcnt vmcnt(8)
	s_waitcnt lgkmcnt(0)
	v_lshl_add_u64 v[200:201], s[52:53], 0, v[200:201]
	s_barrier
	s_setprio 1
	s_waitcnt lgkmcnt(0)
	v_mfma_f32_16x16x128_f8f6f4 v[94:97], v[18:25], v[218:225], 0
	v_mfma_f32_16x16x128_f8f6f4 v[86:89], v[26:33], v[218:225], 0
	v_mfma_f32_16x16x128_f8f6f4 v[78:81], v[18:25], v[226:233], 0
	v_mfma_f32_16x16x128_f8f6f4 v[70:73], v[26:33], v[226:233], 0
	v_mfma_f32_16x16x128_f8f6f4 v[62:65], v[18:25], v[234:241], 0
	v_mfma_f32_16x16x128_f8f6f4 v[54:57], v[26:33], v[234:241], 0
	v_mfma_f32_16x16x128_f8f6f4 v[46:49], v[18:25], v[242:249], 0
	v_mfma_f32_16x16x128_f8f6f4 v[38:41], v[26:33], v[242:249], 0
	s_setprio 0
	s_setprio 1
	v_mfma_f32_16x16x128_f8f6f4 v[90:93], v[2:9], v[218:225], 0
	v_mfma_f32_16x16x128_f8f6f4 v[82:85], v[10:17], v[218:225], 0
	v_mfma_f32_16x16x128_f8f6f4 v[74:77], v[2:9], v[226:233], 0
	v_mfma_f32_16x16x128_f8f6f4 v[66:69], v[10:17], v[226:233], 0
	v_mfma_f32_16x16x128_f8f6f4 v[58:61], v[2:9], v[234:241], 0
	v_mfma_f32_16x16x128_f8f6f4 v[50:53], v[10:17], v[234:241], 0
	v_mfma_f32_16x16x128_f8f6f4 v[42:45], v[2:9], v[242:249], 0
	v_mfma_f32_16x16x128_f8f6f4 v[34:37], v[10:17], v[242:249], 0
	s_setprio 0
	s_barrier
; #define PG8_STAGE(bufoff, gbase, voff) do { _Pragma("unroll") for (int _i = 0; _i < 2; ++_i) \
;         __builtin_amdgcn_global_load_lds((const unsigned*)((const char*)(gbase) + (voff)[_i]), (PG8_LAS unsigned*)(lds + (bufoff) + ldsw + _i * 8192), 16, 0, 0); } while (0)
; #define PG8_STAGE_A(bufoff, kbase, h, gv) do { if constexpr (GATHER) { PG8_STAGE(bufoff, kbase, (gv)[h]); } else { PG8_STAGE(bufoff, (kbase) + (h) * hstep, voffA); } } while (0)
; #define PG8_WAIT_V(n) asm volatile("s_waitcnt vmcnt(" #n ")" ::: "memory")
; #define PG8_WAIT_L(n) asm volatile("s_waitcnt lgkmcnt(" #n ")" ::: "memory")
; #define PG8_BAR __builtin_amdgcn_s_barrier()
; #define PG8_SCHED __builtin_amdgcn_sched_barrier(0)
; template <class Epi, class Sched, bool ALIGN_EPI = false, bool SP2 = false, bool FP8 = false, bool GATHER = false>
; __device__ __forceinline__ void gemm_phase(PG8_LAS unsigned char* lds, const Gemm g, const Sched& S, const Epi& E) {
;     ...
;             PG8_LDB(B0, 1, 0); PG8_LDB(B1, 1, 1); PG8_SCHED; PG8_LDA(At, 1, 0); PG8_STAGE_A(PG8_SA(0, 1), a2, 1, gsel);
;             PG8_WAIT_V(8); PG8_WAIT_L(0); PG8_BAR; PG8_MMA(0, 0, At, B0); PG8_MMA(0, 1, At, B1); PG8_BAR; PG8_SCHED;
;             PG8_LDA(At, 1, 1); PG8_STAGE(PG8_SB(1, 0), b3, voffB); PG8_STAGE(PG8_SB(1, 1), b3 + hstep, voffB); PG8_STAGE_A(PG8_SA(1, 0), a3, 0, gsel);
;             PG8_WAIT_V(8); PG8_WAIT_L(0); PG8_BAR; PG8_MMA(1, 0, At, B0); PG8_MMA(1, 1, At, B1); PG8_BAR; PG8_SCHED;
	s_add_i32 s54, 0, 0x18000
	s_add_i32 s55, 0, 0x1c000
	v_add_u32_e32 v14, s54, v206
	v_add_u32_e32 v30, s55, v206
	ds_read_b128 v[2:5], v14
	ds_read_b128 v[6:9], v14 offset:1024
	ds_read_b128 v[10:13], v14 offset:2048
	ds_read_b128 v[14:17], v14 offset:3072
	ds_read_b128 v[18:21], v30
	ds_read_b128 v[22:25], v30 offset:1024
	ds_read_b128 v[26:29], v30 offset:2048
	ds_read_b128 v[30:33], v30 offset:3072
	s_mov_b32 m0, s63
	ds_read_b128 v[218:221], v207 offset:32768
	ds_read_b128 v[222:225], v207 offset:33792
	ds_read_b128 v[226:229], v207 offset:34816
	ds_read_b128 v[230:233], v207 offset:35840
	ds_read_b128 v[234:237], v207 offset:36864
	ds_read_b128 v[238:241], v207 offset:37888
	ds_read_b128 v[242:245], v207 offset:38912
	ds_read_b128 v[246:249], v207 offset:39936
	global_load_lds_dwordx4 v177, s[52:53]
	s_mov_b32 m0, s65
	s_nop 0
	global_load_lds_dwordx4 v179, s[52:53]
	s_waitcnt vmcnt(8)
	s_waitcnt lgkmcnt(0)
	s_barrier
	s_setprio 1
	s_waitcnt lgkmcnt(0)
	v_mfma_f32_16x16x128_f8f6f4 v[158:161], v[2:9], v[218:225], v[158:161]
	v_mfma_f32_16x16x128_f8f6f4 v[150:153], v[10:17], v[218:225], v[150:153]
	v_mfma_f32_16x16x128_f8f6f4 v[142:145], v[2:9], v[226:233], v[142:145]
	v_mfma_f32_16x16x128_f8f6f4 v[134:137], v[10:17], v[226:233], v[134:137]
	v_mfma_f32_16x16x128_f8f6f4 v[126:129], v[2:9], v[234:241], v[126:129]
	v_mfma_f32_16x16x128_f8f6f4 v[118:121], v[10:17], v[234:241], v[118:121]
	v_mfma_f32_16x16x128_f8f6f4 v[110:113], v[2:9], v[242:249], v[110:113]
	v_mfma_f32_16x16x128_f8f6f4 v[102:105], v[10:17], v[242:249], v[102:105]
	s_setprio 0
	s_setprio 1
	v_mfma_f32_16x16x128_f8f6f4 v[154:157], v[18:25], v[218:225], v[154:157]
	v_mfma_f32_16x16x128_f8f6f4 v[146:149], v[26:33], v[218:225], v[146:149]
	v_mfma_f32_16x16x128_f8f6f4 v[138:141], v[18:25], v[226:233], v[138:141]
	v_mfma_f32_16x16x128_f8f6f4 v[130:133], v[26:33], v[226:233], v[130:133]
	v_mfma_f32_16x16x128_f8f6f4 v[122:125], v[18:25], v[234:241], v[122:125]
	v_mfma_f32_16x16x128_f8f6f4 v[114:117], v[26:33], v[234:241], v[114:117]
	v_mfma_f32_16x16x128_f8f6f4 v[106:109], v[18:25], v[242:249], v[106:109]
	v_mfma_f32_16x16x128_f8f6f4 v[98:101], v[26:33], v[242:249], v[98:101]
	s_setprio 0
	s_barrier
	s_add_i32 s52, s54, s58
	v_lshl_add_u64 v[196:197], v[196:197], 0, s[16:17]
	s_mov_b32 m0, s52
	ds_read_b128 v[218:221], v207 offset:49152
	ds_read_b128 v[222:225], v207 offset:50176
	ds_read_b128 v[226:229], v207 offset:51200
	ds_read_b128 v[230:233], v207 offset:52224
	ds_read_b128 v[234:237], v207 offset:53248
	ds_read_b128 v[238:241], v207 offset:54272
	ds_read_b128 v[242:245], v207 offset:55296
	ds_read_b128 v[246:249], v207 offset:56320
	global_load_lds_dwordx4 v[196:197], off
	s_add_i32 m0, s52, 0x2000
	s_add_u32 s50, s50, 0x20080
	v_lshl_add_u64 v[196:197], v[198:199], 0, s[16:17]
	s_addc_u32 s51, s51, 0
	s_add_i32 s52, s55, s58
	global_load_lds_dwordx4 v[196:197], off
	v_lshl_add_u64 v[196:197], s[50:51], 0, v[168:169]
	s_mov_b32 m0, s52
	s_nop 0
	global_load_lds_dwordx4 v[196:197], off
	v_lshl_add_u64 v[196:197], s[50:51], 0, v[166:167]
	s_add_i32 m0, s52, 0x2000
	s_nop 0
	global_load_lds_dwordx4 v[196:197], off
	v_lshl_add_u64 v[196:197], v[202:203], 0, s[16:17]
	s_mov_b32 m0, s68
	s_nop 0
	global_load_lds_dwordx4 v[196:197], off
	v_lshl_add_u64 v[196:197], v[200:201], 0, s[16:17]
	s_mov_b32 m0, s69
	s_nop 0
	global_load_lds_dwordx4 v[196:197], off
	s_waitcnt vmcnt(8)
	s_waitcnt lgkmcnt(0)
	s_barrier
	s_setprio 1
	s_waitcnt lgkmcnt(0)
	v_mfma_f32_16x16x128_f8f6f4 v[94:97], v[2:9], v[218:225], v[94:97]
	v_mfma_f32_16x16x128_f8f6f4 v[86:89], v[10:17], v[218:225], v[86:89]
	v_mfma_f32_16x16x128_f8f6f4 v[78:81], v[2:9], v[226:233], v[78:81]
	v_mfma_f32_16x16x128_f8f6f4 v[70:73], v[10:17], v[226:233], v[70:73]
	v_mfma_f32_16x16x128_f8f6f4 v[62:65], v[2:9], v[234:241], v[62:65]
	v_mfma_f32_16x16x128_f8f6f4 v[54:57], v[10:17], v[234:241], v[54:57]
	v_mfma_f32_16x16x128_f8f6f4 v[46:49], v[2:9], v[242:249], v[46:49]
	v_mfma_f32_16x16x128_f8f6f4 v[38:41], v[10:17], v[242:249], v[38:41]
	s_setprio 0
	s_setprio 1
	v_mfma_f32_16x16x128_f8f6f4 v[90:93], v[18:25], v[218:225], v[90:93]
	v_mfma_f32_16x16x128_f8f6f4 v[82:85], v[26:33], v[218:225], v[82:85]
	v_mfma_f32_16x16x128_f8f6f4 v[74:77], v[18:25], v[226:233], v[74:77]
	v_mfma_f32_16x16x128_f8f6f4 v[66:69], v[26:33], v[226:233], v[66:69]
	v_mfma_f32_16x16x128_f8f6f4 v[58:61], v[18:25], v[234:241], v[58:61]
	v_mfma_f32_16x16x128_f8f6f4 v[50:53], v[26:33], v[234:241], v[50:53]
	v_mfma_f32_16x16x128_f8f6f4 v[42:45], v[18:25], v[242:249], v[42:45]
	v_mfma_f32_16x16x128_f8f6f4 v[34:37], v[26:33], v[242:249], v[34:37]
	s_setprio 0
	s_add_i32 s83, s83, 2
	s_add_u32 s46, s46, 0x100
	s_addc_u32 s47, s47, 0
	s_cmp_gt_u32 s83, 5
	s_cbranch_scc1 .Lrot1781_exit
	s_barrier
	s_branch .LBB0_1782
; #define PG8_STAGE(bufoff, gbase, voff) do { _Pragma("unroll") for (int _i = 0; _i < 2; ++_i) \
;         __builtin_amdgcn_global_load_lds((const unsigned*)((const char*)(gbase) + (voff)[_i]), (PG8_LAS unsigned*)(lds + (bufoff) + ldsw + _i * 8192), 16, 0, 0); } while (0)
; #define PG8_STAGE_A(bufoff, kbase, h, gv) do { if constexpr (GATHER) { PG8_STAGE(bufoff, kbase, (gv)[h]); } else { PG8_STAGE(bufoff, (kbase) + (h) * hstep, voffA); } } while (0)
; #define PG8_BAR __builtin_amdgcn_s_barrier()
; template <class Epi, class Sched, bool ALIGN_EPI = false, bool SP2 = false, bool FP8 = false, bool GATHER = false>
; __device__ __forceinline__ void gemm_phase(PG8_LAS unsigned char* lds, const Gemm g, const Sched& S, const Epi& E) {
;     ...
;         for (int t = 0; t < nt; t += 2) {
;             const bool last = (t == nt - 2);
;             const char* a1 = cA + (size_t)(t + 1) * kstep;
;             const char* a2 = last ? nA : cA + (size_t)(t + 2) * kstep; const char* b2 = last ? nB : cB + (size_t)(t + 2) * kstep;
;             const char* a3 = a2 + kstep; const char* b3 = b2 + kstep;
;             if (last && has_next) S.a_ready(nxt);
;             if (last) E.pre(cur, wid, lane);
;             if constexpr (GATHER) { if (t == nt - 4 && has_next) { _Pragma("unroll") for (int h_ = 0; h_ < 2; ++h_) _Pragma("unroll") for (int i_ = 0; i_ < 2; ++i_)
;                 asm volatile("global_load_dword %0, %1, off" : "+v"(graw[h_][i_]) : "v"(S.rowtok + (nxt.pm * BM + h_ * HALF + gR[i_])) : "memory"); } }
;             unsigned gsel[2][2];
;             if constexpr (GATHER) { _Pragma("unroll") for (int h_ = 0; h_ < 2; ++h_) _Pragma("unroll") for (int i_ = 0; i_ < 2; ++i_) { if (last && has_next) gnxt[h_][i_] = graw[h_][i_] * (unsigned)(K * 2) + gC[i_]; gsel[h_][i_] = (last && has_next) ? gnxt[h_][i_] : gcur[h_][i_]; } }
;             if constexpr (SP2) {
;             PG8_LDB(B0, 0, 0); PG8_LDB(B1, 0, 1); PG8_SCHED; PG8_LDA(At, 0, 0); PG8_STAGE_A(PG8_SA(1, 1), a1, 1, gcur);
;             PG8_WAIT_V(8); PG8_WAIT_L(0); PG8_BAR; PG8_MMA(0, 0, At, B0); PG8_MMA(0, 1, At, B1); PG8_BAR; PG8_SCHED;
;             PG8_LDA(At, 0, 1); PG8_STAGE(PG8_SB(0, 0), b2, voffB); PG8_STAGE(PG8_SB(0, 1), b2 + hstep, voffB); PG8_STAGE_A(PG8_SA(0, 0), a2, 0, gsel);
;             PG8_WAIT_V(8); PG8_WAIT_L(0); PG8_BAR; PG8_MMA(1, 0, At, B0); PG8_MMA(1, 1, At, B1); PG8_BAR; PG8_SCHED;
.LBB0_1781:
	s_add_u32 s50, s6, s46
	s_addc_u32 s51, s7, s47
	s_add_u32 s52, s50, 0x19200100
	s_addc_u32 s53, s51, 0
	s_and_b64 s[50:51], s[54:55], exec
	s_cselect_b32 s53, s9, s53
	s_cselect_b32 s52, s8, s52
	s_add_u32 s84, s20, s46
	s_addc_u32 s85, s82, s47
	s_and_b64 s[50:51], s[54:55], exec
	s_cselect_b32 s51, s35, s85
	s_cselect_b32 s50, s34, s84
	v_lshl_add_u32 v2, v213, 10, v1
	s_and_b64 vcc, s[44:45], s[54:55]
	v_cndmask_b32_e32 v209, v209, v2, vcc
	v_cndmask_b32_e32 v170, v217, v2, vcc
	v_lshl_add_u32 v2, v214, 10, v204
	v_cndmask_b32_e32 v210, v210, v2, vcc
	v_cndmask_b32_e32 v200, v180, v2, vcc
	v_add_u32_e32 v2, s74, v206
	v_add_u32_e32 v14, s75, v206
	ds_read_b128 v[18:21], v2
	ds_read_b128 v[22:25], v2 offset:1024
	ds_read_b128 v[26:29], v2 offset:2048
	ds_read_b128 v[30:33], v2 offset:3072
	ds_read_b128 v[2:5], v14
	ds_read_b128 v[6:9], v14 offset:1024
	ds_read_b128 v[10:13], v14 offset:2048
	ds_read_b128 v[14:17], v14 offset:3072
	v_lshl_add_u32 v177, v215, 10, v1
	v_lshl_add_u32 v179, v216, 10, v204
	v_cndmask_b32_e32 v211, v211, v177, vcc
	v_cndmask_b32_e32 v212, v212, v179, vcc
	v_cndmask_b32_e32 v177, v178, v177, vcc
	v_cndmask_b32_e32 v179, v176, v179, vcc
	v_lshl_add_u64 v[196:197], v[194:195], 0, s[46:47]
	s_add_i32 m0, s61, 0xc000
	ds_read_b128 v[218:221], v207
	ds_read_b128 v[222:225], v207 offset:1024
	ds_read_b128 v[226:229], v207 offset:2048
	ds_read_b128 v[230:233], v207 offset:3072
	ds_read_b128 v[234:237], v207 offset:4096
	ds_read_b128 v[238:241], v207 offset:5120
	ds_read_b128 v[242:245], v207 offset:6144
	ds_read_b128 v[246:249], v207 offset:7168
	global_load_lds_dwordx4 v[196:197], off
	v_lshl_add_u64 v[196:197], v[192:193], 0, s[46:47]
	s_add_i32 m0, s61, 0xe000
	s_nop 0
	global_load_lds_dwordx4 v[196:197], off
	s_waitcnt vmcnt(8)
	s_waitcnt lgkmcnt(0)
	s_barrier
	s_setprio 1
	s_waitcnt lgkmcnt(0)
	v_mfma_f32_16x16x128_f8f6f4 v[158:161], v[18:25], v[218:225], v[158:161]
	v_mfma_f32_16x16x128_f8f6f4 v[150:153], v[26:33], v[218:225], v[150:153]
	v_mfma_f32_16x16x128_f8f6f4 v[142:145], v[18:25], v[226:233], v[142:145]
	v_mfma_f32_16x16x128_f8f6f4 v[134:137], v[26:33], v[226:233], v[134:137]
	v_mfma_f32_16x16x128_f8f6f4 v[126:129], v[18:25], v[234:241], v[126:129]
	v_mfma_f32_16x16x128_f8f6f4 v[118:121], v[26:33], v[234:241], v[118:121]
	v_mfma_f32_16x16x128_f8f6f4 v[110:113], v[18:25], v[242:249], v[110:113]
	v_mfma_f32_16x16x128_f8f6f4 v[102:105], v[26:33], v[242:249], v[102:105]
	s_setprio 0
	s_setprio 1
	v_mfma_f32_16x16x128_f8f6f4 v[154:157], v[2:9], v[218:225], v[154:157]
	v_mfma_f32_16x16x128_f8f6f4 v[146:149], v[10:17], v[218:225], v[146:149]
	v_mfma_f32_16x16x128_f8f6f4 v[138:141], v[2:9], v[226:233], v[138:141]
	v_mfma_f32_16x16x128_f8f6f4 v[130:133], v[10:17], v[226:233], v[130:133]
	v_mfma_f32_16x16x128_f8f6f4 v[122:125], v[2:9], v[234:241], v[122:125]
	v_mfma_f32_16x16x128_f8f6f4 v[114:117], v[10:17], v[234:241], v[114:117]
	v_mfma_f32_16x16x128_f8f6f4 v[106:109], v[2:9], v[242:249], v[106:109]
	v_mfma_f32_16x16x128_f8f6f4 v[98:101], v[10:17], v[242:249], v[98:101]
	s_setprio 0
	s_barrier
	s_add_i32 s54, s74, s58
	v_lshl_add_u64 v[196:197], s[50:51], 0, v[168:169]
	s_mov_b32 m0, s54
	ds_read_b128 v[218:221], v207 offset:16384
	ds_read_b128 v[222:225], v207 offset:17408
	ds_read_b128 v[226:229], v207 offset:18432
	ds_read_b128 v[230:233], v207 offset:19456
	ds_read_b128 v[234:237], v207 offset:20480
	ds_read_b128 v[238:241], v207 offset:21504
	ds_read_b128 v[242:245], v207 offset:22528
	ds_read_b128 v[246:249], v207 offset:23552
	global_load_lds_dwordx4 v[196:197], off
	s_add_i32 m0, s54, 0x2000
	s_add_u32 s54, s50, 0x20000
	v_lshl_add_u64 v[198:199], s[50:51], 0, v[166:167]
	s_addc_u32 s55, s51, 0
	s_add_i32 s84, s75, s58
	global_load_lds_dwordx4 v[198:199], off
	v_lshl_add_u64 v[202:203], s[54:55], 0, v[168:169]
	s_mov_b32 m0, s84
	v_mov_b32_e32 v201, v171
	global_load_lds_dwordx4 v[202:203], off
	v_lshl_add_u64 v[202:203], s[54:55], 0, v[166:167]
	s_add_i32 m0, s84, 0x2000
	s_nop 0
	global_load_lds_dwordx4 v[202:203], off
	s_mov_b32 m0, s61
	v_lshl_add_u64 v[202:203], s[52:53], 0, v[170:171]
	global_load_lds_dwordx4 v170, s[52:53]
	s_mov_b32 m0, s62
	s_nop 0
	global_load_lds_dwordx4 v200, s[52:53]
	s_waitcnt vmcnt(8)
	s_waitcnt lgkmcnt(0)
	v_lshl_add_u64 v[200:201], s[52:53], 0, v[200:201]
	s_barrier
	s_setprio 1
	s_waitcnt lgkmcnt(0)
	v_mfma_f32_16x16x128_f8f6f4 v[94:97], v[18:25], v[218:225], v[94:97]
	v_mfma_f32_16x16x128_f8f6f4 v[86:89], v[26:33], v[218:225], v[86:89]
	v_mfma_f32_16x16x128_f8f6f4 v[78:81], v[18:25], v[226:233], v[78:81]
	v_mfma_f32_16x16x128_f8f6f4 v[70:73], v[26:33], v[226:233], v[70:73]
	v_mfma_f32_16x16x128_f8f6f4 v[62:65], v[18:25], v[234:241], v[62:65]
	v_mfma_f32_16x16x128_f8f6f4 v[54:57], v[26:33], v[234:241], v[54:57]
	v_mfma_f32_16x16x128_f8f6f4 v[46:49], v[18:25], v[242:249], v[46:49]
	v_mfma_f32_16x16x128_f8f6f4 v[38:41], v[26:33], v[242:249], v[38:41]
	s_setprio 0
	s_setprio 1
	v_mfma_f32_16x16x128_f8f6f4 v[90:93], v[2:9], v[218:225], v[90:93]
	v_mfma_f32_16x16x128_f8f6f4 v[82:85], v[10:17], v[218:225], v[82:85]
	v_mfma_f32_16x16x128_f8f6f4 v[74:77], v[2:9], v[226:233], v[74:77]
	v_mfma_f32_16x16x128_f8f6f4 v[66:69], v[10:17], v[226:233], v[66:69]
	v_mfma_f32_16x16x128_f8f6f4 v[58:61], v[2:9], v[234:241], v[58:61]
	v_mfma_f32_16x16x128_f8f6f4 v[50:53], v[10:17], v[234:241], v[50:53]
	v_mfma_f32_16x16x128_f8f6f4 v[42:45], v[2:9], v[242:249], v[42:45]
	v_mfma_f32_16x16x128_f8f6f4 v[34:37], v[10:17], v[242:249], v[34:37]
	s_setprio 0
	s_barrier
; #define PG8_STAGE(bufoff, gbase, voff) do { _Pragma("unroll") for (int _i = 0; _i < 2; ++_i) \
;         __builtin_amdgcn_global_load_lds((const unsigned*)((const char*)(gbase) + (voff)[_i]), (PG8_LAS unsigned*)(lds + (bufoff) + ldsw + _i * 8192), 16, 0, 0); } while (0)
; #define PG8_STAGE_A(bufoff, kbase, h, gv) do { if constexpr (GATHER) { PG8_STAGE(bufoff, kbase, (gv)[h]); } else { PG8_STAGE(bufoff, (kbase) + (h) * hstep, voffA); } } while (0)
; #define PG8_WAIT_V(n) asm volatile("s_waitcnt vmcnt(" #n ")" ::: "memory")
; #define PG8_WAIT_L(n) asm volatile("s_waitcnt lgkmcnt(" #n ")" ::: "memory")
; #define PG8_BAR __builtin_amdgcn_s_barrier()
; #define PG8_SCHED __builtin_amdgcn_sched_barrier(0)
; template <class Epi, class Sched, bool ALIGN_EPI = false, bool SP2 = false, bool FP8 = false, bool GATHER = false>
; __device__ __forceinline__ void gemm_phase(PG8_LAS unsigned char* lds, const Gemm g, const Sched& S, const Epi& E) {
;     ...
;             PG8_LDB(B0, 1, 0); PG8_LDB(B1, 1, 1); PG8_SCHED; PG8_LDA(At, 1, 0); PG8_STAGE_A(PG8_SA(0, 1), a2, 1, gsel);
;             PG8_WAIT_V(8); PG8_WAIT_L(0); PG8_BAR; PG8_MMA(0, 0, At, B0); PG8_MMA(0, 1, At, B1); PG8_BAR; PG8_SCHED;
;             PG8_LDA(At, 1, 1); PG8_STAGE(PG8_SB(1, 0), b3, voffB); PG8_STAGE(PG8_SB(1, 1), b3 + hstep, voffB); PG8_STAGE_A(PG8_SA(1, 0), a3, 0, gsel);
;             PG8_WAIT_V(8); PG8_WAIT_L(0); PG8_BAR; PG8_MMA(1, 0, At, B0); PG8_MMA(1, 1, At, B1); PG8_BAR; PG8_SCHED;
	s_add_i32 s54, 0, 0x18000
	s_add_i32 s55, 0, 0x1c000
	v_add_u32_e32 v14, s54, v206
	v_add_u32_e32 v30, s55, v206
	ds_read_b128 v[2:5], v14
	ds_read_b128 v[6:9], v14 offset:1024
	ds_read_b128 v[10:13], v14 offset:2048
	ds_read_b128 v[14:17], v14 offset:3072
	ds_read_b128 v[18:21], v30
	ds_read_b128 v[22:25], v30 offset:1024
	ds_read_b128 v[26:29], v30 offset:2048
	ds_read_b128 v[30:33], v30 offset:3072
	s_mov_b32 m0, s63
	ds_read_b128 v[218:221], v207 offset:32768
	ds_read_b128 v[222:225], v207 offset:33792
	ds_read_b128 v[226:229], v207 offset:34816
	ds_read_b128 v[230:233], v207 offset:35840
	ds_read_b128 v[234:237], v207 offset:36864
	ds_read_b128 v[238:241], v207 offset:37888
	ds_read_b128 v[242:245], v207 offset:38912
	ds_read_b128 v[246:249], v207 offset:39936
	global_load_lds_dwordx4 v177, s[52:53]
	s_mov_b32 m0, s65
	s_nop 0
	global_load_lds_dwordx4 v179, s[52:53]
	s_waitcnt vmcnt(8)
	s_waitcnt lgkmcnt(0)
	s_barrier
	s_setprio 1
	s_waitcnt lgkmcnt(0)
	v_mfma_f32_16x16x128_f8f6f4 v[158:161], v[2:9], v[218:225], v[158:161]
	v_mfma_f32_16x16x128_f8f6f4 v[150:153], v[10:17], v[218:225], v[150:153]
	v_mfma_f32_16x16x128_f8f6f4 v[142:145], v[2:9], v[226:233], v[142:145]
	v_mfma_f32_16x16x128_f8f6f4 v[134:137], v[10:17], v[226:233], v[134:137]
	v_mfma_f32_16x16x128_f8f6f4 v[126:129], v[2:9], v[234:241], v[126:129]
	v_mfma_f32_16x16x128_f8f6f4 v[118:121], v[10:17], v[234:241], v[118:121]
	v_mfma_f32_16x16x128_f8f6f4 v[110:113], v[2:9], v[242:249], v[110:113]
	v_mfma_f32_16x16x128_f8f6f4 v[102:105], v[10:17], v[242:249], v[102:105]
	s_setprio 0
	s_setprio 1
	v_mfma_f32_16x16x128_f8f6f4 v[154:157], v[18:25], v[218:225], v[154:157]
	v_mfma_f32_16x16x128_f8f6f4 v[146:149], v[26:33], v[218:225], v[146:149]
	v_mfma_f32_16x16x128_f8f6f4 v[138:141], v[18:25], v[226:233], v[138:141]
	v_mfma_f32_16x16x128_f8f6f4 v[130:133], v[26:33], v[226:233], v[130:133]
	v_mfma_f32_16x16x128_f8f6f4 v[122:125], v[18:25], v[234:241], v[122:125]
	v_mfma_f32_16x16x128_f8f6f4 v[114:117], v[26:33], v[234:241], v[114:117]
	v_mfma_f32_16x16x128_f8f6f4 v[106:109], v[18:25], v[242:249], v[106:109]
	v_mfma_f32_16x16x128_f8f6f4 v[98:101], v[26:33], v[242:249], v[98:101]
	s_setprio 0
	s_barrier
	s_add_i32 s52, s54, s58
	v_lshl_add_u64 v[196:197], v[196:197], 0, s[16:17]
	s_mov_b32 m0, s52
	ds_read_b128 v[218:221], v207 offset:49152
	ds_read_b128 v[222:225], v207 offset:50176
	ds_read_b128 v[226:229], v207 offset:51200
	ds_read_b128 v[230:233], v207 offset:52224
	ds_read_b128 v[234:237], v207 offset:53248
	ds_read_b128 v[238:241], v207 offset:54272
	ds_read_b128 v[242:245], v207 offset:55296
	ds_read_b128 v[246:249], v207 offset:56320
	global_load_lds_dwordx4 v[196:197], off
	s_add_i32 m0, s52, 0x2000
	s_add_u32 s50, s50, 0x20080
	v_lshl_add_u64 v[196:197], v[198:199], 0, s[16:17]
	s_addc_u32 s51, s51, 0
	s_add_i32 s52, s55, s58
	global_load_lds_dwordx4 v[196:197], off
	v_lshl_add_u64 v[196:197], s[50:51], 0, v[168:169]
	s_mov_b32 m0, s52
	s_nop 0
	global_load_lds_dwordx4 v[196:197], off
	v_lshl_add_u64 v[196:197], s[50:51], 0, v[166:167]
	s_add_i32 m0, s52, 0x2000
	s_nop 0
	global_load_lds_dwordx4 v[196:197], off
	v_lshl_add_u64 v[196:197], v[202:203], 0, s[16:17]
	s_mov_b32 m0, s68
	s_nop 0
	global_load_lds_dwordx4 v[196:197], off
	v_lshl_add_u64 v[196:197], v[200:201], 0, s[16:17]
	s_mov_b32 m0, s69
	s_nop 0
	global_load_lds_dwordx4 v[196:197], off
	s_waitcnt vmcnt(8)
	s_waitcnt lgkmcnt(0)
	s_barrier
	s_setprio 1
	s_waitcnt lgkmcnt(0)
	v_mfma_f32_16x16x128_f8f6f4 v[94:97], v[2:9], v[218:225], v[94:97]
	v_mfma_f32_16x16x128_f8f6f4 v[86:89], v[10:17], v[218:225], v[86:89]
	v_mfma_f32_16x16x128_f8f6f4 v[78:81], v[2:9], v[226:233], v[78:81]
	v_mfma_f32_16x16x128_f8f6f4 v[70:73], v[10:17], v[226:233], v[70:73]
	v_mfma_f32_16x16x128_f8f6f4 v[62:65], v[2:9], v[234:241], v[62:65]
	v_mfma_f32_16x16x128_f8f6f4 v[54:57], v[10:17], v[234:241], v[54:57]
	v_mfma_f32_16x16x128_f8f6f4 v[46:49], v[2:9], v[242:249], v[46:49]
	v_mfma_f32_16x16x128_f8f6f4 v[38:41], v[10:17], v[242:249], v[38:41]
	s_setprio 0
	s_setprio 1
	v_mfma_f32_16x16x128_f8f6f4 v[90:93], v[18:25], v[218:225], v[90:93]
	v_mfma_f32_16x16x128_f8f6f4 v[82:85], v[26:33], v[218:225], v[82:85]
	v_mfma_f32_16x16x128_f8f6f4 v[74:77], v[18:25], v[226:233], v[74:77]
	v_mfma_f32_16x16x128_f8f6f4 v[66:69], v[26:33], v[226:233], v[66:69]
	v_mfma_f32_16x16x128_f8f6f4 v[58:61], v[18:25], v[234:241], v[58:61]
	v_mfma_f32_16x16x128_f8f6f4 v[50:53], v[26:33], v[234:241], v[50:53]
	v_mfma_f32_16x16x128_f8f6f4 v[42:45], v[18:25], v[242:249], v[42:45]
	v_mfma_f32_16x16x128_f8f6f4 v[34:37], v[26:33], v[242:249], v[34:37]
	s_setprio 0
	s_add_i32 s83, s83, 2
	s_add_u32 s46, s46, 0x100
	s_addc_u32 s47, s47, 0
	s_cmp_gt_u32 s83, 5
	s_cbranch_scc1 .Lrot1781_exit
	s_barrier

; #define PG8_BAR __builtin_amdgcn_s_barrier()
; template <class Epi, class Sched, bool ALIGN_EPI = false, bool SP2 = false, bool FP8 = false, bool GATHER = false>
; __device__ __forceinline__ void gemm_phase(PG8_LAS unsigned char* lds, const Gemm g, const Sched& S, const Epi& E) {
;     ...
;             if constexpr (GATHER) { if (t == nt - 4 && has_next) { _Pragma("unroll") for (int h_ = 0; h_ < 2; ++h_) _Pragma("unroll") for (int i_ = 0; i_ < 2; ++i_)
;                 asm volatile("global_load_dword %0, %1, off" : "+v"(graw[h_][i_]) : "v"(S.rowtok + (nxt.pm * BM + h_ * HALF + gR[i_])) : "memory"); } }
;     ...
;         if constexpr (FP8) asm volatile("s_nop 15\n\ts_nop 15" ::: "memory");
;         if constexpr (ALIGN_EPI) { if (wr == 0) PG8_BAR; }
.LBB0_1784:
	s_cmpk_lg_i32 s46, 0x200
	s_cselect_b64 s[50:51], -1, 0
	s_or_b64 s[50:51], s[48:49], s[50:51]
	s_and_b64 vcc, exec, s[50:51]
	s_cbranch_vccnz .LBB0_1781
	global_load_dword v213, v[190:191], off
	global_load_dword v214, v[188:189], off
	global_load_dword v215, v[186:187], off
	global_load_dword v216, v[184:185], off
	s_branch .LBB0_1781
.Lrot1781_exit:
	s_barrier
.LBB0_1786:
	s_nop 15
	s_nop 15
	s_and_b64 vcc, exec, s[24:25]
	s_cbranch_vccz .LBB0_1788
	s_barrier

; #define PG8_STAGE(bufoff, gbase, voff) do { _Pragma("unroll") for (int _i = 0; _i < 2; ++_i) \
;         __builtin_amdgcn_global_load_lds((const unsigned*)((const char*)(gbase) + (voff)[_i]), (PG8_LAS unsigned*)(lds + (bufoff) + ldsw + _i * 8192), 16, 0, 0); } while (0)
; template <class Epi, class Sched, bool ALIGN_EPI = false, bool SP2 = false, bool FP8 = false, bool GATHER = false>
; __device__ __forceinline__ void gemm_phase(PG8_LAS unsigned char* lds, const Gemm g, const Sched& S, const Epi& E) {
;     ...
;         for (int t = 0; t < nt; t += 2) {
;             const bool last = (t == nt - 2);
;             const char* a1 = cA + (size_t)(t + 1) * kstep;
;             const char* a2 = last ? nA : cA + (size_t)(t + 2) * kstep; const char* b2 = last ? nB : cB + (size_t)(t + 2) * kstep;
;             const char* a3 = a2 + kstep; const char* b3 = b2 + kstep;
;             if (last && has_next) S.a_ready(nxt);
;             if (last) E.pre(cur, wid, lane);
;             if constexpr (GATHER) { if (t == nt - 4 && has_next) { _Pragma("unroll") for (int h_ = 0; h_ < 2; ++h_) _Pragma("unroll") for (int i_ = 0; i_ < 2; ++i_)
;                 asm volatile("global_load_dword %0, %1, off" : "+v"(graw[h_][i_]) : "v"(S.rowtok + (nxt.pm * BM + h_ * HALF + gR[i_])) : "memory"); } }
;             unsigned gsel[2][2];
;             if constexpr (GATHER) { _Pragma("unroll") for (int h_ = 0; h_ < 2; ++h_) _Pragma("unroll") for (int i_ = 0; i_ < 2; ++i_) { if (last && has_next) gnxt[h_][i_] = graw[h_][i_] * (unsigned)(K * 2) + gC[i_]; gsel[h_][i_] = (last && has_next) ? gnxt[h_][i_] : gcur[h_][i_]; } }
;             if constexpr (SP2) {
;             PG8_LDB(B0, 0, 0); PG8_LDB(B1, 0, 1); PG8_SCHED; PG8_LDA(At, 0, 0); PG8_STAGE_A(PG8_SA(1, 1), a1, 1, gcur);
;             PG8_WAIT_V(8); PG8_WAIT_L(0); PG8_BAR; PG8_MMA(0, 0, At, B0); PG8_MMA(0, 1, At, B1); PG8_BAR; PG8_SCHED;
;             PG8_LDA(At, 0, 1); PG8_STAGE(PG8_SB(0, 0), b2, voffB); PG8_STAGE(PG8_SB(0, 1), b2 + hstep, voffB); PG8_STAGE_A(PG8_SA(0, 0), a2, 0, gsel);
;             PG8_WAIT_V(8); PG8_WAIT_L(0); PG8_BAR; PG8_MMA(1, 0, At, B0); PG8_MMA(1, 1, At, B1); PG8_BAR; PG8_SCHED;
;             PG8_LDB(B0, 1, 0); PG8_LDB(B1, 1, 1); PG8_SCHED; PG8_LDA(At, 1, 0); PG8_STAGE_A(PG8_SA(0, 1), a2, 1, gsel);
;             PG8_WAIT_V(8); PG8_WAIT_L(0); PG8_BAR; PG8_MMA(0, 0, At, B0); PG8_MMA(0, 1, At, B1); PG8_BAR; PG8_SCHED;
.Lpeel1856_body:
	v_add_u32_e32 v2, s74, v191
	v_add_u32_e32 v14, s75, v191
	ds_read_b128 v[18:21], v2
	ds_read_b128 v[22:25], v2 offset:1024
	ds_read_b128 v[26:29], v2 offset:2048
	ds_read_b128 v[30:33], v2 offset:3072
	ds_read_b128 v[2:5], v14
	ds_read_b128 v[6:9], v14 offset:1024
	ds_read_b128 v[10:13], v14 offset:2048
	ds_read_b128 v[14:17], v14 offset:3072
	s_add_u32 s48, s44, 0xfffe0080
	s_addc_u32 s49, s45, -1
	s_and_b64 s[46:47], s[46:47], exec
	s_cselect_b32 s49, s78, s49
	s_cselect_b32 s48, s79, s48
	s_cselect_b32 s47, s25, s80
	s_cselect_b32 s46, s24, s35
	v_lshl_add_u64 v[218:219], s[44:45], 0, v[172:173]
	s_add_i32 m0, s58, 0xc000
	ds_read_b128 v[182:185], v192
	ds_read_b128 v[186:189], v192 offset:1024
	ds_read_b128 v[194:197], v192 offset:2048
	ds_read_b128 v[198:201], v192 offset:3072
	ds_read_b128 v[202:205], v192 offset:4096
	ds_read_b128 v[206:209], v192 offset:5120
	ds_read_b128 v[210:213], v192 offset:6144
	ds_read_b128 v[214:217], v192 offset:7168
	global_load_lds_dwordx4 v[218:219], off
	v_lshl_add_u64 v[218:219], s[44:45], 0, v[174:175]
	s_add_i32 m0, s58, 0xe000
	s_nop 0
	global_load_lds_dwordx4 v[218:219], off
	s_waitcnt vmcnt(8)
	s_waitcnt lgkmcnt(0)
	s_barrier
	s_setprio 1
	s_waitcnt lgkmcnt(0)
	v_mfma_f32_16x16x128_f8f6f4 v[158:161], v[18:25], v[182:189], 0
	v_mfma_f32_16x16x128_f8f6f4 v[154:157], v[26:33], v[182:189], 0
	v_mfma_f32_16x16x128_f8f6f4 v[150:153], v[18:25], v[194:201], 0
	v_mfma_f32_16x16x128_f8f6f4 v[146:149], v[26:33], v[194:201], 0
	v_mfma_f32_16x16x128_f8f6f4 v[130:133], v[18:25], v[202:209], 0
	v_mfma_f32_16x16x128_f8f6f4 v[122:125], v[26:33], v[202:209], 0
	v_mfma_f32_16x16x128_f8f6f4 v[118:121], v[18:25], v[210:217], 0
	v_mfma_f32_16x16x128_f8f6f4 v[114:117], v[26:33], v[210:217], 0
	s_setprio 0
	s_setprio 1
	v_mfma_f32_16x16x128_f8f6f4 v[142:145], v[2:9], v[182:189], 0
	v_mfma_f32_16x16x128_f8f6f4 v[138:141], v[10:17], v[182:189], 0
	v_mfma_f32_16x16x128_f8f6f4 v[134:137], v[2:9], v[194:201], 0
	v_mfma_f32_16x16x128_f8f6f4 v[126:129], v[10:17], v[194:201], 0
	v_mfma_f32_16x16x128_f8f6f4 v[110:113], v[2:9], v[202:209], 0
	v_mfma_f32_16x16x128_f8f6f4 v[106:109], v[10:17], v[202:209], 0
	v_mfma_f32_16x16x128_f8f6f4 v[102:105], v[2:9], v[210:217], 0
	v_mfma_f32_16x16x128_f8f6f4 v[98:101], v[10:17], v[210:217], 0
	s_setprio 0
	s_barrier
	s_add_i32 s82, s74, s56
	v_lshl_add_u64 v[182:183], s[46:47], 0, v[166:167]
	s_mov_b32 m0, s82
	ds_read_b128 v[194:197], v192 offset:16384
	ds_read_b128 v[198:201], v192 offset:17408
	ds_read_b128 v[202:205], v192 offset:18432
	ds_read_b128 v[206:209], v192 offset:19456
	ds_read_b128 v[210:213], v192 offset:20480
	ds_read_b128 v[214:217], v192 offset:21504
	ds_read_b128 v[218:221], v192 offset:22528
	ds_read_b128 v[222:225], v192 offset:23552
	global_load_lds_dwordx4 v[182:183], off
	s_add_i32 m0, s82, 0x2000
	s_add_u32 s82, s46, 0x20000
	v_lshl_add_u64 v[184:185], s[46:47], 0, v[162:163]
	s_addc_u32 s83, s47, 0
	s_add_i32 s84, s75, s56
	global_load_lds_dwordx4 v[184:185], off
	v_lshl_add_u64 v[186:187], s[82:83], 0, v[166:167]
	s_mov_b32 m0, s84
	v_lshl_add_u64 v[188:189], s[48:49], 0, v[164:165]
	global_load_lds_dwordx4 v[186:187], off
	v_lshl_add_u64 v[186:187], s[82:83], 0, v[162:163]
	s_add_i32 m0, s84, 0x2000
	s_nop 0
	global_load_lds_dwordx4 v[186:187], off
	v_lshl_add_u64 v[186:187], s[48:49], 0, v[168:169]
	s_mov_b32 m0, s58
	s_nop 0
	global_load_lds_dwordx4 v[186:187], off
	s_mov_b32 m0, s59
	s_nop 0
	global_load_lds_dwordx4 v[188:189], off
	s_waitcnt vmcnt(8)
	s_waitcnt lgkmcnt(0)
	s_barrier
	s_setprio 1
	s_waitcnt lgkmcnt(0)
	v_mfma_f32_16x16x128_f8f6f4 v[94:97], v[18:25], v[194:201], 0
	v_mfma_f32_16x16x128_f8f6f4 v[90:93], v[26:33], v[194:201], 0
	v_mfma_f32_16x16x128_f8f6f4 v[86:89], v[18:25], v[202:209], 0
	v_mfma_f32_16x16x128_f8f6f4 v[82:85], v[26:33], v[202:209], 0
	v_mfma_f32_16x16x128_f8f6f4 v[66:69], v[18:25], v[210:217], 0
	v_mfma_f32_16x16x128_f8f6f4 v[58:61], v[26:33], v[210:217], 0
	v_mfma_f32_16x16x128_f8f6f4 v[54:57], v[18:25], v[218:225], 0
	v_mfma_f32_16x16x128_f8f6f4 v[50:53], v[26:33], v[218:225], 0
	s_setprio 0
	s_setprio 1
	v_mfma_f32_16x16x128_f8f6f4 v[78:81], v[2:9], v[194:201], 0
	v_mfma_f32_16x16x128_f8f6f4 v[74:77], v[10:17], v[194:201], 0
	v_mfma_f32_16x16x128_f8f6f4 v[70:73], v[2:9], v[202:209], 0
	v_mfma_f32_16x16x128_f8f6f4 v[62:65], v[10:17], v[202:209], 0
	v_mfma_f32_16x16x128_f8f6f4 v[46:49], v[2:9], v[210:217], 0
	v_mfma_f32_16x16x128_f8f6f4 v[42:45], v[10:17], v[210:217], 0
	v_mfma_f32_16x16x128_f8f6f4 v[38:41], v[2:9], v[218:225], 0
	v_mfma_f32_16x16x128_f8f6f4 v[34:37], v[10:17], v[218:225], 0
	s_setprio 0
	s_barrier
	s_add_i32 s82, 0, 0x18000
	s_add_i32 s83, 0, 0x1c000
	v_add_u32_e32 v14, s82, v191
	v_add_u32_e32 v30, s83, v191
	ds_read_b128 v[2:5], v14
	ds_read_b128 v[6:9], v14 offset:1024
	ds_read_b128 v[10:13], v14 offset:2048
	ds_read_b128 v[14:17], v14 offset:3072
	ds_read_b128 v[18:21], v30
	ds_read_b128 v[22:25], v30 offset:1024
	ds_read_b128 v[26:29], v30 offset:2048
	ds_read_b128 v[30:33], v30 offset:3072
	s_add_u32 s48, s48, 0x20000
	s_addc_u32 s49, s49, 0
	s_mov_b32 m0, s60
	v_lshl_add_u64 v[226:227], s[48:49], 0, v[168:169]
	ds_read_b128 v[194:197], v192 offset:32768
	ds_read_b128 v[198:201], v192 offset:33792
	ds_read_b128 v[202:205], v192 offset:34816
	ds_read_b128 v[206:209], v192 offset:35840
	ds_read_b128 v[210:213], v192 offset:36864
	ds_read_b128 v[214:217], v192 offset:37888
	ds_read_b128 v[218:221], v192 offset:38912
	ds_read_b128 v[222:225], v192 offset:39936
	global_load_lds_dwordx4 v[226:227], off
	v_lshl_add_u64 v[226:227], s[48:49], 0, v[164:165]
	s_mov_b32 m0, s61
	s_nop 0
	global_load_lds_dwordx4 v[226:227], off
	s_waitcnt vmcnt(8)
	s_waitcnt lgkmcnt(0)
	s_barrier
; #define PG8_STAGE(bufoff, gbase, voff) do { _Pragma("unroll") for (int _i = 0; _i < 2; ++_i) \
;         __builtin_amdgcn_global_load_lds((const unsigned*)((const char*)(gbase) + (voff)[_i]), (PG8_LAS unsigned*)(lds + (bufoff) + ldsw + _i * 8192), 16, 0, 0); } while (0)
; #define PG8_STAGE_A(bufoff, kbase, h, gv) do { if constexpr (GATHER) { PG8_STAGE(bufoff, kbase, (gv)[h]); } else { PG8_STAGE(bufoff, (kbase) + (h) * hstep, voffA); } } while (0)
; #define PG8_WAIT_V(n) asm volatile("s_waitcnt vmcnt(" #n ")" ::: "memory")
; #define PG8_WAIT_L(n) asm volatile("s_waitcnt lgkmcnt(" #n ")" ::: "memory")
; #define PG8_BAR __builtin_amdgcn_s_barrier()
; #define PG8_SCHED __builtin_amdgcn_sched_barrier(0)
; template <class Epi, class Sched, bool ALIGN_EPI = false, bool SP2 = false, bool FP8 = false, bool GATHER = false>
; __device__ __forceinline__ void gemm_phase(PG8_LAS unsigned char* lds, const Gemm g, const Sched& S, const Epi& E) {
;     ...
;         for (int t = 0; t < nt; t += 2) {
;             const bool last = (t == nt - 2);
;             const char* a1 = cA + (size_t)(t + 1) * kstep;
;             const char* a2 = last ? nA : cA + (size_t)(t + 2) * kstep; const char* b2 = last ? nB : cB + (size_t)(t + 2) * kstep;
;             const char* a3 = a2 + kstep; const char* b3 = b2 + kstep;
;     ...
;             PG8_LDB(B0, 0, 0); PG8_LDB(B1, 0, 1); PG8_SCHED; PG8_LDA(At, 0, 0); PG8_STAGE_A(PG8_SA(1, 1), a1, 1, gcur);
;             PG8_WAIT_V(8); PG8_WAIT_L(0); PG8_BAR; PG8_MMA(0, 0, At, B0); PG8_MMA(0, 1, At, B1); PG8_BAR; PG8_SCHED;
;             PG8_LDA(At, 0, 1); PG8_STAGE(PG8_SB(0, 0), b2, voffB); PG8_STAGE(PG8_SB(0, 1), b2 + hstep, voffB); PG8_STAGE_A(PG8_SA(0, 0), a2, 0, gsel);
;             PG8_WAIT_V(8); PG8_WAIT_L(0); PG8_BAR; PG8_MMA(1, 0, At, B0); PG8_MMA(1, 1, At, B1); PG8_BAR; PG8_SCHED;
;             PG8_LDB(B0, 1, 0); PG8_LDB(B1, 1, 1); PG8_SCHED; PG8_LDA(At, 1, 0); PG8_STAGE_A(PG8_SA(0, 1), a2, 1, gsel);
;             PG8_WAIT_V(8); PG8_WAIT_L(0); PG8_BAR; PG8_MMA(0, 0, At, B0); PG8_MMA(0, 1, At, B1); PG8_BAR; PG8_SCHED;
;             PG8_LDA(At, 1, 1); PG8_STAGE(PG8_SB(1, 0), b3, voffB); PG8_STAGE(PG8_SB(1, 1), b3 + hstep, voffB); PG8_STAGE_A(PG8_SA(1, 0), a3, 0, gsel);
;             PG8_WAIT_V(8); PG8_WAIT_L(0); PG8_BAR; PG8_MMA(1, 0, At, B0); PG8_MMA(1, 1, At, B1); PG8_BAR; PG8_SCHED;
	s_setprio 1
	s_waitcnt lgkmcnt(0)
	v_mfma_f32_16x16x128_f8f6f4 v[158:161], v[2:9], v[194:201], v[158:161]
	v_mfma_f32_16x16x128_f8f6f4 v[154:157], v[10:17], v[194:201], v[154:157]
	v_mfma_f32_16x16x128_f8f6f4 v[150:153], v[2:9], v[202:209], v[150:153]
	v_mfma_f32_16x16x128_f8f6f4 v[146:149], v[10:17], v[202:209], v[146:149]
	v_mfma_f32_16x16x128_f8f6f4 v[130:133], v[2:9], v[210:217], v[130:133]
	v_mfma_f32_16x16x128_f8f6f4 v[122:125], v[10:17], v[210:217], v[122:125]
	v_mfma_f32_16x16x128_f8f6f4 v[118:121], v[2:9], v[218:225], v[118:121]
	v_mfma_f32_16x16x128_f8f6f4 v[114:117], v[10:17], v[218:225], v[114:117]
	s_setprio 0
	s_setprio 1
	v_mfma_f32_16x16x128_f8f6f4 v[142:145], v[18:25], v[194:201], v[142:145]
	v_mfma_f32_16x16x128_f8f6f4 v[138:141], v[26:33], v[194:201], v[138:141]
	v_mfma_f32_16x16x128_f8f6f4 v[134:137], v[18:25], v[202:209], v[134:137]
	v_mfma_f32_16x16x128_f8f6f4 v[126:129], v[26:33], v[202:209], v[126:129]
	v_mfma_f32_16x16x128_f8f6f4 v[110:113], v[18:25], v[210:217], v[110:113]
	v_mfma_f32_16x16x128_f8f6f4 v[106:109], v[26:33], v[210:217], v[106:109]
	v_mfma_f32_16x16x128_f8f6f4 v[102:105], v[18:25], v[218:225], v[102:105]
	v_mfma_f32_16x16x128_f8f6f4 v[98:101], v[26:33], v[218:225], v[98:101]
	s_setprio 0
	s_barrier
	s_add_i32 s48, s82, s56
	v_lshl_add_u64 v[182:183], v[182:183], 0, s[14:15]
	s_mov_b32 m0, s48
	ds_read_b128 v[194:197], v192 offset:49152
	ds_read_b128 v[198:201], v192 offset:50176
	ds_read_b128 v[202:205], v192 offset:51200
	ds_read_b128 v[206:209], v192 offset:52224
	ds_read_b128 v[210:213], v192 offset:53248
	ds_read_b128 v[214:217], v192 offset:54272
	ds_read_b128 v[218:221], v192 offset:55296
	ds_read_b128 v[222:225], v192 offset:56320
	global_load_lds_dwordx4 v[182:183], off
	s_add_i32 m0, s48, 0x2000
	s_add_u32 s46, s46, 0x20080
	v_lshl_add_u64 v[182:183], v[184:185], 0, s[14:15]
	s_addc_u32 s47, s47, 0
	s_add_i32 s48, s83, s56
	global_load_lds_dwordx4 v[182:183], off
	v_lshl_add_u64 v[182:183], s[46:47], 0, v[166:167]
	s_mov_b32 m0, s48
	s_nop 0
	global_load_lds_dwordx4 v[182:183], off
	v_lshl_add_u64 v[182:183], s[46:47], 0, v[162:163]
	s_add_i32 m0, s48, 0x2000
	s_nop 0
	global_load_lds_dwordx4 v[182:183], off
	v_lshl_add_u64 v[182:183], v[186:187], 0, s[14:15]
	s_mov_b32 m0, s67
	s_nop 0
	global_load_lds_dwordx4 v[182:183], off
	v_lshl_add_u64 v[182:183], v[188:189], 0, s[14:15]
	s_mov_b32 m0, s68
	s_nop 0
	global_load_lds_dwordx4 v[182:183], off
	s_waitcnt vmcnt(8)
	s_waitcnt lgkmcnt(0)
	s_barrier
	s_setprio 1
	s_waitcnt lgkmcnt(0)
	v_mfma_f32_16x16x128_f8f6f4 v[94:97], v[2:9], v[194:201], v[94:97]
	v_mfma_f32_16x16x128_f8f6f4 v[90:93], v[10:17], v[194:201], v[90:93]
	v_mfma_f32_16x16x128_f8f6f4 v[86:89], v[2:9], v[202:209], v[86:89]
	v_mfma_f32_16x16x128_f8f6f4 v[82:85], v[10:17], v[202:209], v[82:85]
	v_mfma_f32_16x16x128_f8f6f4 v[66:69], v[2:9], v[210:217], v[66:69]
	v_mfma_f32_16x16x128_f8f6f4 v[58:61], v[10:17], v[210:217], v[58:61]
	v_mfma_f32_16x16x128_f8f6f4 v[54:57], v[2:9], v[218:225], v[54:57]
	v_mfma_f32_16x16x128_f8f6f4 v[50:53], v[10:17], v[218:225], v[50:53]
	s_setprio 0
	s_setprio 1
	v_mfma_f32_16x16x128_f8f6f4 v[78:81], v[18:25], v[194:201], v[78:81]
	v_mfma_f32_16x16x128_f8f6f4 v[74:77], v[26:33], v[194:201], v[74:77]
	v_mfma_f32_16x16x128_f8f6f4 v[70:73], v[18:25], v[202:209], v[70:73]
	v_mfma_f32_16x16x128_f8f6f4 v[62:65], v[26:33], v[202:209], v[62:65]
	v_mfma_f32_16x16x128_f8f6f4 v[46:49], v[18:25], v[210:217], v[46:49]
	v_mfma_f32_16x16x128_f8f6f4 v[42:45], v[26:33], v[210:217], v[42:45]
	v_mfma_f32_16x16x128_f8f6f4 v[38:41], v[18:25], v[218:225], v[38:41]
	v_mfma_f32_16x16x128_f8f6f4 v[34:37], v[26:33], v[218:225], v[34:37]
	s_setprio 0
	s_add_i32 s81, s81, 2
	s_add_u32 s44, s44, 0x100
	s_addc_u32 s45, s45, 0
	s_add_u32 s35, s35, 0x100
	s_addc_u32 s80, s80, 0
	s_cmp_gt_u32 s81, 5
	s_cbranch_scc1 .Lrot1856_exit
	s_barrier
	s_branch .LBB0_1857
.LBB0_1856:
	v_add_u32_e32 v2, s74, v191
	v_add_u32_e32 v14, s75, v191
	ds_read_b128 v[18:21], v2
	ds_read_b128 v[22:25], v2 offset:1024
	ds_read_b128 v[26:29], v2 offset:2048
	ds_read_b128 v[30:33], v2 offset:3072
	ds_read_b128 v[2:5], v14
	ds_read_b128 v[6:9], v14 offset:1024
	ds_read_b128 v[10:13], v14 offset:2048
	ds_read_b128 v[14:17], v14 offset:3072
	s_add_u32 s48, s44, 0xfffe0080
	s_addc_u32 s49, s45, -1
	s_and_b64 s[46:47], s[46:47], exec
	s_cselect_b32 s49, s78, s49
	s_cselect_b32 s48, s79, s48
	s_cselect_b32 s47, s25, s80
	s_cselect_b32 s46, s24, s35
	v_lshl_add_u64 v[218:219], s[44:45], 0, v[172:173]
	s_add_i32 m0, s58, 0xc000
	ds_read_b128 v[182:185], v192
	ds_read_b128 v[186:189], v192 offset:1024
	ds_read_b128 v[194:197], v192 offset:2048
	ds_read_b128 v[198:201], v192 offset:3072
	ds_read_b128 v[202:205], v192 offset:4096
	ds_read_b128 v[206:209], v192 offset:5120
	ds_read_b128 v[210:213], v192 offset:6144
	ds_read_b128 v[214:217], v192 offset:7168
	global_load_lds_dwordx4 v[218:219], off
	v_lshl_add_u64 v[218:219], s[44:45], 0, v[174:175]
	s_add_i32 m0, s58, 0xe000
	s_nop 0
	global_load_lds_dwordx4 v[218:219], off
	s_waitcnt vmcnt(8)
	s_waitcnt lgkmcnt(0)
	s_barrier
; #define PG8_STAGE(bufoff, gbase, voff) do { _Pragma("unroll") for (int _i = 0; _i < 2; ++_i) \
;         __builtin_amdgcn_global_load_lds((const unsigned*)((const char*)(gbase) + (voff)[_i]), (PG8_LAS unsigned*)(lds + (bufoff) + ldsw + _i * 8192), 16, 0, 0); } while (0)
; #define PG8_STAGE_A(bufoff, kbase, h, gv) do { if constexpr (GATHER) { PG8_STAGE(bufoff, kbase, (gv)[h]); } else { PG8_STAGE(bufoff, (kbase) + (h) * hstep, voffA); } } while (0)
; #define PG8_WAIT_V(n) asm volatile("s_waitcnt vmcnt(" #n ")" ::: "memory")
; #define PG8_WAIT_L(n) asm volatile("s_waitcnt lgkmcnt(" #n ")" ::: "memory")
; #define PG8_BAR __builtin_amdgcn_s_barrier()
; #define PG8_SCHED __builtin_amdgcn_sched_barrier(0)
; template <class Epi, class Sched, bool ALIGN_EPI = false, bool SP2 = false, bool FP8 = false, bool GATHER = false>
; __device__ __forceinline__ void gemm_phase(PG8_LAS unsigned char* lds, const Gemm g, const Sched& S, const Epi& E) {
;     ...
;             PG8_LDB(B0, 0, 0); PG8_LDB(B1, 0, 1); PG8_SCHED; PG8_LDA(At, 0, 0); PG8_STAGE_A(PG8_SA(1, 1), a1, 1, gcur);
;             PG8_WAIT_V(8); PG8_WAIT_L(0); PG8_BAR; PG8_MMA(0, 0, At, B0); PG8_MMA(0, 1, At, B1); PG8_BAR; PG8_SCHED;
;             PG8_LDA(At, 0, 1); PG8_STAGE(PG8_SB(0, 0), b2, voffB); PG8_STAGE(PG8_SB(0, 1), b2 + hstep, voffB); PG8_STAGE_A(PG8_SA(0, 0), a2, 0, gsel);
;             PG8_WAIT_V(8); PG8_WAIT_L(0); PG8_BAR; PG8_MMA(1, 0, At, B0); PG8_MMA(1, 1, At, B1); PG8_BAR; PG8_SCHED;
;             PG8_LDB(B0, 1, 0); PG8_LDB(B1, 1, 1); PG8_SCHED; PG8_LDA(At, 1, 0); PG8_STAGE_A(PG8_SA(0, 1), a2, 1, gsel);
;             PG8_WAIT_V(8); PG8_WAIT_L(0); PG8_BAR; PG8_MMA(0, 0, At, B0); PG8_MMA(0, 1, At, B1); PG8_BAR; PG8_SCHED;
;             PG8_LDA(At, 1, 1); PG8_STAGE(PG8_SB(1, 0), b3, voffB); PG8_STAGE(PG8_SB(1, 1), b3 + hstep, voffB); PG8_STAGE_A(PG8_SA(1, 0), a3, 0, gsel);
;             PG8_WAIT_V(8); PG8_WAIT_L(0); PG8_BAR; PG8_MMA(1, 0, At, B0); PG8_MMA(1, 1, At, B1); PG8_BAR; PG8_SCHED;
	s_setprio 1
	s_waitcnt lgkmcnt(0)
	v_mfma_f32_16x16x128_f8f6f4 v[158:161], v[18:25], v[182:189], v[158:161]
	v_mfma_f32_16x16x128_f8f6f4 v[154:157], v[26:33], v[182:189], v[154:157]
	v_mfma_f32_16x16x128_f8f6f4 v[150:153], v[18:25], v[194:201], v[150:153]
	v_mfma_f32_16x16x128_f8f6f4 v[146:149], v[26:33], v[194:201], v[146:149]
	v_mfma_f32_16x16x128_f8f6f4 v[130:133], v[18:25], v[202:209], v[130:133]
	v_mfma_f32_16x16x128_f8f6f4 v[122:125], v[26:33], v[202:209], v[122:125]
	v_mfma_f32_16x16x128_f8f6f4 v[118:121], v[18:25], v[210:217], v[118:121]
	v_mfma_f32_16x16x128_f8f6f4 v[114:117], v[26:33], v[210:217], v[114:117]
	s_setprio 0
	s_setprio 1
	v_mfma_f32_16x16x128_f8f6f4 v[142:145], v[2:9], v[182:189], v[142:145]
	v_mfma_f32_16x16x128_f8f6f4 v[138:141], v[10:17], v[182:189], v[138:141]
	v_mfma_f32_16x16x128_f8f6f4 v[134:137], v[2:9], v[194:201], v[134:137]
	v_mfma_f32_16x16x128_f8f6f4 v[126:129], v[10:17], v[194:201], v[126:129]
	v_mfma_f32_16x16x128_f8f6f4 v[110:113], v[2:9], v[202:209], v[110:113]
	v_mfma_f32_16x16x128_f8f6f4 v[106:109], v[10:17], v[202:209], v[106:109]
	v_mfma_f32_16x16x128_f8f6f4 v[102:105], v[2:9], v[210:217], v[102:105]
	v_mfma_f32_16x16x128_f8f6f4 v[98:101], v[10:17], v[210:217], v[98:101]
	s_setprio 0
	s_barrier
	s_add_i32 s82, s74, s56
	v_lshl_add_u64 v[182:183], s[46:47], 0, v[166:167]
	s_mov_b32 m0, s82
	ds_read_b128 v[194:197], v192 offset:16384
	ds_read_b128 v[198:201], v192 offset:17408
	ds_read_b128 v[202:205], v192 offset:18432
	ds_read_b128 v[206:209], v192 offset:19456
	ds_read_b128 v[210:213], v192 offset:20480
	ds_read_b128 v[214:217], v192 offset:21504
	ds_read_b128 v[218:221], v192 offset:22528
	ds_read_b128 v[222:225], v192 offset:23552
	global_load_lds_dwordx4 v[182:183], off
	s_add_i32 m0, s82, 0x2000
	s_add_u32 s82, s46, 0x20000
	v_lshl_add_u64 v[184:185], s[46:47], 0, v[162:163]
	s_addc_u32 s83, s47, 0
	s_add_i32 s84, s75, s56
	global_load_lds_dwordx4 v[184:185], off
	v_lshl_add_u64 v[186:187], s[82:83], 0, v[166:167]
	s_mov_b32 m0, s84
	v_lshl_add_u64 v[188:189], s[48:49], 0, v[164:165]
	global_load_lds_dwordx4 v[186:187], off
	v_lshl_add_u64 v[186:187], s[82:83], 0, v[162:163]
	s_add_i32 m0, s84, 0x2000
	s_nop 0
	global_load_lds_dwordx4 v[186:187], off
	v_lshl_add_u64 v[186:187], s[48:49], 0, v[168:169]
	s_mov_b32 m0, s58
	s_nop 0
	global_load_lds_dwordx4 v[186:187], off
	s_mov_b32 m0, s59
	s_nop 0
	global_load_lds_dwordx4 v[188:189], off
	s_waitcnt vmcnt(8)
	s_waitcnt lgkmcnt(0)
	s_barrier
	s_setprio 1
	s_waitcnt lgkmcnt(0)
	v_mfma_f32_16x16x128_f8f6f4 v[94:97], v[18:25], v[194:201], v[94:97]
	v_mfma_f32_16x16x128_f8f6f4 v[90:93], v[26:33], v[194:201], v[90:93]
	v_mfma_f32_16x16x128_f8f6f4 v[86:89], v[18:25], v[202:209], v[86:89]
	v_mfma_f32_16x16x128_f8f6f4 v[82:85], v[26:33], v[202:209], v[82:85]
	v_mfma_f32_16x16x128_f8f6f4 v[66:69], v[18:25], v[210:217], v[66:69]
	v_mfma_f32_16x16x128_f8f6f4 v[58:61], v[26:33], v[210:217], v[58:61]
	v_mfma_f32_16x16x128_f8f6f4 v[54:57], v[18:25], v[218:225], v[54:57]
	v_mfma_f32_16x16x128_f8f6f4 v[50:53], v[26:33], v[218:225], v[50:53]
	s_setprio 0
	s_setprio 1
	v_mfma_f32_16x16x128_f8f6f4 v[78:81], v[2:9], v[194:201], v[78:81]
	v_mfma_f32_16x16x128_f8f6f4 v[74:77], v[10:17], v[194:201], v[74:77]
	v_mfma_f32_16x16x128_f8f6f4 v[70:73], v[2:9], v[202:209], v[70:73]
	v_mfma_f32_16x16x128_f8f6f4 v[62:65], v[10:17], v[202:209], v[62:65]
	v_mfma_f32_16x16x128_f8f6f4 v[46:49], v[2:9], v[210:217], v[46:49]
	v_mfma_f32_16x16x128_f8f6f4 v[42:45], v[10:17], v[210:217], v[42:45]
	v_mfma_f32_16x16x128_f8f6f4 v[38:41], v[2:9], v[218:225], v[38:41]
	v_mfma_f32_16x16x128_f8f6f4 v[34:37], v[10:17], v[218:225], v[34:37]
	s_setprio 0
	s_barrier
	s_add_i32 s82, 0, 0x18000
	s_add_i32 s83, 0, 0x1c000
	v_add_u32_e32 v14, s82, v191
	v_add_u32_e32 v30, s83, v191
	ds_read_b128 v[2:5], v14
	ds_read_b128 v[6:9], v14 offset:1024
	ds_read_b128 v[10:13], v14 offset:2048
	ds_read_b128 v[14:17], v14 offset:3072
	ds_read_b128 v[18:21], v30
	ds_read_b128 v[22:25], v30 offset:1024
	ds_read_b128 v[26:29], v30 offset:2048
	ds_read_b128 v[30:33], v30 offset:3072
	s_add_u32 s48, s48, 0x20000
	s_addc_u32 s49, s49, 0
	s_mov_b32 m0, s60
	v_lshl_add_u64 v[226:227], s[48:49], 0, v[168:169]
	ds_read_b128 v[194:197], v192 offset:32768
	ds_read_b128 v[198:201], v192 offset:33792
	ds_read_b128 v[202:205], v192 offset:34816
	ds_read_b128 v[206:209], v192 offset:35840
	ds_read_b128 v[210:213], v192 offset:36864
	ds_read_b128 v[214:217], v192 offset:37888
	ds_read_b128 v[218:221], v192 offset:38912
	ds_read_b128 v[222:225], v192 offset:39936
	global_load_lds_dwordx4 v[226:227], off
	v_lshl_add_u64 v[226:227], s[48:49], 0, v[164:165]
	s_mov_b32 m0, s61
	s_nop 0
	global_load_lds_dwordx4 v[226:227], off
	s_waitcnt vmcnt(8)
	s_waitcnt lgkmcnt(0)
	s_barrier
; #define PG8_STAGE(bufoff, gbase, voff) do { _Pragma("unroll") for (int _i = 0; _i < 2; ++_i) \
;         __builtin_amdgcn_global_load_lds((const unsigned*)((const char*)(gbase) + (voff)[_i]), (PG8_LAS unsigned*)(lds + (bufoff) + ldsw + _i * 8192), 16, 0, 0); } while (0)
; #define PG8_STAGE_A(bufoff, kbase, h, gv) do { if constexpr (GATHER) { PG8_STAGE(bufoff, kbase, (gv)[h]); } else { PG8_STAGE(bufoff, (kbase) + (h) * hstep, voffA); } } while (0)
; #define PG8_WAIT_V(n) asm volatile("s_waitcnt vmcnt(" #n ")" ::: "memory")
; #define PG8_WAIT_L(n) asm volatile("s_waitcnt lgkmcnt(" #n ")" ::: "memory")
; #define PG8_BAR __builtin_amdgcn_s_barrier()
; #define PG8_SCHED __builtin_amdgcn_sched_barrier(0)
; template <class Epi, class Sched, bool ALIGN_EPI = false, bool SP2 = false, bool FP8 = false, bool GATHER = false>
; __device__ __forceinline__ void gemm_phase(PG8_LAS unsigned char* lds, const Gemm g, const Sched& S, const Epi& E) {
;     ...
;             PG8_LDB(B0, 0, 0); PG8_LDB(B1, 0, 1); PG8_SCHED; PG8_LDA(At, 0, 0); PG8_STAGE_A(PG8_SA(1, 1), a1, 1, gcur);
;             PG8_WAIT_V(8); PG8_WAIT_L(0); PG8_BAR; PG8_MMA(0, 0, At, B0); PG8_MMA(0, 1, At, B1); PG8_BAR; PG8_SCHED;
;             PG8_LDA(At, 0, 1); PG8_STAGE(PG8_SB(0, 0), b2, voffB); PG8_STAGE(PG8_SB(0, 1), b2 + hstep, voffB); PG8_STAGE_A(PG8_SA(0, 0), a2, 0, gsel);
;             PG8_WAIT_V(8); PG8_WAIT_L(0); PG8_BAR; PG8_MMA(1, 0, At, B0); PG8_MMA(1, 1, At, B1); PG8_BAR; PG8_SCHED;
;             PG8_LDB(B0, 1, 0); PG8_LDB(B1, 1, 1); PG8_SCHED; PG8_LDA(At, 1, 0); PG8_STAGE_A(PG8_SA(0, 1), a2, 1, gsel);
;             PG8_WAIT_V(8); PG8_WAIT_L(0); PG8_BAR; PG8_MMA(0, 0, At, B0); PG8_MMA(0, 1, At, B1); PG8_BAR; PG8_SCHED;
;             PG8_LDA(At, 1, 1); PG8_STAGE(PG8_SB(1, 0), b3, voffB); PG8_STAGE(PG8_SB(1, 1), b3 + hstep, voffB); PG8_STAGE_A(PG8_SA(1, 0), a3, 0, gsel);
;             PG8_WAIT_V(8); PG8_WAIT_L(0); PG8_BAR; PG8_MMA(1, 0, At, B0); PG8_MMA(1, 1, At, B1); PG8_BAR; PG8_SCHED;
	s_setprio 1
	s_waitcnt lgkmcnt(0)
	v_mfma_f32_16x16x128_f8f6f4 v[158:161], v[2:9], v[194:201], v[158:161]
	v_mfma_f32_16x16x128_f8f6f4 v[154:157], v[10:17], v[194:201], v[154:157]
	v_mfma_f32_16x16x128_f8f6f4 v[150:153], v[2:9], v[202:209], v[150:153]
	v_mfma_f32_16x16x128_f8f6f4 v[146:149], v[10:17], v[202:209], v[146:149]
	v_mfma_f32_16x16x128_f8f6f4 v[130:133], v[2:9], v[210:217], v[130:133]
	v_mfma_f32_16x16x128_f8f6f4 v[122:125], v[10:17], v[210:217], v[122:125]
	v_mfma_f32_16x16x128_f8f6f4 v[118:121], v[2:9], v[218:225], v[118:121]
	v_mfma_f32_16x16x128_f8f6f4 v[114:117], v[10:17], v[218:225], v[114:117]
	s_setprio 0
	s_setprio 1
	v_mfma_f32_16x16x128_f8f6f4 v[142:145], v[18:25], v[194:201], v[142:145]
	v_mfma_f32_16x16x128_f8f6f4 v[138:141], v[26:33], v[194:201], v[138:141]
	v_mfma_f32_16x16x128_f8f6f4 v[134:137], v[18:25], v[202:209], v[134:137]
	v_mfma_f32_16x16x128_f8f6f4 v[126:129], v[26:33], v[202:209], v[126:129]
	v_mfma_f32_16x16x128_f8f6f4 v[110:113], v[18:25], v[210:217], v[110:113]
	v_mfma_f32_16x16x128_f8f6f4 v[106:109], v[26:33], v[210:217], v[106:109]
	v_mfma_f32_16x16x128_f8f6f4 v[102:105], v[18:25], v[218:225], v[102:105]
	v_mfma_f32_16x16x128_f8f6f4 v[98:101], v[26:33], v[218:225], v[98:101]
	s_setprio 0
	s_barrier
	s_add_i32 s48, s82, s56
	v_lshl_add_u64 v[182:183], v[182:183], 0, s[14:15]
	s_mov_b32 m0, s48
	ds_read_b128 v[194:197], v192 offset:49152
	ds_read_b128 v[198:201], v192 offset:50176
	ds_read_b128 v[202:205], v192 offset:51200
	ds_read_b128 v[206:209], v192 offset:52224
	ds_read_b128 v[210:213], v192 offset:53248
	ds_read_b128 v[214:217], v192 offset:54272
	ds_read_b128 v[218:221], v192 offset:55296
	ds_read_b128 v[222:225], v192 offset:56320
	global_load_lds_dwordx4 v[182:183], off
	s_add_i32 m0, s48, 0x2000
	s_add_u32 s46, s46, 0x20080
	v_lshl_add_u64 v[182:183], v[184:185], 0, s[14:15]
	s_addc_u32 s47, s47, 0
	s_add_i32 s48, s83, s56
	global_load_lds_dwordx4 v[182:183], off
	v_lshl_add_u64 v[182:183], s[46:47], 0, v[166:167]
	s_mov_b32 m0, s48
	s_nop 0
	global_load_lds_dwordx4 v[182:183], off
	v_lshl_add_u64 v[182:183], s[46:47], 0, v[162:163]
	s_add_i32 m0, s48, 0x2000
	s_nop 0
	global_load_lds_dwordx4 v[182:183], off
	v_lshl_add_u64 v[182:183], v[186:187], 0, s[14:15]
	s_mov_b32 m0, s67
	s_nop 0
	global_load_lds_dwordx4 v[182:183], off
	v_lshl_add_u64 v[182:183], v[188:189], 0, s[14:15]
	s_mov_b32 m0, s68
	s_nop 0
	global_load_lds_dwordx4 v[182:183], off
	s_waitcnt vmcnt(8)
	s_waitcnt lgkmcnt(0)
	s_barrier
	s_setprio 1
	s_waitcnt lgkmcnt(0)
	v_mfma_f32_16x16x128_f8f6f4 v[94:97], v[2:9], v[194:201], v[94:97]
	v_mfma_f32_16x16x128_f8f6f4 v[90:93], v[10:17], v[194:201], v[90:93]
	v_mfma_f32_16x16x128_f8f6f4 v[86:89], v[2:9], v[202:209], v[86:89]
	v_mfma_f32_16x16x128_f8f6f4 v[82:85], v[10:17], v[202:209], v[82:85]
	v_mfma_f32_16x16x128_f8f6f4 v[66:69], v[2:9], v[210:217], v[66:69]
	v_mfma_f32_16x16x128_f8f6f4 v[58:61], v[10:17], v[210:217], v[58:61]
	v_mfma_f32_16x16x128_f8f6f4 v[54:57], v[2:9], v[218:225], v[54:57]
	v_mfma_f32_16x16x128_f8f6f4 v[50:53], v[10:17], v[218:225], v[50:53]
	s_setprio 0
	s_setprio 1
	v_mfma_f32_16x16x128_f8f6f4 v[78:81], v[18:25], v[194:201], v[78:81]
	v_mfma_f32_16x16x128_f8f6f4 v[74:77], v[26:33], v[194:201], v[74:77]
	v_mfma_f32_16x16x128_f8f6f4 v[70:73], v[18:25], v[202:209], v[70:73]
	v_mfma_f32_16x16x128_f8f6f4 v[62:65], v[26:33], v[202:209], v[62:65]
	v_mfma_f32_16x16x128_f8f6f4 v[46:49], v[18:25], v[210:217], v[46:49]
	v_mfma_f32_16x16x128_f8f6f4 v[42:45], v[26:33], v[210:217], v[42:45]
	v_mfma_f32_16x16x128_f8f6f4 v[38:41], v[18:25], v[218:225], v[38:41]
	v_mfma_f32_16x16x128_f8f6f4 v[34:37], v[26:33], v[218:225], v[34:37]
	s_setprio 0
	s_add_i32 s81, s81, 2
	s_add_u32 s44, s44, 0x100
	s_addc_u32 s45, s45, 0
	s_add_u32 s35, s35, 0x100
	s_addc_u32 s80, s80, 0
	s_cmp_gt_u32 s81, 5
	s_cbranch_scc1 .Lrot1856_exit
	s_barrier

; #define PG8_BAR __builtin_amdgcn_s_barrier()
; template <class Epi, class Sched, bool ALIGN_EPI = false, bool SP2 = false, bool FP8 = false, bool GATHER = false>
; __device__ __forceinline__ void gemm_phase(PG8_LAS unsigned char* lds, const Gemm g, const Sched& S, const Epi& E) {
;     ...
;         if constexpr (FP8) asm volatile("s_nop 15\n\ts_nop 15" ::: "memory");
;         if constexpr (ALIGN_EPI) { if (wr == 0) PG8_BAR; }
;     __device__ __forceinline__ void pre(const pg8::Unit& u, int wid, int lane) const {
;         if (wid == 0) lds_dma16(bias + (size_t)(u.pn >> 8) * 1024 + (u.pn & 255) * 256 + lane * 4, (unsigned)(uintptr_t)(lds + LDS_EPI));
;         if (wid == 1) lds_dma16(row_w + (size_t)u.pm * 256 + lane * 4, (unsigned)(uintptr_t)(lds + LDS_EPI + 1024)); }
.LBB0_1862:
	s_andn2_b64 vcc, exec, s[48:49]
	s_cbranch_vccnz .LBB0_1856
	s_cmp_lg_u32 s55, 0
	s_cbranch_scc1 .LBB0_1856
	s_add_i32 s48, 0, 0x20000
	s_mov_b32 s49, m0
	s_mov_b32 m0, s48
	s_nop 0
	global_load_lds_dwordx4 v[180:181], off
	s_mov_b32 m0, s49
	s_branch .LBB0_1856
.Lrot1856_exit:
	s_barrier
.LBB0_1865:
	s_nop 15
	s_nop 15
	s_and_b64 vcc, exec, s[16:17]
	s_cbranch_vccz .LBB0_1867
	s_barrier
